# all 13 GEMM K-loop heads pinned to 64-byte boundaries (padding sits after unconditional branches, never executed)
# baseline (speedup 1.0000x reference)
.Lpeelph1b_0:
	s_add_i32 s73, s60, 2
	s_add_u32 s61, s58, 0xfffc0080
	s_addc_u32 s62, s59, -1
	s_add_i32 s74, 0, 0x10000
	s_cmp_eq_u32 s68, s60
	s_cselect_b32 s63, s39, s62
	s_cselect_b32 s62, s43, s61
	s_cselect_b32 s61, s47, s72
	s_cselect_b32 s60, s55, s71
	s_add_i32 s76, 0, 0x14000
	v_add_u32_e32 v156, s74, v165
	v_add_u32_e32 v166, s76, v165
	ds_read_b128 v[144:147], v156
	ds_read_b128 v[148:151], v156 offset:1024
	ds_read_b128 v[152:155], v156 offset:2048
	ds_read_b128 v[156:159], v156 offset:3072
	ds_read_b128 v[160:163], v166
	ds_read_b128 v[170:173], v166 offset:1024
	ds_read_b128 v[174:177], v166 offset:2048
	ds_read_b128 v[180:183], v166 offset:3072
	v_lshl_add_u64 v[216:217], s[58:59], 0, v[142:143]
	s_add_i32 m0, s8, 0xc000
	ds_read_b128 v[184:187], v178
	ds_read_b128 v[188:191], v178 offset:1024
	ds_read_b128 v[192:195], v178 offset:2048
	ds_read_b128 v[196:199], v178 offset:3072
	ds_read_b128 v[200:203], v178 offset:4096
	ds_read_b128 v[204:207], v178 offset:5120
	ds_read_b128 v[208:211], v178 offset:6144
	ds_read_b128 v[212:215], v178 offset:7168
	global_load_lds_dwordx4 v[216:217], off
	v_lshl_add_u64 v[216:217], s[58:59], 0, v[140:141]
	s_add_i32 m0, s8, 0xe000
	s_nop 0
	global_load_lds_dwordx4 v[216:217], off
	s_waitcnt vmcnt(8)
	s_waitcnt lgkmcnt(0)
	s_barrier
	s_setprio 1
	v_mfma_f32_16x16x32_bf16 v[126:129], v[144:147], v[184:187], 0
	v_mfma_f32_16x16x32_bf16 v[122:125], v[152:155], v[184:187], 0
	v_mfma_f32_16x16x32_bf16 v[110:113], v[144:147], v[192:195], 0
	v_mfma_f32_16x16x32_bf16 v[106:109], v[152:155], v[192:195], 0
	v_mfma_f32_16x16x32_bf16 v[94:97], v[144:147], v[200:203], 0
	v_mfma_f32_16x16x32_bf16 v[90:93], v[152:155], v[200:203], 0
	v_mfma_f32_16x16x32_bf16 v[78:81], v[144:147], v[208:211], 0
	v_mfma_f32_16x16x32_bf16 v[74:77], v[152:155], v[208:211], 0
	v_mfma_f32_16x16x32_bf16 v[126:129], v[148:151], v[188:191], v[126:129]
	v_mfma_f32_16x16x32_bf16 v[122:125], v[156:159], v[188:191], v[122:125]
	v_mfma_f32_16x16x32_bf16 v[110:113], v[148:151], v[196:199], v[110:113]
	v_mfma_f32_16x16x32_bf16 v[106:109], v[156:159], v[196:199], v[106:109]
	v_mfma_f32_16x16x32_bf16 v[94:97], v[148:151], v[204:207], v[94:97]
	v_mfma_f32_16x16x32_bf16 v[90:93], v[156:159], v[204:207], v[90:93]
	v_mfma_f32_16x16x32_bf16 v[78:81], v[148:151], v[212:215], v[78:81]
	v_mfma_f32_16x16x32_bf16 v[74:77], v[156:159], v[212:215], v[74:77]
	s_setprio 0
	s_setprio 1
	v_mfma_f32_16x16x32_bf16 v[118:121], v[160:163], v[184:187], 0
	v_mfma_f32_16x16x32_bf16 v[114:117], v[174:177], v[184:187], 0
	v_mfma_f32_16x16x32_bf16 v[102:105], v[160:163], v[192:195], 0
	v_mfma_f32_16x16x32_bf16 v[98:101], v[174:177], v[192:195], 0
	v_mfma_f32_16x16x32_bf16 v[86:89], v[160:163], v[200:203], 0
	v_mfma_f32_16x16x32_bf16 v[82:85], v[174:177], v[200:203], 0
	v_mfma_f32_16x16x32_bf16 v[70:73], v[160:163], v[208:211], 0
	v_mfma_f32_16x16x32_bf16 v[66:69], v[174:177], v[208:211], 0
	v_mfma_f32_16x16x32_bf16 v[118:121], v[170:173], v[188:191], v[118:121]
	v_mfma_f32_16x16x32_bf16 v[114:117], v[180:183], v[188:191], v[114:117]
	v_mfma_f32_16x16x32_bf16 v[102:105], v[170:173], v[196:199], v[102:105]
	v_mfma_f32_16x16x32_bf16 v[98:101], v[180:183], v[196:199], v[98:101]
	v_mfma_f32_16x16x32_bf16 v[86:89], v[170:173], v[204:207], v[86:89]
	v_mfma_f32_16x16x32_bf16 v[82:85], v[180:183], v[204:207], v[82:85]
	v_mfma_f32_16x16x32_bf16 v[70:73], v[170:173], v[212:215], v[70:73]
	v_mfma_f32_16x16x32_bf16 v[66:69], v[180:183], v[212:215], v[66:69]
	s_setprio 0
	s_barrier
	s_add_i32 s74, s74, s1
	v_lshl_add_u64 v[216:217], s[60:61], 0, v[130:131]
	s_mov_b32 m0, s74
	ds_read_b128 v[184:187], v178 offset:16384
	ds_read_b128 v[188:191], v178 offset:17408
	ds_read_b128 v[192:195], v178 offset:18432
	ds_read_b128 v[196:199], v178 offset:19456
	ds_read_b128 v[200:203], v178 offset:20480
	ds_read_b128 v[204:207], v178 offset:21504
	ds_read_b128 v[208:211], v178 offset:22528
	ds_read_b128 v[212:215], v178 offset:23552
	global_load_lds_dwordx4 v[216:217], off
	s_add_i32 m0, s74, 0x2000
	s_add_u32 s74, s60, 0x40000
	v_lshl_add_u64 v[218:219], s[60:61], 0, v[132:133]
	s_addc_u32 s75, s61, 0
	s_add_i32 s76, s76, s1
	global_load_lds_dwordx4 v[218:219], off
	v_lshl_add_u64 v[220:221], s[74:75], 0, v[130:131]
	s_mov_b32 m0, s76
	v_lshl_add_u64 v[222:223], s[62:63], 0, v[136:137]
	global_load_lds_dwordx4 v[220:221], off
	v_lshl_add_u64 v[220:221], s[74:75], 0, v[132:133]
	s_add_i32 m0, s76, 0x2000
	s_nop 0
	global_load_lds_dwordx4 v[220:221], off
	v_lshl_add_u64 v[220:221], s[62:63], 0, v[134:135]
	s_mov_b32 m0, s8
	s_nop 0
	global_load_lds_dwordx4 v[220:221], off
	s_mov_b32 m0, s11
	s_nop 0
	global_load_lds_dwordx4 v[222:223], off
	s_waitcnt vmcnt(8)
	s_waitcnt lgkmcnt(0)
	s_barrier
	s_setprio 1
	v_mfma_f32_16x16x32_bf16 v[62:65], v[144:147], v[184:187], 0
	v_mfma_f32_16x16x32_bf16 v[58:61], v[152:155], v[184:187], 0
	v_mfma_f32_16x16x32_bf16 v[46:49], v[144:147], v[192:195], 0
	v_mfma_f32_16x16x32_bf16 v[42:45], v[152:155], v[192:195], 0
	v_mfma_f32_16x16x32_bf16 v[30:33], v[144:147], v[200:203], 0
	v_mfma_f32_16x16x32_bf16 v[26:29], v[152:155], v[200:203], 0
	v_mfma_f32_16x16x32_bf16 v[14:17], v[144:147], v[208:211], 0
	v_mfma_f32_16x16x32_bf16 v[10:13], v[152:155], v[208:211], 0
	v_mfma_f32_16x16x32_bf16 v[62:65], v[148:151], v[188:191], v[62:65]
	v_mfma_f32_16x16x32_bf16 v[58:61], v[156:159], v[188:191], v[58:61]
	v_mfma_f32_16x16x32_bf16 v[46:49], v[148:151], v[196:199], v[46:49]
	v_mfma_f32_16x16x32_bf16 v[42:45], v[156:159], v[196:199], v[42:45]
	v_mfma_f32_16x16x32_bf16 v[30:33], v[148:151], v[204:207], v[30:33]
	v_mfma_f32_16x16x32_bf16 v[26:29], v[156:159], v[204:207], v[26:29]
	v_mfma_f32_16x16x32_bf16 v[14:17], v[148:151], v[212:215], v[14:17]
	v_mfma_f32_16x16x32_bf16 v[10:13], v[156:159], v[212:215], v[10:13]
	s_setprio 0
	s_setprio 1
	v_mfma_f32_16x16x32_bf16 v[54:57], v[160:163], v[184:187], 0
	v_mfma_f32_16x16x32_bf16 v[50:53], v[174:177], v[184:187], 0
	v_mfma_f32_16x16x32_bf16 v[38:41], v[160:163], v[192:195], 0
	v_mfma_f32_16x16x32_bf16 v[34:37], v[174:177], v[192:195], 0
	v_mfma_f32_16x16x32_bf16 v[22:25], v[160:163], v[200:203], 0
	v_mfma_f32_16x16x32_bf16 v[18:21], v[174:177], v[200:203], 0
	v_mfma_f32_16x16x32_bf16 v[6:9], v[160:163], v[208:211], 0
	v_mfma_f32_16x16x32_bf16 v[2:5], v[174:177], v[208:211], 0
	v_mfma_f32_16x16x32_bf16 v[54:57], v[170:173], v[188:191], v[54:57]
	v_mfma_f32_16x16x32_bf16 v[50:53], v[180:183], v[188:191], v[50:53]
	v_mfma_f32_16x16x32_bf16 v[38:41], v[170:173], v[196:199], v[38:41]
	v_mfma_f32_16x16x32_bf16 v[34:37], v[180:183], v[196:199], v[34:37]
	v_mfma_f32_16x16x32_bf16 v[22:25], v[170:173], v[204:207], v[22:25]
	v_mfma_f32_16x16x32_bf16 v[18:21], v[180:183], v[204:207], v[18:21]
	v_mfma_f32_16x16x32_bf16 v[6:9], v[170:173], v[212:215], v[6:9]
	v_mfma_f32_16x16x32_bf16 v[2:5], v[180:183], v[212:215], v[2:5]
	s_setprio 0
	s_barrier
	s_add_i32 s74, 0, 0x18000
	s_add_i32 s75, 0, 0x1c000
	v_add_u32_e32 v156, s74, v165
	v_add_u32_e32 v166, s75, v165
	ds_read_b128 v[144:147], v156
	ds_read_b128 v[148:151], v156 offset:1024
	ds_read_b128 v[152:155], v156 offset:2048
	ds_read_b128 v[156:159], v156 offset:3072
	ds_read_b128 v[160:163], v166
	ds_read_b128 v[170:173], v166 offset:1024
	ds_read_b128 v[174:177], v166 offset:2048
	ds_read_b128 v[180:183], v166 offset:3072
	s_add_u32 s62, s62, 0x40000
	s_addc_u32 s63, s63, 0
	s_mov_b32 m0, s16
	v_lshl_add_u64 v[232:233], s[62:63], 0, v[134:135]
	ds_read_b128 v[184:187], v178 offset:32768
	ds_read_b128 v[188:191], v178 offset:33792
	ds_read_b128 v[192:195], v178 offset:34816
	ds_read_b128 v[196:199], v178 offset:35840
	ds_read_b128 v[200:203], v178 offset:36864
	ds_read_b128 v[204:207], v178 offset:37888
	ds_read_b128 v[208:211], v178 offset:38912
	ds_read_b128 v[212:215], v178 offset:39936
	global_load_lds_dwordx4 v[232:233], off
	v_lshl_add_u64 v[232:233], s[62:63], 0, v[136:137]
	s_mov_b32 m0, s25
	s_nop 0
	global_load_lds_dwordx4 v[232:233], off
	s_waitcnt vmcnt(8)
	s_waitcnt lgkmcnt(0)
	s_barrier
	s_setprio 1
	v_mfma_f32_16x16x32_bf16 v[126:129], v[144:147], v[184:187], v[126:129]
	v_mfma_f32_16x16x32_bf16 v[122:125], v[152:155], v[184:187], v[122:125]
	v_mfma_f32_16x16x32_bf16 v[110:113], v[144:147], v[192:195], v[110:113]
	v_mfma_f32_16x16x32_bf16 v[106:109], v[152:155], v[192:195], v[106:109]
	v_mfma_f32_16x16x32_bf16 v[94:97], v[144:147], v[200:203], v[94:97]
	v_mfma_f32_16x16x32_bf16 v[90:93], v[152:155], v[200:203], v[90:93]
	v_mfma_f32_16x16x32_bf16 v[78:81], v[144:147], v[208:211], v[78:81]
	v_mfma_f32_16x16x32_bf16 v[74:77], v[152:155], v[208:211], v[74:77]
	v_mfma_f32_16x16x32_bf16 v[126:129], v[148:151], v[188:191], v[126:129]
	v_mfma_f32_16x16x32_bf16 v[122:125], v[156:159], v[188:191], v[122:125]
	v_mfma_f32_16x16x32_bf16 v[110:113], v[148:151], v[196:199], v[110:113]
	v_mfma_f32_16x16x32_bf16 v[106:109], v[156:159], v[196:199], v[106:109]
	v_mfma_f32_16x16x32_bf16 v[94:97], v[148:151], v[204:207], v[94:97]
	v_mfma_f32_16x16x32_bf16 v[90:93], v[156:159], v[204:207], v[90:93]
	v_mfma_f32_16x16x32_bf16 v[78:81], v[148:151], v[212:215], v[78:81]
	v_mfma_f32_16x16x32_bf16 v[74:77], v[156:159], v[212:215], v[74:77]
	s_setprio 0
	s_setprio 1
	v_mfma_f32_16x16x32_bf16 v[118:121], v[160:163], v[184:187], v[118:121]
	v_mfma_f32_16x16x32_bf16 v[114:117], v[174:177], v[184:187], v[114:117]
	v_mfma_f32_16x16x32_bf16 v[102:105], v[160:163], v[192:195], v[102:105]
	v_mfma_f32_16x16x32_bf16 v[98:101], v[174:177], v[192:195], v[98:101]
	v_mfma_f32_16x16x32_bf16 v[86:89], v[160:163], v[200:203], v[86:89]
	v_mfma_f32_16x16x32_bf16 v[82:85], v[174:177], v[200:203], v[82:85]
	v_mfma_f32_16x16x32_bf16 v[70:73], v[160:163], v[208:211], v[70:73]
	v_mfma_f32_16x16x32_bf16 v[66:69], v[174:177], v[208:211], v[66:69]
	v_mfma_f32_16x16x32_bf16 v[118:121], v[170:173], v[188:191], v[118:121]
	v_mfma_f32_16x16x32_bf16 v[114:117], v[180:183], v[188:191], v[114:117]
	v_mfma_f32_16x16x32_bf16 v[102:105], v[170:173], v[196:199], v[102:105]
	v_mfma_f32_16x16x32_bf16 v[98:101], v[180:183], v[196:199], v[98:101]
	v_mfma_f32_16x16x32_bf16 v[86:89], v[170:173], v[204:207], v[86:89]
	v_mfma_f32_16x16x32_bf16 v[82:85], v[180:183], v[204:207], v[82:85]
	v_mfma_f32_16x16x32_bf16 v[70:73], v[170:173], v[212:215], v[70:73]
	v_mfma_f32_16x16x32_bf16 v[66:69], v[180:183], v[212:215], v[66:69]
	s_setprio 0
	s_barrier
	s_add_i32 s62, s74, s1
	v_lshl_add_u64 v[216:217], v[216:217], 0, s[56:57]
	s_mov_b32 m0, s62
	ds_read_b128 v[184:187], v178 offset:49152
	ds_read_b128 v[188:191], v178 offset:50176
	ds_read_b128 v[192:195], v178 offset:51200
	ds_read_b128 v[196:199], v178 offset:52224
	ds_read_b128 v[200:203], v178 offset:53248
	ds_read_b128 v[204:207], v178 offset:54272
	ds_read_b128 v[208:211], v178 offset:55296
	ds_read_b128 v[212:215], v178 offset:56320
	global_load_lds_dwordx4 v[216:217], off
	s_add_i32 m0, s62, 0x2000
	s_add_u32 s60, s60, 0x40080
	v_lshl_add_u64 v[216:217], v[218:219], 0, s[56:57]
	s_addc_u32 s61, s61, 0
	s_add_i32 s62, s75, s1
	global_load_lds_dwordx4 v[216:217], off
	v_lshl_add_u64 v[216:217], s[60:61], 0, v[130:131]
	s_mov_b32 m0, s62
	s_nop 0
	global_load_lds_dwordx4 v[216:217], off
	v_lshl_add_u64 v[216:217], s[60:61], 0, v[132:133]
	s_add_i32 m0, s62, 0x2000
	s_nop 0
	global_load_lds_dwordx4 v[216:217], off
	v_lshl_add_u64 v[216:217], v[220:221], 0, s[56:57]
	s_mov_b32 m0, s64
	s_nop 0
	global_load_lds_dwordx4 v[216:217], off
	v_lshl_add_u64 v[216:217], v[222:223], 0, s[56:57]
	s_mov_b32 m0, s65
	s_nop 0
	global_load_lds_dwordx4 v[216:217], off
	s_waitcnt vmcnt(8)
	s_waitcnt lgkmcnt(0)
	s_barrier
	s_setprio 1
	v_mfma_f32_16x16x32_bf16 v[62:65], v[144:147], v[184:187], v[62:65]
	v_mfma_f32_16x16x32_bf16 v[58:61], v[152:155], v[184:187], v[58:61]
	v_mfma_f32_16x16x32_bf16 v[46:49], v[144:147], v[192:195], v[46:49]
	v_mfma_f32_16x16x32_bf16 v[42:45], v[152:155], v[192:195], v[42:45]
	v_mfma_f32_16x16x32_bf16 v[30:33], v[144:147], v[200:203], v[30:33]
	v_mfma_f32_16x16x32_bf16 v[26:29], v[152:155], v[200:203], v[26:29]
	v_mfma_f32_16x16x32_bf16 v[14:17], v[144:147], v[208:211], v[14:17]
	v_mfma_f32_16x16x32_bf16 v[10:13], v[152:155], v[208:211], v[10:13]
	v_mfma_f32_16x16x32_bf16 v[62:65], v[148:151], v[188:191], v[62:65]
	v_mfma_f32_16x16x32_bf16 v[58:61], v[156:159], v[188:191], v[58:61]
	v_mfma_f32_16x16x32_bf16 v[46:49], v[148:151], v[196:199], v[46:49]
	v_mfma_f32_16x16x32_bf16 v[42:45], v[156:159], v[196:199], v[42:45]
	v_mfma_f32_16x16x32_bf16 v[30:33], v[148:151], v[204:207], v[30:33]
	v_mfma_f32_16x16x32_bf16 v[26:29], v[156:159], v[204:207], v[26:29]
	v_mfma_f32_16x16x32_bf16 v[14:17], v[148:151], v[212:215], v[14:17]
	v_mfma_f32_16x16x32_bf16 v[10:13], v[156:159], v[212:215], v[10:13]
	s_setprio 0
	s_setprio 1
	v_mfma_f32_16x16x32_bf16 v[54:57], v[160:163], v[184:187], v[54:57]
	v_mfma_f32_16x16x32_bf16 v[50:53], v[174:177], v[184:187], v[50:53]
	v_mfma_f32_16x16x32_bf16 v[38:41], v[160:163], v[192:195], v[38:41]
	v_mfma_f32_16x16x32_bf16 v[34:37], v[174:177], v[192:195], v[34:37]
	v_mfma_f32_16x16x32_bf16 v[22:25], v[160:163], v[200:203], v[22:25]
	v_mfma_f32_16x16x32_bf16 v[18:21], v[174:177], v[200:203], v[18:21]
	v_mfma_f32_16x16x32_bf16 v[6:9], v[160:163], v[208:211], v[6:9]
	v_mfma_f32_16x16x32_bf16 v[2:5], v[174:177], v[208:211], v[2:5]
	v_mfma_f32_16x16x32_bf16 v[54:57], v[170:173], v[188:191], v[54:57]
	v_mfma_f32_16x16x32_bf16 v[50:53], v[180:183], v[188:191], v[50:53]
	v_mfma_f32_16x16x32_bf16 v[38:41], v[170:173], v[196:199], v[38:41]
	v_mfma_f32_16x16x32_bf16 v[34:37], v[180:183], v[196:199], v[34:37]
	v_mfma_f32_16x16x32_bf16 v[22:25], v[170:173], v[204:207], v[22:25]
	v_mfma_f32_16x16x32_bf16 v[18:21], v[180:183], v[204:207], v[18:21]
	v_mfma_f32_16x16x32_bf16 v[6:9], v[170:173], v[212:215], v[6:9]
	v_mfma_f32_16x16x32_bf16 v[2:5], v[180:183], v[212:215], v[2:5]
	s_setprio 0
	s_barrier
	s_add_u32 s71, s71, 0x100
	s_addc_u32 s72, s72, 0
	s_add_u32 s58, s58, 0x100
	s_addc_u32 s59, s59, 0
	s_cmp_ge_i32 s73, s0
	s_mov_b32 s60, s73
	s_cbranch_scc0 .LBB0_229
	s_branch .Lpeelexitph1b
	.p2align	6

.Lpeelph1f_0:
	s_add_i32 s71, s58, 2
	s_add_u32 s59, s54, 0xfffe0080
	s_addc_u32 s60, s55, -1
	s_add_i32 s72, 0, 0x10000
	s_cmp_eq_u32 s65, s58
	s_cselect_b32 s61, s39, s60
	s_cselect_b32 s60, s41, s59
	s_cselect_b32 s59, s43, s70
	s_cselect_b32 s58, s53, s69
	s_add_i32 s73, 0, 0x14000
	v_add_u32_e32 v2, s72, v198
	v_add_u32_e32 v6, s73, v198
	ds_read_b128 v[26:29], v2
	ds_read_b128 v[30:33], v2 offset:1024
	ds_read_b128 v[18:21], v2 offset:2048
	ds_read_b128 v[22:25], v2 offset:3072
	ds_read_b128 v[10:13], v6
	ds_read_b128 v[14:17], v6 offset:1024
	ds_read_b128 v[2:5], v6 offset:2048
	ds_read_b128 v[6:9], v6 offset:3072
	v_lshl_add_u64 v[170:171], s[54:55], 0, v[186:187]
	s_add_i32 m0, s8, 0xc000
	ds_read_b128 v[188:191], v200
	ds_read_b128 v[192:195], v200 offset:1024
	ds_read_b128 v[202:205], v200 offset:2048
	ds_read_b128 v[206:209], v200 offset:3072
	ds_read_b128 v[210:213], v200 offset:4096
	ds_read_b128 v[214:217], v200 offset:5120
	ds_read_b128 v[236:239], v200 offset:6144
	ds_read_b128 v[240:243], v200 offset:7168
	global_load_lds_dwordx4 v[170:171], off
	v_lshl_add_u64 v[170:171], s[54:55], 0, v[184:185]
	s_add_i32 m0, s8, 0xe000
	s_nop 0
	global_load_lds_dwordx4 v[170:171], off
	s_waitcnt vmcnt(8)
	s_waitcnt lgkmcnt(0)
	s_barrier
	s_setprio 1
	v_mfma_scale_f32_16x16x128_f8f6f4 v[158:161], v[26:33], v[188:195], 0, v196, v169 op_sel_hi:[0,0,0]
	v_mfma_scale_f32_16x16x128_f8f6f4 v[154:157], v[18:25], v[188:195], 0, v196, v169 op_sel_hi:[0,0,0]
	v_mfma_scale_f32_16x16x128_f8f6f4 v[142:145], v[26:33], v[202:209], 0, v196, v169 op_sel_hi:[0,0,0]
	v_mfma_scale_f32_16x16x128_f8f6f4 v[138:141], v[18:25], v[202:209], 0, v196, v169 op_sel_hi:[0,0,0]
	v_mfma_scale_f32_16x16x128_f8f6f4 v[126:129], v[26:33], v[210:217], 0, v196, v169 op_sel_hi:[0,0,0]
	v_mfma_scale_f32_16x16x128_f8f6f4 v[122:125], v[18:25], v[210:217], 0, v196, v169 op_sel_hi:[0,0,0]
	v_mfma_scale_f32_16x16x128_f8f6f4 v[110:113], v[26:33], v[236:243], 0, v196, v169 op_sel_hi:[0,0,0]
	v_mfma_scale_f32_16x16x128_f8f6f4 v[106:109], v[18:25], v[236:243], 0, v196, v169 op_sel_hi:[0,0,0]
	s_setprio 0
	s_setprio 1
	v_mfma_scale_f32_16x16x128_f8f6f4 v[150:153], v[10:17], v[188:195], 0, v196, v169 op_sel_hi:[0,0,0]
	v_mfma_scale_f32_16x16x128_f8f6f4 v[146:149], v[2:9], v[188:195], 0, v196, v169 op_sel_hi:[0,0,0]
	v_mfma_scale_f32_16x16x128_f8f6f4 v[134:137], v[10:17], v[202:209], 0, v196, v169 op_sel_hi:[0,0,0]
	v_mfma_scale_f32_16x16x128_f8f6f4 v[130:133], v[2:9], v[202:209], 0, v196, v169 op_sel_hi:[0,0,0]
	v_mfma_scale_f32_16x16x128_f8f6f4 v[118:121], v[10:17], v[210:217], 0, v196, v169 op_sel_hi:[0,0,0]
	v_mfma_scale_f32_16x16x128_f8f6f4 v[114:117], v[2:9], v[210:217], 0, v196, v169 op_sel_hi:[0,0,0]
	v_mfma_scale_f32_16x16x128_f8f6f4 v[102:105], v[10:17], v[236:243], 0, v196, v169 op_sel_hi:[0,0,0]
	v_mfma_scale_f32_16x16x128_f8f6f4 v[98:101], v[2:9], v[236:243], 0, v196, v169 op_sel_hi:[0,0,0]
	s_setprio 0
	s_barrier
	s_add_i32 s72, s72, s1
	v_lshl_add_u64 v[188:189], s[58:59], 0, v[162:163]
	s_mov_b32 m0, s72
	ds_read_b128 v[202:205], v200 offset:16384
	ds_read_b128 v[206:209], v200 offset:17408
	ds_read_b128 v[210:213], v200 offset:18432
	ds_read_b128 v[214:217], v200 offset:19456
	ds_read_b128 v[236:239], v200 offset:20480
	ds_read_b128 v[240:243], v200 offset:21504
	ds_read_b128 v[244:247], v200 offset:22528
	ds_read_b128 v[248:251], v200 offset:23552
	global_load_lds_dwordx4 v[188:189], off
	s_add_i32 m0, s72, 0x2000
	s_add_u32 s74, s58, 0x20000
	v_lshl_add_u64 v[190:191], s[58:59], 0, v[164:165]
	s_addc_u32 s75, s59, 0
	s_add_i32 s72, s73, s1
	global_load_lds_dwordx4 v[190:191], off
	v_lshl_add_u64 v[170:171], s[74:75], 0, v[162:163]
	s_mov_b32 m0, s72
	v_lshl_add_u64 v[192:193], s[60:61], 0, v[178:179]
	global_load_lds_dwordx4 v[170:171], off
	v_lshl_add_u64 v[170:171], s[74:75], 0, v[164:165]
	s_add_i32 m0, s72, 0x2000
	v_lshl_add_u64 v[194:195], s[60:61], 0, v[180:181]
	global_load_lds_dwordx4 v[170:171], off
	s_mov_b32 m0, s8
	s_nop 0
	global_load_lds_dwordx4 v[192:193], off
	s_mov_b32 m0, s11
	s_nop 0
	global_load_lds_dwordx4 v[194:195], off
	s_waitcnt vmcnt(8)
	s_waitcnt lgkmcnt(0)
	s_barrier
	s_setprio 1
	v_mfma_scale_f32_16x16x128_f8f6f4 v[94:97], v[26:33], v[202:209], 0, v196, v169 op_sel_hi:[0,0,0]
	v_mfma_scale_f32_16x16x128_f8f6f4 v[90:93], v[18:25], v[202:209], 0, v196, v169 op_sel_hi:[0,0,0]
	v_mfma_scale_f32_16x16x128_f8f6f4 v[78:81], v[26:33], v[210:217], 0, v196, v169 op_sel_hi:[0,0,0]
	v_mfma_scale_f32_16x16x128_f8f6f4 v[74:77], v[18:25], v[210:217], 0, v196, v169 op_sel_hi:[0,0,0]
	v_mfma_scale_f32_16x16x128_f8f6f4 v[62:65], v[26:33], v[236:243], 0, v196, v169 op_sel_hi:[0,0,0]
	v_mfma_scale_f32_16x16x128_f8f6f4 v[58:61], v[18:25], v[236:243], 0, v196, v169 op_sel_hi:[0,0,0]
	v_mfma_scale_f32_16x16x128_f8f6f4 v[46:49], v[26:33], v[244:251], 0, v196, v169 op_sel_hi:[0,0,0]
	v_mfma_scale_f32_16x16x128_f8f6f4 v[42:45], v[18:25], v[244:251], 0, v196, v169 op_sel_hi:[0,0,0]
	s_setprio 0
	s_setprio 1
	v_mfma_scale_f32_16x16x128_f8f6f4 v[86:89], v[10:17], v[202:209], 0, v196, v169 op_sel_hi:[0,0,0]
	v_mfma_scale_f32_16x16x128_f8f6f4 v[82:85], v[2:9], v[202:209], 0, v196, v169 op_sel_hi:[0,0,0]
	v_mfma_scale_f32_16x16x128_f8f6f4 v[70:73], v[10:17], v[210:217], 0, v196, v169 op_sel_hi:[0,0,0]
	v_mfma_scale_f32_16x16x128_f8f6f4 v[66:69], v[2:9], v[210:217], 0, v196, v169 op_sel_hi:[0,0,0]
	v_mfma_scale_f32_16x16x128_f8f6f4 v[54:57], v[10:17], v[236:243], 0, v196, v169 op_sel_hi:[0,0,0]
	v_mfma_scale_f32_16x16x128_f8f6f4 v[50:53], v[2:9], v[236:243], 0, v196, v169 op_sel_hi:[0,0,0]
	v_mfma_scale_f32_16x16x128_f8f6f4 v[38:41], v[10:17], v[244:251], 0, v196, v169 op_sel_hi:[0,0,0]
	v_mfma_scale_f32_16x16x128_f8f6f4 v[34:37], v[2:9], v[244:251], 0, v196, v169 op_sel_hi:[0,0,0]
	s_setprio 0
	s_barrier
	s_add_i32 s72, 0, 0x18000
	s_add_i32 s73, 0, 0x1c000
	v_add_u32_e32 v2, s72, v198
	v_add_u32_e32 v6, s73, v198
	ds_read_b128 v[26:29], v2
	ds_read_b128 v[30:33], v2 offset:1024
	ds_read_b128 v[18:21], v2 offset:2048
	ds_read_b128 v[22:25], v2 offset:3072
	ds_read_b128 v[10:13], v6
	ds_read_b128 v[14:17], v6 offset:1024
	ds_read_b128 v[2:5], v6 offset:2048
	ds_read_b128 v[6:9], v6 offset:3072
	s_add_u32 s60, s60, 0x20000
	s_addc_u32 s61, s61, 0
	s_mov_b32 m0, s16
	v_lshl_add_u64 v[170:171], s[60:61], 0, v[178:179]
	ds_read_b128 v[202:205], v200 offset:32768
	ds_read_b128 v[206:209], v200 offset:33792
	ds_read_b128 v[210:213], v200 offset:34816
	ds_read_b128 v[214:217], v200 offset:35840
	ds_read_b128 v[236:239], v200 offset:36864
	ds_read_b128 v[240:243], v200 offset:37888
	ds_read_b128 v[244:247], v200 offset:38912
	ds_read_b128 v[248:251], v200 offset:39936
	global_load_lds_dwordx4 v[170:171], off
	v_lshl_add_u64 v[170:171], s[60:61], 0, v[180:181]
	s_mov_b32 m0, s25
	s_nop 0
	global_load_lds_dwordx4 v[170:171], off
	s_waitcnt vmcnt(8)
	s_waitcnt lgkmcnt(0)
	s_barrier
	s_setprio 1
	v_mfma_scale_f32_16x16x128_f8f6f4 v[158:161], v[26:33], v[202:209], v[158:161], v196, v169 op_sel_hi:[0,0,0]
	v_mfma_scale_f32_16x16x128_f8f6f4 v[154:157], v[18:25], v[202:209], v[154:157], v196, v169 op_sel_hi:[0,0,0]
	v_mfma_scale_f32_16x16x128_f8f6f4 v[142:145], v[26:33], v[210:217], v[142:145], v196, v169 op_sel_hi:[0,0,0]
	v_mfma_scale_f32_16x16x128_f8f6f4 v[138:141], v[18:25], v[210:217], v[138:141], v196, v169 op_sel_hi:[0,0,0]
	v_mfma_scale_f32_16x16x128_f8f6f4 v[126:129], v[26:33], v[236:243], v[126:129], v196, v169 op_sel_hi:[0,0,0]
	v_mfma_scale_f32_16x16x128_f8f6f4 v[122:125], v[18:25], v[236:243], v[122:125], v196, v169 op_sel_hi:[0,0,0]
	v_mfma_scale_f32_16x16x128_f8f6f4 v[110:113], v[26:33], v[244:251], v[110:113], v196, v169 op_sel_hi:[0,0,0]
	v_mfma_scale_f32_16x16x128_f8f6f4 v[106:109], v[18:25], v[244:251], v[106:109], v196, v169 op_sel_hi:[0,0,0]
	s_setprio 0
	s_setprio 1
	v_mfma_scale_f32_16x16x128_f8f6f4 v[150:153], v[10:17], v[202:209], v[150:153], v196, v169 op_sel_hi:[0,0,0]
	v_mfma_scale_f32_16x16x128_f8f6f4 v[146:149], v[2:9], v[202:209], v[146:149], v196, v169 op_sel_hi:[0,0,0]
	v_mfma_scale_f32_16x16x128_f8f6f4 v[134:137], v[10:17], v[210:217], v[134:137], v196, v169 op_sel_hi:[0,0,0]
	v_mfma_scale_f32_16x16x128_f8f6f4 v[130:133], v[2:9], v[210:217], v[130:133], v196, v169 op_sel_hi:[0,0,0]
	v_mfma_scale_f32_16x16x128_f8f6f4 v[118:121], v[10:17], v[236:243], v[118:121], v196, v169 op_sel_hi:[0,0,0]
	v_mfma_scale_f32_16x16x128_f8f6f4 v[114:117], v[2:9], v[236:243], v[114:117], v196, v169 op_sel_hi:[0,0,0]
	v_mfma_scale_f32_16x16x128_f8f6f4 v[102:105], v[10:17], v[244:251], v[102:105], v196, v169 op_sel_hi:[0,0,0]
	v_mfma_scale_f32_16x16x128_f8f6f4 v[98:101], v[2:9], v[244:251], v[98:101], v196, v169 op_sel_hi:[0,0,0]
	s_setprio 0
	s_barrier
	s_add_i32 s60, s72, s1
	v_lshl_add_u64 v[170:171], v[188:189], 0, s[56:57]
	s_mov_b32 m0, s60
	ds_read_b128 v[202:205], v200 offset:49152
	ds_read_b128 v[206:209], v200 offset:50176
	ds_read_b128 v[210:213], v200 offset:51200
	ds_read_b128 v[214:217], v200 offset:52224
	ds_read_b128 v[236:239], v200 offset:53248
	ds_read_b128 v[240:243], v200 offset:54272
	ds_read_b128 v[244:247], v200 offset:55296
	ds_read_b128 v[248:251], v200 offset:56320
	global_load_lds_dwordx4 v[170:171], off
	s_add_i32 m0, s60, 0x2000
	s_add_u32 s58, s58, 0x20080
	v_lshl_add_u64 v[170:171], v[190:191], 0, s[56:57]
	s_addc_u32 s59, s59, 0
	s_add_i32 s60, s73, s1
	global_load_lds_dwordx4 v[170:171], off
	v_lshl_add_u64 v[170:171], s[58:59], 0, v[162:163]
	s_mov_b32 m0, s60
	s_nop 0
	global_load_lds_dwordx4 v[170:171], off
	v_lshl_add_u64 v[170:171], s[58:59], 0, v[164:165]
	s_add_i32 m0, s60, 0x2000
	s_nop 0
	global_load_lds_dwordx4 v[170:171], off
	v_lshl_add_u64 v[170:171], v[192:193], 0, s[56:57]
	s_mov_b32 m0, s62
	s_nop 0
	global_load_lds_dwordx4 v[170:171], off
	v_lshl_add_u64 v[170:171], v[194:195], 0, s[56:57]
	s_mov_b32 m0, s63
	s_nop 0
	global_load_lds_dwordx4 v[170:171], off
	s_waitcnt vmcnt(8)
	s_waitcnt lgkmcnt(0)
	s_barrier
	s_setprio 1
	v_mfma_scale_f32_16x16x128_f8f6f4 v[94:97], v[26:33], v[202:209], v[94:97], v196, v169 op_sel_hi:[0,0,0]
	v_mfma_scale_f32_16x16x128_f8f6f4 v[90:93], v[18:25], v[202:209], v[90:93], v196, v169 op_sel_hi:[0,0,0]
	v_mfma_scale_f32_16x16x128_f8f6f4 v[78:81], v[26:33], v[210:217], v[78:81], v196, v169 op_sel_hi:[0,0,0]
	v_mfma_scale_f32_16x16x128_f8f6f4 v[74:77], v[18:25], v[210:217], v[74:77], v196, v169 op_sel_hi:[0,0,0]
	v_mfma_scale_f32_16x16x128_f8f6f4 v[62:65], v[26:33], v[236:243], v[62:65], v196, v169 op_sel_hi:[0,0,0]
	v_mfma_scale_f32_16x16x128_f8f6f4 v[58:61], v[18:25], v[236:243], v[58:61], v196, v169 op_sel_hi:[0,0,0]
	v_mfma_scale_f32_16x16x128_f8f6f4 v[46:49], v[26:33], v[244:251], v[46:49], v196, v169 op_sel_hi:[0,0,0]
	v_mfma_scale_f32_16x16x128_f8f6f4 v[42:45], v[18:25], v[244:251], v[42:45], v196, v169 op_sel_hi:[0,0,0]
	s_setprio 0
	s_setprio 1
	v_mfma_scale_f32_16x16x128_f8f6f4 v[86:89], v[10:17], v[202:209], v[86:89], v196, v169 op_sel_hi:[0,0,0]
	v_mfma_scale_f32_16x16x128_f8f6f4 v[82:85], v[2:9], v[202:209], v[82:85], v196, v169 op_sel_hi:[0,0,0]
	v_mfma_scale_f32_16x16x128_f8f6f4 v[70:73], v[10:17], v[210:217], v[70:73], v196, v169 op_sel_hi:[0,0,0]
	v_mfma_scale_f32_16x16x128_f8f6f4 v[66:69], v[2:9], v[210:217], v[66:69], v196, v169 op_sel_hi:[0,0,0]
	v_mfma_scale_f32_16x16x128_f8f6f4 v[54:57], v[10:17], v[236:243], v[54:57], v196, v169 op_sel_hi:[0,0,0]
	v_mfma_scale_f32_16x16x128_f8f6f4 v[50:53], v[2:9], v[236:243], v[50:53], v196, v169 op_sel_hi:[0,0,0]
	v_mfma_scale_f32_16x16x128_f8f6f4 v[38:41], v[10:17], v[244:251], v[38:41], v196, v169 op_sel_hi:[0,0,0]
	v_mfma_scale_f32_16x16x128_f8f6f4 v[34:37], v[2:9], v[244:251], v[34:37], v196, v169 op_sel_hi:[0,0,0]
	s_setprio 0
	s_barrier
	s_add_u32 s69, s69, 0x100
	s_addc_u32 s70, s70, 0
	s_add_u32 s54, s54, 0x100
	s_addc_u32 s55, s55, 0
	s_cmp_ge_i32 s71, s0
	s_mov_b32 s58, s71
	s_cbranch_scc0 .LBB0_298
	s_branch .Lpeelexitph1f
	.p2align	6

.Lpeelph3_0:
	s_add_i32 s73, s68, 2
	s_add_u32 s69, s64, 0xfffc0080
	s_addc_u32 s70, s65, -1
	s_add_i32 s74, 0, 0x10000
	s_cmp_eq_u32 s24, s68
	s_cselect_b32 s71, s59, s70
	s_cselect_b32 s70, s58, s69
	s_cselect_b32 s69, s51, s72
	s_cselect_b32 s68, s53, s66
	s_add_i32 s76, 0, 0x14000
	v_add_u32_e32 v152, s74, v220
	v_add_u32_e32 v164, s76, v220
	ds_read_b128 v[106:109], v152
	ds_read_b128 v[110:113], v152 offset:1024
	ds_read_b128 v[114:117], v152 offset:2048
	ds_read_b128 v[152:155], v152 offset:3072
	ds_read_b128 v[156:159], v164
	ds_read_b128 v[160:163], v164 offset:1024
	ds_read_b128 v[170:173], v164 offset:2048
	ds_read_b128 v[174:177], v164 offset:3072
	v_lshl_add_u64 v[164:165], s[64:65], 0, v[150:151]
	s_add_i32 m0, s14, 0xc000
	ds_read_b128 v[178:181], v222
	ds_read_b128 v[182:185], v222 offset:1024
	ds_read_b128 v[186:189], v222 offset:2048
	ds_read_b128 v[190:193], v222 offset:3072
	ds_read_b128 v[194:197], v222 offset:4096
	ds_read_b128 v[198:201], v222 offset:5120
	ds_read_b128 v[202:205], v222 offset:6144
	ds_read_b128 v[206:209], v222 offset:7168
	global_load_lds_dwordx4 v[164:165], off
	v_lshl_add_u64 v[164:165], s[64:65], 0, v[148:149]
	s_add_i32 m0, s14, 0xe000
	s_nop 0
	global_load_lds_dwordx4 v[164:165], off
	s_waitcnt vmcnt(8)
	s_waitcnt lgkmcnt(0)
	s_barrier
	s_setprio 1
	v_mfma_f32_16x16x32_bf16 v[138:141], v[106:109], v[178:181], 0
	v_mfma_f32_16x16x32_bf16 v[62:65], v[114:117], v[178:181], 0
	v_mfma_f32_16x16x32_bf16 v[130:133], v[106:109], v[186:189], 0
	v_mfma_f32_16x16x32_bf16 v[54:57], v[114:117], v[186:189], 0
	v_mfma_f32_16x16x32_bf16 v[122:125], v[106:109], v[194:197], 0
	v_mfma_f32_16x16x32_bf16 v[46:49], v[114:117], v[194:197], 0
	v_mfma_f32_16x16x32_bf16 v[102:105], v[106:109], v[202:205], 0
	v_mfma_f32_16x16x32_bf16 v[38:41], v[114:117], v[202:205], 0
	v_mfma_f32_16x16x32_bf16 v[138:141], v[110:113], v[182:185], v[138:141]
	v_mfma_f32_16x16x32_bf16 v[62:65], v[152:155], v[182:185], v[62:65]
	v_mfma_f32_16x16x32_bf16 v[130:133], v[110:113], v[190:193], v[130:133]
	v_mfma_f32_16x16x32_bf16 v[54:57], v[152:155], v[190:193], v[54:57]
	v_mfma_f32_16x16x32_bf16 v[122:125], v[110:113], v[198:201], v[122:125]
	v_mfma_f32_16x16x32_bf16 v[46:49], v[152:155], v[198:201], v[46:49]
	v_mfma_f32_16x16x32_bf16 v[102:105], v[110:113], v[206:209], v[102:105]
	v_mfma_f32_16x16x32_bf16 v[38:41], v[152:155], v[206:209], v[38:41]
	s_setprio 0
	s_setprio 1
	v_mfma_f32_16x16x32_bf16 v[134:137], v[156:159], v[178:181], 0
	v_mfma_f32_16x16x32_bf16 v[58:61], v[170:173], v[178:181], 0
	v_mfma_f32_16x16x32_bf16 v[126:129], v[156:159], v[186:189], 0
	v_mfma_f32_16x16x32_bf16 v[50:53], v[170:173], v[186:189], 0
	v_mfma_f32_16x16x32_bf16 v[118:121], v[156:159], v[194:197], 0
	v_mfma_f32_16x16x32_bf16 v[42:45], v[170:173], v[194:197], 0
	v_mfma_f32_16x16x32_bf16 v[98:101], v[156:159], v[202:205], 0
	v_mfma_f32_16x16x32_bf16 v[34:37], v[170:173], v[202:205], 0
	v_mfma_f32_16x16x32_bf16 v[134:137], v[160:163], v[182:185], v[134:137]
	v_mfma_f32_16x16x32_bf16 v[58:61], v[174:177], v[182:185], v[58:61]
	v_mfma_f32_16x16x32_bf16 v[126:129], v[160:163], v[190:193], v[126:129]
	v_mfma_f32_16x16x32_bf16 v[50:53], v[174:177], v[190:193], v[50:53]
	v_mfma_f32_16x16x32_bf16 v[118:121], v[160:163], v[198:201], v[118:121]
	v_mfma_f32_16x16x32_bf16 v[42:45], v[174:177], v[198:201], v[42:45]
	v_mfma_f32_16x16x32_bf16 v[98:101], v[160:163], v[206:209], v[98:101]
	v_mfma_f32_16x16x32_bf16 v[34:37], v[174:177], v[206:209], v[34:37]
	s_setprio 0
	s_barrier
	s_add_i32 s74, s74, s13
	v_lshl_add_u64 v[164:165], s[68:69], 0, v[166:167]
	s_mov_b32 m0, s74
	ds_read_b128 v[178:181], v222 offset:16384
	ds_read_b128 v[182:185], v222 offset:17408
	ds_read_b128 v[186:189], v222 offset:18432
	ds_read_b128 v[190:193], v222 offset:19456
	ds_read_b128 v[194:197], v222 offset:20480
	ds_read_b128 v[198:201], v222 offset:21504
	ds_read_b128 v[202:205], v222 offset:22528
	ds_read_b128 v[206:209], v222 offset:23552
	global_load_lds_dwordx4 v[164:165], off
	s_add_i32 m0, s74, 0x2000
	s_add_u32 s74, s68, 0x8000
	v_lshl_add_u64 v[210:211], s[68:69], 0, v[142:143]
	s_addc_u32 s75, s69, 0
	s_add_i32 s76, s76, s13
	global_load_lds_dwordx4 v[210:211], off
	v_lshl_add_u64 v[212:213], s[74:75], 0, v[166:167]
	s_mov_b32 m0, s76
	v_lshl_add_u64 v[214:215], s[70:71], 0, v[146:147]
	global_load_lds_dwordx4 v[212:213], off
	v_lshl_add_u64 v[212:213], s[74:75], 0, v[142:143]
	s_add_i32 m0, s76, 0x2000
	s_nop 0
	global_load_lds_dwordx4 v[212:213], off
	v_lshl_add_u64 v[212:213], s[70:71], 0, v[144:145]
	s_mov_b32 m0, s14
	s_nop 0
	global_load_lds_dwordx4 v[212:213], off
	s_mov_b32 m0, s15
	s_nop 0
	global_load_lds_dwordx4 v[214:215], off
	s_waitcnt vmcnt(8)
	s_waitcnt lgkmcnt(0)
	s_barrier
	s_setprio 1
	v_mfma_f32_16x16x32_bf16 v[94:97], v[106:109], v[178:181], 0
	v_mfma_f32_16x16x32_bf16 v[30:33], v[114:117], v[178:181], 0
	v_mfma_f32_16x16x32_bf16 v[86:89], v[106:109], v[186:189], 0
	v_mfma_f32_16x16x32_bf16 v[22:25], v[114:117], v[186:189], 0
	v_mfma_f32_16x16x32_bf16 v[78:81], v[106:109], v[194:197], 0
	v_mfma_f32_16x16x32_bf16 v[14:17], v[114:117], v[194:197], 0
	v_mfma_f32_16x16x32_bf16 v[70:73], v[106:109], v[202:205], 0
	v_mfma_f32_16x16x32_bf16 v[6:9], v[114:117], v[202:205], 0
	v_mfma_f32_16x16x32_bf16 v[94:97], v[110:113], v[182:185], v[94:97]
	v_mfma_f32_16x16x32_bf16 v[30:33], v[152:155], v[182:185], v[30:33]
	v_mfma_f32_16x16x32_bf16 v[86:89], v[110:113], v[190:193], v[86:89]
	v_mfma_f32_16x16x32_bf16 v[22:25], v[152:155], v[190:193], v[22:25]
	v_mfma_f32_16x16x32_bf16 v[78:81], v[110:113], v[198:201], v[78:81]
	v_mfma_f32_16x16x32_bf16 v[14:17], v[152:155], v[198:201], v[14:17]
	v_mfma_f32_16x16x32_bf16 v[70:73], v[110:113], v[206:209], v[70:73]
	v_mfma_f32_16x16x32_bf16 v[6:9], v[152:155], v[206:209], v[6:9]
	s_setprio 0
	s_setprio 1
	v_mfma_f32_16x16x32_bf16 v[90:93], v[156:159], v[178:181], 0
	v_mfma_f32_16x16x32_bf16 v[26:29], v[170:173], v[178:181], 0
	v_mfma_f32_16x16x32_bf16 v[82:85], v[156:159], v[186:189], 0
	v_mfma_f32_16x16x32_bf16 v[18:21], v[170:173], v[186:189], 0
	v_mfma_f32_16x16x32_bf16 v[74:77], v[156:159], v[194:197], 0
	v_mfma_f32_16x16x32_bf16 v[10:13], v[170:173], v[194:197], 0
	v_mfma_f32_16x16x32_bf16 v[66:69], v[156:159], v[202:205], 0
	v_mfma_f32_16x16x32_bf16 v[2:5], v[170:173], v[202:205], 0
	v_mfma_f32_16x16x32_bf16 v[90:93], v[160:163], v[182:185], v[90:93]
	v_mfma_f32_16x16x32_bf16 v[26:29], v[174:177], v[182:185], v[26:29]
	v_mfma_f32_16x16x32_bf16 v[82:85], v[160:163], v[190:193], v[82:85]
	v_mfma_f32_16x16x32_bf16 v[18:21], v[174:177], v[190:193], v[18:21]
	v_mfma_f32_16x16x32_bf16 v[74:77], v[160:163], v[198:201], v[74:77]
	v_mfma_f32_16x16x32_bf16 v[10:13], v[174:177], v[198:201], v[10:13]
	v_mfma_f32_16x16x32_bf16 v[66:69], v[160:163], v[206:209], v[66:69]
	v_mfma_f32_16x16x32_bf16 v[2:5], v[174:177], v[206:209], v[2:5]
	s_setprio 0
	s_barrier
	s_add_i32 s74, 0, 0x18000
	s_add_i32 s75, 0, 0x1c000
	v_add_u32_e32 v152, s74, v220
	v_add_u32_e32 v174, s75, v220
	ds_read_b128 v[106:109], v152
	ds_read_b128 v[110:113], v152 offset:1024
	ds_read_b128 v[114:117], v152 offset:2048
	ds_read_b128 v[152:155], v152 offset:3072
	ds_read_b128 v[156:159], v174
	ds_read_b128 v[160:163], v174 offset:1024
	ds_read_b128 v[170:173], v174 offset:2048
	ds_read_b128 v[174:177], v174 offset:3072
	s_add_u32 s70, s70, 0x40000
	s_addc_u32 s71, s71, 0
	s_mov_b32 m0, s16
	v_lshl_add_u64 v[216:217], s[70:71], 0, v[144:145]
	ds_read_b128 v[178:181], v222 offset:32768
	ds_read_b128 v[182:185], v222 offset:33792
	ds_read_b128 v[186:189], v222 offset:34816
	ds_read_b128 v[190:193], v222 offset:35840
	ds_read_b128 v[194:197], v222 offset:36864
	ds_read_b128 v[198:201], v222 offset:37888
	ds_read_b128 v[202:205], v222 offset:38912
	ds_read_b128 v[206:209], v222 offset:39936
	global_load_lds_dwordx4 v[216:217], off
	v_lshl_add_u64 v[216:217], s[70:71], 0, v[146:147]
	s_mov_b32 m0, s20
	s_nop 0
	global_load_lds_dwordx4 v[216:217], off
	s_waitcnt vmcnt(8)
	s_waitcnt lgkmcnt(0)
	s_barrier
	s_setprio 1
	v_mfma_f32_16x16x32_bf16 v[138:141], v[106:109], v[178:181], v[138:141]
	v_mfma_f32_16x16x32_bf16 v[62:65], v[114:117], v[178:181], v[62:65]
	v_mfma_f32_16x16x32_bf16 v[130:133], v[106:109], v[186:189], v[130:133]
	v_mfma_f32_16x16x32_bf16 v[54:57], v[114:117], v[186:189], v[54:57]
	v_mfma_f32_16x16x32_bf16 v[122:125], v[106:109], v[194:197], v[122:125]
	v_mfma_f32_16x16x32_bf16 v[46:49], v[114:117], v[194:197], v[46:49]
	v_mfma_f32_16x16x32_bf16 v[102:105], v[106:109], v[202:205], v[102:105]
	v_mfma_f32_16x16x32_bf16 v[38:41], v[114:117], v[202:205], v[38:41]
	v_mfma_f32_16x16x32_bf16 v[138:141], v[110:113], v[182:185], v[138:141]
	v_mfma_f32_16x16x32_bf16 v[62:65], v[152:155], v[182:185], v[62:65]
	v_mfma_f32_16x16x32_bf16 v[130:133], v[110:113], v[190:193], v[130:133]
	v_mfma_f32_16x16x32_bf16 v[54:57], v[152:155], v[190:193], v[54:57]
	v_mfma_f32_16x16x32_bf16 v[122:125], v[110:113], v[198:201], v[122:125]
	v_mfma_f32_16x16x32_bf16 v[46:49], v[152:155], v[198:201], v[46:49]
	v_mfma_f32_16x16x32_bf16 v[102:105], v[110:113], v[206:209], v[102:105]
	v_mfma_f32_16x16x32_bf16 v[38:41], v[152:155], v[206:209], v[38:41]
	s_setprio 0
	s_setprio 1
	v_mfma_f32_16x16x32_bf16 v[134:137], v[156:159], v[178:181], v[134:137]
	v_mfma_f32_16x16x32_bf16 v[58:61], v[170:173], v[178:181], v[58:61]
	v_mfma_f32_16x16x32_bf16 v[126:129], v[156:159], v[186:189], v[126:129]
	v_mfma_f32_16x16x32_bf16 v[50:53], v[170:173], v[186:189], v[50:53]
	v_mfma_f32_16x16x32_bf16 v[118:121], v[156:159], v[194:197], v[118:121]
	v_mfma_f32_16x16x32_bf16 v[42:45], v[170:173], v[194:197], v[42:45]
	v_mfma_f32_16x16x32_bf16 v[98:101], v[156:159], v[202:205], v[98:101]
	v_mfma_f32_16x16x32_bf16 v[34:37], v[170:173], v[202:205], v[34:37]
	v_mfma_f32_16x16x32_bf16 v[134:137], v[160:163], v[182:185], v[134:137]
	v_mfma_f32_16x16x32_bf16 v[58:61], v[174:177], v[182:185], v[58:61]
	v_mfma_f32_16x16x32_bf16 v[126:129], v[160:163], v[190:193], v[126:129]
	v_mfma_f32_16x16x32_bf16 v[50:53], v[174:177], v[190:193], v[50:53]
	v_mfma_f32_16x16x32_bf16 v[118:121], v[160:163], v[198:201], v[118:121]
	v_mfma_f32_16x16x32_bf16 v[42:45], v[174:177], v[198:201], v[42:45]
	v_mfma_f32_16x16x32_bf16 v[98:101], v[160:163], v[206:209], v[98:101]
	v_mfma_f32_16x16x32_bf16 v[34:37], v[174:177], v[206:209], v[34:37]
	s_setprio 0
	s_barrier
	s_add_i32 s70, s74, s13
	v_lshl_add_u64 v[164:165], v[164:165], 0, s[56:57]
	s_mov_b32 m0, s70
	ds_read_b128 v[178:181], v222 offset:49152
	ds_read_b128 v[182:185], v222 offset:50176
	ds_read_b128 v[186:189], v222 offset:51200
	ds_read_b128 v[190:193], v222 offset:52224
	ds_read_b128 v[194:197], v222 offset:53248
	ds_read_b128 v[198:201], v222 offset:54272
	ds_read_b128 v[202:205], v222 offset:55296
	ds_read_b128 v[206:209], v222 offset:56320
	global_load_lds_dwordx4 v[164:165], off
	s_add_i32 m0, s70, 0x2000
	s_add_u32 s68, s68, 0x8080
	v_lshl_add_u64 v[164:165], v[210:211], 0, s[56:57]
	s_addc_u32 s69, s69, 0
	s_add_i32 s70, s75, s13
	global_load_lds_dwordx4 v[164:165], off
	v_lshl_add_u64 v[164:165], s[68:69], 0, v[166:167]
	s_mov_b32 m0, s70
	s_nop 0
	global_load_lds_dwordx4 v[164:165], off
	v_lshl_add_u64 v[164:165], s[68:69], 0, v[142:143]
	s_add_i32 m0, s70, 0x2000
	s_nop 0
	global_load_lds_dwordx4 v[164:165], off
	v_lshl_add_u64 v[164:165], v[212:213], 0, s[56:57]
	s_mov_b32 m0, s21
	s_nop 0
	global_load_lds_dwordx4 v[164:165], off
	v_lshl_add_u64 v[164:165], v[214:215], 0, s[56:57]
	s_mov_b32 m0, s22
	s_nop 0
	global_load_lds_dwordx4 v[164:165], off
	s_waitcnt vmcnt(8)
	s_waitcnt lgkmcnt(0)
	s_barrier
	s_setprio 1
	v_mfma_f32_16x16x32_bf16 v[94:97], v[106:109], v[178:181], v[94:97]
	v_mfma_f32_16x16x32_bf16 v[30:33], v[114:117], v[178:181], v[30:33]
	v_mfma_f32_16x16x32_bf16 v[86:89], v[106:109], v[186:189], v[86:89]
	v_mfma_f32_16x16x32_bf16 v[22:25], v[114:117], v[186:189], v[22:25]
	v_mfma_f32_16x16x32_bf16 v[78:81], v[106:109], v[194:197], v[78:81]
	v_mfma_f32_16x16x32_bf16 v[14:17], v[114:117], v[194:197], v[14:17]
	v_mfma_f32_16x16x32_bf16 v[70:73], v[106:109], v[202:205], v[70:73]
	v_mfma_f32_16x16x32_bf16 v[6:9], v[114:117], v[202:205], v[6:9]
	v_mfma_f32_16x16x32_bf16 v[94:97], v[110:113], v[182:185], v[94:97]
	v_mfma_f32_16x16x32_bf16 v[30:33], v[152:155], v[182:185], v[30:33]
	v_mfma_f32_16x16x32_bf16 v[86:89], v[110:113], v[190:193], v[86:89]
	v_mfma_f32_16x16x32_bf16 v[22:25], v[152:155], v[190:193], v[22:25]
	v_mfma_f32_16x16x32_bf16 v[78:81], v[110:113], v[198:201], v[78:81]
	v_mfma_f32_16x16x32_bf16 v[14:17], v[152:155], v[198:201], v[14:17]
	v_mfma_f32_16x16x32_bf16 v[70:73], v[110:113], v[206:209], v[70:73]
	v_mfma_f32_16x16x32_bf16 v[6:9], v[152:155], v[206:209], v[6:9]
	s_setprio 0
	s_setprio 1
	v_mfma_f32_16x16x32_bf16 v[90:93], v[156:159], v[178:181], v[90:93]
	v_mfma_f32_16x16x32_bf16 v[26:29], v[170:173], v[178:181], v[26:29]
	v_mfma_f32_16x16x32_bf16 v[82:85], v[156:159], v[186:189], v[82:85]
	v_mfma_f32_16x16x32_bf16 v[18:21], v[170:173], v[186:189], v[18:21]
	v_mfma_f32_16x16x32_bf16 v[74:77], v[156:159], v[194:197], v[74:77]
	v_mfma_f32_16x16x32_bf16 v[10:13], v[170:173], v[194:197], v[10:13]
	v_mfma_f32_16x16x32_bf16 v[66:69], v[156:159], v[202:205], v[66:69]
	v_mfma_f32_16x16x32_bf16 v[2:5], v[170:173], v[202:205], v[2:5]
	v_mfma_f32_16x16x32_bf16 v[90:93], v[160:163], v[182:185], v[90:93]
	v_mfma_f32_16x16x32_bf16 v[26:29], v[174:177], v[182:185], v[26:29]
	v_mfma_f32_16x16x32_bf16 v[82:85], v[160:163], v[190:193], v[82:85]
	v_mfma_f32_16x16x32_bf16 v[18:21], v[174:177], v[190:193], v[18:21]
	v_mfma_f32_16x16x32_bf16 v[74:77], v[160:163], v[198:201], v[74:77]
	v_mfma_f32_16x16x32_bf16 v[10:13], v[174:177], v[198:201], v[10:13]
	v_mfma_f32_16x16x32_bf16 v[66:69], v[160:163], v[206:209], v[66:69]
	v_mfma_f32_16x16x32_bf16 v[2:5], v[174:177], v[206:209], v[2:5]
	s_setprio 0
	s_barrier
	s_add_u32 s66, s66, 0x100
	s_addc_u32 s72, s72, 0
	s_add_u32 s64, s64, 0x100
	s_addc_u32 s65, s65, 0
	s_cmp_ge_i32 s73, s1
	s_mov_b32 s68, s73
	s_cbranch_scc0 .LBB0_469
	s_branch .Lpeelexitph3
	.p2align	6

.Lpeelph6_0:
	s_add_i32 s84, s68, 2
	s_add_u32 s69, s74, 0xfffc0080
	s_addc_u32 s70, s75, -1
	s_add_i32 s88, 0, 0x10000
	s_cmp_eq_u32 s72, s68
	s_cselect_b32 s71, s29, s70
	s_cselect_b32 s70, s43, s69
	s_cselect_b32 s69, s55, s79
	s_cselect_b32 s68, s59, s77
	s_add_i32 s92, 0, 0x14000
	v_add_u32_e32 v78, s88, v204
	v_add_u32_e32 v170, s92, v204
	ds_read_b128 v[58:61], v78
	ds_read_b128 v[62:65], v78 offset:1024
	ds_read_b128 v[74:77], v78 offset:2048
	ds_read_b128 v[78:81], v78 offset:3072
	ds_read_b128 v[146:149], v170
	ds_read_b128 v[150:153], v170 offset:1024
	ds_read_b128 v[154:157], v170 offset:2048
	ds_read_b128 v[170:173], v170 offset:3072
	v_lshl_add_u64 v[202:203], s[74:75], 0, v[180:181]
	s_add_i32 m0, s15, 0xc000
	ds_read_b128 v[174:177], v208
	ds_read_b128 v[182:185], v208 offset:1024
	ds_read_b128 v[186:189], v208 offset:2048
	ds_read_b128 v[190:193], v208 offset:3072
	ds_read_b128 v[194:197], v208 offset:4096
	ds_read_b128 v[198:201], v208 offset:5120
	ds_read_b128 v[210:213], v208 offset:6144
	ds_read_b128 v[214:217], v208 offset:7168
	global_load_lds_dwordx4 v[202:203], off
	v_lshl_add_u64 v[202:203], s[74:75], 0, v[178:179]
	s_add_i32 m0, s15, 0xe000
	s_nop 0
	global_load_lds_dwordx4 v[202:203], off
	s_waitcnt vmcnt(8)
	s_waitcnt lgkmcnt(0)
	s_barrier
	s_setprio 1
	v_mfma_f32_16x16x32_bf16 v[142:145], v[58:61], v[174:177], 0
	v_mfma_f32_16x16x32_bf16 v[138:141], v[74:77], v[174:177], 0
	v_mfma_f32_16x16x32_bf16 v[126:129], v[58:61], v[186:189], 0
	v_mfma_f32_16x16x32_bf16 v[122:125], v[74:77], v[186:189], 0
	v_mfma_f32_16x16x32_bf16 v[110:113], v[58:61], v[194:197], 0
	v_mfma_f32_16x16x32_bf16 v[106:109], v[74:77], v[194:197], 0
	v_mfma_f32_16x16x32_bf16 v[94:97], v[58:61], v[210:213], 0
	v_mfma_f32_16x16x32_bf16 v[90:93], v[74:77], v[210:213], 0
	v_mfma_f32_16x16x32_bf16 v[142:145], v[62:65], v[182:185], v[142:145]
	v_mfma_f32_16x16x32_bf16 v[138:141], v[78:81], v[182:185], v[138:141]
	v_mfma_f32_16x16x32_bf16 v[126:129], v[62:65], v[190:193], v[126:129]
	v_mfma_f32_16x16x32_bf16 v[122:125], v[78:81], v[190:193], v[122:125]
	v_mfma_f32_16x16x32_bf16 v[110:113], v[62:65], v[198:201], v[110:113]
	v_mfma_f32_16x16x32_bf16 v[106:109], v[78:81], v[198:201], v[106:109]
	v_mfma_f32_16x16x32_bf16 v[94:97], v[62:65], v[214:217], v[94:97]
	v_mfma_f32_16x16x32_bf16 v[90:93], v[78:81], v[214:217], v[90:93]
	s_setprio 0
	s_setprio 1
	v_mfma_f32_16x16x32_bf16 v[134:137], v[146:149], v[174:177], 0
	v_mfma_f32_16x16x32_bf16 v[130:133], v[154:157], v[174:177], 0
	v_mfma_f32_16x16x32_bf16 v[118:121], v[146:149], v[186:189], 0
	v_mfma_f32_16x16x32_bf16 v[114:117], v[154:157], v[186:189], 0
	v_mfma_f32_16x16x32_bf16 v[102:105], v[146:149], v[194:197], 0
	v_mfma_f32_16x16x32_bf16 v[98:101], v[154:157], v[194:197], 0
	v_mfma_f32_16x16x32_bf16 v[86:89], v[146:149], v[210:213], 0
	v_mfma_f32_16x16x32_bf16 v[82:85], v[154:157], v[210:213], 0
	v_mfma_f32_16x16x32_bf16 v[134:137], v[150:153], v[182:185], v[134:137]
	v_mfma_f32_16x16x32_bf16 v[130:133], v[170:173], v[182:185], v[130:133]
	v_mfma_f32_16x16x32_bf16 v[118:121], v[150:153], v[190:193], v[118:121]
	v_mfma_f32_16x16x32_bf16 v[114:117], v[170:173], v[190:193], v[114:117]
	v_mfma_f32_16x16x32_bf16 v[102:105], v[150:153], v[198:201], v[102:105]
	v_mfma_f32_16x16x32_bf16 v[98:101], v[170:173], v[198:201], v[98:101]
	v_mfma_f32_16x16x32_bf16 v[86:89], v[150:153], v[214:217], v[86:89]
	v_mfma_f32_16x16x32_bf16 v[82:85], v[170:173], v[214:217], v[82:85]
	s_setprio 0
	s_barrier
	s_add_i32 s88, s88, s14
	v_lshl_add_u64 v[202:203], s[68:69], 0, v[166:167]
	s_mov_b32 m0, s88
	ds_read_b128 v[174:177], v208 offset:16384
	ds_read_b128 v[182:185], v208 offset:17408
	ds_read_b128 v[186:189], v208 offset:18432
	ds_read_b128 v[190:193], v208 offset:19456
	ds_read_b128 v[194:197], v208 offset:20480
	ds_read_b128 v[198:201], v208 offset:21504
	ds_read_b128 v[210:213], v208 offset:22528
	ds_read_b128 v[214:217], v208 offset:23552
	global_load_lds_dwordx4 v[202:203], off
	s_add_i32 m0, s88, 0x2000
	s_add_u32 s90, s68, 0x40000
	v_lshl_add_u64 v[218:219], s[68:69], 0, v[158:159]
	s_addc_u32 s91, s69, 0
	s_add_i32 s88, s92, s14
	global_load_lds_dwordx4 v[218:219], off
	v_lshl_add_u64 v[220:221], s[90:91], 0, v[166:167]
	s_mov_b32 m0, s88
	v_lshl_add_u64 v[222:223], s[70:71], 0, v[162:163]
	global_load_lds_dwordx4 v[220:221], off
	v_lshl_add_u64 v[220:221], s[90:91], 0, v[158:159]
	s_add_i32 m0, s88, 0x2000
	s_nop 0
	global_load_lds_dwordx4 v[220:221], off
	v_lshl_add_u64 v[220:221], s[70:71], 0, v[160:161]
	s_mov_b32 m0, s15
	s_nop 0
	global_load_lds_dwordx4 v[220:221], off
	s_mov_b32 m0, s16
	s_nop 0
	global_load_lds_dwordx4 v[222:223], off
	s_waitcnt vmcnt(8)
	s_waitcnt lgkmcnt(0)
	s_barrier
	s_setprio 1
	v_mfma_f32_16x16x32_bf16 v[70:73], v[58:61], v[174:177], 0
	v_mfma_f32_16x16x32_bf16 v[66:69], v[74:77], v[174:177], 0
	v_mfma_f32_16x16x32_bf16 v[46:49], v[58:61], v[186:189], 0
	v_mfma_f32_16x16x32_bf16 v[42:45], v[74:77], v[186:189], 0
	v_mfma_f32_16x16x32_bf16 v[30:33], v[58:61], v[194:197], 0
	v_mfma_f32_16x16x32_bf16 v[26:29], v[74:77], v[194:197], 0
	v_mfma_f32_16x16x32_bf16 v[14:17], v[58:61], v[210:213], 0
	v_mfma_f32_16x16x32_bf16 v[10:13], v[74:77], v[210:213], 0
	v_mfma_f32_16x16x32_bf16 v[70:73], v[62:65], v[182:185], v[70:73]
	v_mfma_f32_16x16x32_bf16 v[66:69], v[78:81], v[182:185], v[66:69]
	v_mfma_f32_16x16x32_bf16 v[46:49], v[62:65], v[190:193], v[46:49]
	v_mfma_f32_16x16x32_bf16 v[42:45], v[78:81], v[190:193], v[42:45]
	v_mfma_f32_16x16x32_bf16 v[30:33], v[62:65], v[198:201], v[30:33]
	v_mfma_f32_16x16x32_bf16 v[26:29], v[78:81], v[198:201], v[26:29]
	v_mfma_f32_16x16x32_bf16 v[14:17], v[62:65], v[214:217], v[14:17]
	v_mfma_f32_16x16x32_bf16 v[10:13], v[78:81], v[214:217], v[10:13]
	s_setprio 0
	s_setprio 1
	v_mfma_f32_16x16x32_bf16 v[54:57], v[146:149], v[174:177], 0
	v_mfma_f32_16x16x32_bf16 v[50:53], v[154:157], v[174:177], 0
	v_mfma_f32_16x16x32_bf16 v[38:41], v[146:149], v[186:189], 0
	v_mfma_f32_16x16x32_bf16 v[34:37], v[154:157], v[186:189], 0
	v_mfma_f32_16x16x32_bf16 v[22:25], v[146:149], v[194:197], 0
	v_mfma_f32_16x16x32_bf16 v[18:21], v[154:157], v[194:197], 0
	v_mfma_f32_16x16x32_bf16 v[6:9], v[146:149], v[210:213], 0
	v_mfma_f32_16x16x32_bf16 v[2:5], v[154:157], v[210:213], 0
	v_mfma_f32_16x16x32_bf16 v[54:57], v[150:153], v[182:185], v[54:57]
	v_mfma_f32_16x16x32_bf16 v[50:53], v[170:173], v[182:185], v[50:53]
	v_mfma_f32_16x16x32_bf16 v[38:41], v[150:153], v[190:193], v[38:41]
	v_mfma_f32_16x16x32_bf16 v[34:37], v[170:173], v[190:193], v[34:37]
	v_mfma_f32_16x16x32_bf16 v[22:25], v[150:153], v[198:201], v[22:25]
	v_mfma_f32_16x16x32_bf16 v[18:21], v[170:173], v[198:201], v[18:21]
	v_mfma_f32_16x16x32_bf16 v[6:9], v[150:153], v[214:217], v[6:9]
	v_mfma_f32_16x16x32_bf16 v[2:5], v[170:173], v[214:217], v[2:5]
	s_setprio 0
	s_barrier
	s_add_i32 s88, 0, 0x18000
	s_add_i32 s90, 0, 0x1c000
	v_add_u32_e32 v78, s88, v204
	v_add_u32_e32 v170, s90, v204
	ds_read_b128 v[58:61], v78
	ds_read_b128 v[62:65], v78 offset:1024
	ds_read_b128 v[74:77], v78 offset:2048
	ds_read_b128 v[78:81], v78 offset:3072
	ds_read_b128 v[146:149], v170
	ds_read_b128 v[150:153], v170 offset:1024
	ds_read_b128 v[154:157], v170 offset:2048
	ds_read_b128 v[170:173], v170 offset:3072
	s_add_u32 s70, s70, 0x40000
	s_addc_u32 s71, s71, 0
	s_mov_b32 m0, s20
	v_lshl_add_u64 v[232:233], s[70:71], 0, v[160:161]
	ds_read_b128 v[174:177], v208 offset:32768
	ds_read_b128 v[182:185], v208 offset:33792
	ds_read_b128 v[186:189], v208 offset:34816
	ds_read_b128 v[190:193], v208 offset:35840
	ds_read_b128 v[194:197], v208 offset:36864
	ds_read_b128 v[198:201], v208 offset:37888
	ds_read_b128 v[210:213], v208 offset:38912
	ds_read_b128 v[214:217], v208 offset:39936
	global_load_lds_dwordx4 v[232:233], off
	v_lshl_add_u64 v[232:233], s[70:71], 0, v[162:163]
	s_mov_b32 m0, s21
	s_nop 0
	global_load_lds_dwordx4 v[232:233], off
	s_waitcnt vmcnt(8)
	s_waitcnt lgkmcnt(0)
	s_barrier
	s_setprio 1
	v_mfma_f32_16x16x32_bf16 v[142:145], v[58:61], v[174:177], v[142:145]
	v_mfma_f32_16x16x32_bf16 v[138:141], v[74:77], v[174:177], v[138:141]
	v_mfma_f32_16x16x32_bf16 v[126:129], v[58:61], v[186:189], v[126:129]
	v_mfma_f32_16x16x32_bf16 v[122:125], v[74:77], v[186:189], v[122:125]
	v_mfma_f32_16x16x32_bf16 v[110:113], v[58:61], v[194:197], v[110:113]
	v_mfma_f32_16x16x32_bf16 v[106:109], v[74:77], v[194:197], v[106:109]
	v_mfma_f32_16x16x32_bf16 v[94:97], v[58:61], v[210:213], v[94:97]
	v_mfma_f32_16x16x32_bf16 v[90:93], v[74:77], v[210:213], v[90:93]
	v_mfma_f32_16x16x32_bf16 v[142:145], v[62:65], v[182:185], v[142:145]
	v_mfma_f32_16x16x32_bf16 v[138:141], v[78:81], v[182:185], v[138:141]
	v_mfma_f32_16x16x32_bf16 v[126:129], v[62:65], v[190:193], v[126:129]
	v_mfma_f32_16x16x32_bf16 v[122:125], v[78:81], v[190:193], v[122:125]
	v_mfma_f32_16x16x32_bf16 v[110:113], v[62:65], v[198:201], v[110:113]
	v_mfma_f32_16x16x32_bf16 v[106:109], v[78:81], v[198:201], v[106:109]
	v_mfma_f32_16x16x32_bf16 v[94:97], v[62:65], v[214:217], v[94:97]
	v_mfma_f32_16x16x32_bf16 v[90:93], v[78:81], v[214:217], v[90:93]
	s_setprio 0
	s_setprio 1
	v_mfma_f32_16x16x32_bf16 v[134:137], v[146:149], v[174:177], v[134:137]
	v_mfma_f32_16x16x32_bf16 v[130:133], v[154:157], v[174:177], v[130:133]
	v_mfma_f32_16x16x32_bf16 v[118:121], v[146:149], v[186:189], v[118:121]
	v_mfma_f32_16x16x32_bf16 v[114:117], v[154:157], v[186:189], v[114:117]
	v_mfma_f32_16x16x32_bf16 v[102:105], v[146:149], v[194:197], v[102:105]
	v_mfma_f32_16x16x32_bf16 v[98:101], v[154:157], v[194:197], v[98:101]
	v_mfma_f32_16x16x32_bf16 v[86:89], v[146:149], v[210:213], v[86:89]
	v_mfma_f32_16x16x32_bf16 v[82:85], v[154:157], v[210:213], v[82:85]
	v_mfma_f32_16x16x32_bf16 v[134:137], v[150:153], v[182:185], v[134:137]
	v_mfma_f32_16x16x32_bf16 v[130:133], v[170:173], v[182:185], v[130:133]
	v_mfma_f32_16x16x32_bf16 v[118:121], v[150:153], v[190:193], v[118:121]
	v_mfma_f32_16x16x32_bf16 v[114:117], v[170:173], v[190:193], v[114:117]
	v_mfma_f32_16x16x32_bf16 v[102:105], v[150:153], v[198:201], v[102:105]
	v_mfma_f32_16x16x32_bf16 v[98:101], v[170:173], v[198:201], v[98:101]
	v_mfma_f32_16x16x32_bf16 v[86:89], v[150:153], v[214:217], v[86:89]
	v_mfma_f32_16x16x32_bf16 v[82:85], v[170:173], v[214:217], v[82:85]
	s_setprio 0
	s_barrier
	s_add_i32 s70, s88, s14
	v_lshl_add_u64 v[202:203], v[202:203], 0, s[56:57]
	s_mov_b32 m0, s70
	ds_read_b128 v[174:177], v208 offset:49152
	ds_read_b128 v[182:185], v208 offset:50176
	ds_read_b128 v[186:189], v208 offset:51200
	ds_read_b128 v[190:193], v208 offset:52224
	ds_read_b128 v[194:197], v208 offset:53248
	ds_read_b128 v[198:201], v208 offset:54272
	ds_read_b128 v[210:213], v208 offset:55296
	ds_read_b128 v[214:217], v208 offset:56320
	global_load_lds_dwordx4 v[202:203], off
	s_add_i32 m0, s70, 0x2000
	s_add_u32 s68, s68, 0x40080
	v_lshl_add_u64 v[202:203], v[218:219], 0, s[56:57]
	s_addc_u32 s69, s69, 0
	s_add_i32 s70, s90, s14
	global_load_lds_dwordx4 v[202:203], off
	v_lshl_add_u64 v[202:203], s[68:69], 0, v[166:167]
	s_mov_b32 m0, s70
	s_nop 0
	global_load_lds_dwordx4 v[202:203], off
	v_lshl_add_u64 v[202:203], s[68:69], 0, v[158:159]
	s_add_i32 m0, s70, 0x2000
	s_nop 0
	global_load_lds_dwordx4 v[202:203], off
	v_lshl_add_u64 v[202:203], v[220:221], 0, s[56:57]
	s_mov_b32 m0, s24
	s_nop 0
	global_load_lds_dwordx4 v[202:203], off
	v_lshl_add_u64 v[202:203], v[222:223], 0, s[56:57]
	s_mov_b32 m0, s25
	s_nop 0
	global_load_lds_dwordx4 v[202:203], off
	s_waitcnt vmcnt(8)
	s_waitcnt lgkmcnt(0)
	s_barrier
	s_setprio 1
	v_mfma_f32_16x16x32_bf16 v[70:73], v[58:61], v[174:177], v[70:73]
	v_mfma_f32_16x16x32_bf16 v[66:69], v[74:77], v[174:177], v[66:69]
	v_mfma_f32_16x16x32_bf16 v[46:49], v[58:61], v[186:189], v[46:49]
	v_mfma_f32_16x16x32_bf16 v[42:45], v[74:77], v[186:189], v[42:45]
	v_mfma_f32_16x16x32_bf16 v[30:33], v[58:61], v[194:197], v[30:33]
	v_mfma_f32_16x16x32_bf16 v[26:29], v[74:77], v[194:197], v[26:29]
	v_mfma_f32_16x16x32_bf16 v[14:17], v[58:61], v[210:213], v[14:17]
	v_mfma_f32_16x16x32_bf16 v[10:13], v[74:77], v[210:213], v[10:13]
	v_mfma_f32_16x16x32_bf16 v[70:73], v[62:65], v[182:185], v[70:73]
	v_mfma_f32_16x16x32_bf16 v[66:69], v[78:81], v[182:185], v[66:69]
	v_mfma_f32_16x16x32_bf16 v[46:49], v[62:65], v[190:193], v[46:49]
	v_mfma_f32_16x16x32_bf16 v[42:45], v[78:81], v[190:193], v[42:45]
	v_mfma_f32_16x16x32_bf16 v[30:33], v[62:65], v[198:201], v[30:33]
	v_mfma_f32_16x16x32_bf16 v[26:29], v[78:81], v[198:201], v[26:29]
	v_mfma_f32_16x16x32_bf16 v[14:17], v[62:65], v[214:217], v[14:17]
	v_mfma_f32_16x16x32_bf16 v[10:13], v[78:81], v[214:217], v[10:13]
	s_setprio 0
	s_setprio 1
	v_mfma_f32_16x16x32_bf16 v[54:57], v[146:149], v[174:177], v[54:57]
	v_mfma_f32_16x16x32_bf16 v[50:53], v[154:157], v[174:177], v[50:53]
	v_mfma_f32_16x16x32_bf16 v[38:41], v[146:149], v[186:189], v[38:41]
	v_mfma_f32_16x16x32_bf16 v[34:37], v[154:157], v[186:189], v[34:37]
	v_mfma_f32_16x16x32_bf16 v[22:25], v[146:149], v[194:197], v[22:25]
	v_mfma_f32_16x16x32_bf16 v[18:21], v[154:157], v[194:197], v[18:21]
	v_mfma_f32_16x16x32_bf16 v[6:9], v[146:149], v[210:213], v[6:9]
	v_mfma_f32_16x16x32_bf16 v[2:5], v[154:157], v[210:213], v[2:5]
	v_mfma_f32_16x16x32_bf16 v[54:57], v[150:153], v[182:185], v[54:57]
	v_mfma_f32_16x16x32_bf16 v[50:53], v[170:173], v[182:185], v[50:53]
	v_mfma_f32_16x16x32_bf16 v[38:41], v[150:153], v[190:193], v[38:41]
	v_mfma_f32_16x16x32_bf16 v[34:37], v[170:173], v[190:193], v[34:37]
	v_mfma_f32_16x16x32_bf16 v[22:25], v[150:153], v[198:201], v[22:25]
	v_mfma_f32_16x16x32_bf16 v[18:21], v[170:173], v[198:201], v[18:21]
	v_mfma_f32_16x16x32_bf16 v[6:9], v[150:153], v[214:217], v[6:9]
	v_mfma_f32_16x16x32_bf16 v[2:5], v[170:173], v[214:217], v[2:5]
	s_setprio 0
	s_barrier
	s_add_u32 s77, s77, 0x100
	s_addc_u32 s79, s79, 0
	s_add_u32 s74, s74, 0x100
	s_addc_u32 s75, s75, 0
	s_cmp_ge_i32 s84, s1
	s_mov_b32 s68, s84
	s_cbranch_scc0 .LBB0_664
	s_branch .Lpeelexitph6
	.p2align	6

.Lpeelph7b_0:
	s_add_i32 s69, s58, 2
	s_add_u32 s59, s54, 0xfffc0080
	s_addc_u32 s60, s55, -1
	s_add_i32 s70, 0, 0x10000
	s_cmp_eq_u32 s53, s58
	s_cselect_b32 s61, s43, s60
	s_cselect_b32 s60, s45, s59
	v_add_u32_e32 v146, s70, v151
	s_cselect_b32 s59, s64, s68
	s_cselect_b32 s58, s65, s66
	s_add_i32 s72, 0, 0x14000
	ds_read_b128 v[142:145], v146
	ds_read_b128 v[156:159], v146 offset:1024
	ds_read_b128 v[160:163], v146 offset:2048
	ds_read_b128 v[170:173], v146 offset:3072
	v_add_u32_e32 v146, s72, v151
	ds_read_b128 v[174:177], v146
	ds_read_b128 v[178:181], v146 offset:1024
	ds_read_b128 v[182:185], v146 offset:2048
	ds_read_b128 v[186:189], v146 offset:3072
	v_lshl_add_u64 v[146:147], s[54:55], 0, v[140:141]
	s_add_i32 m0, s16, 0xc000
	ds_read_b128 v[190:193], v154
	ds_read_b128 v[194:197], v154 offset:1024
	ds_read_b128 v[198:201], v154 offset:2048
	ds_read_b128 v[202:205], v154 offset:3072
	ds_read_b128 v[206:209], v154 offset:4096
	ds_read_b128 v[210:213], v154 offset:5120
	ds_read_b128 v[214:217], v154 offset:6144
	ds_read_b128 v[218:221], v154 offset:7168
	global_load_lds_dwordx4 v[146:147], off
	v_lshl_add_u64 v[146:147], s[54:55], 0, v[138:139]
	s_add_i32 m0, s16, 0xe000
	s_nop 0
	global_load_lds_dwordx4 v[146:147], off
	s_waitcnt vmcnt(8)
	s_waitcnt lgkmcnt(0)
	s_barrier
	s_setprio 1
	v_mfma_f32_16x16x32_bf16 v[126:129], v[142:145], v[190:193], 0
	v_mfma_f32_16x16x32_bf16 v[118:121], v[160:163], v[190:193], 0
	v_mfma_f32_16x16x32_bf16 v[110:113], v[142:145], v[198:201], 0
	v_mfma_f32_16x16x32_bf16 v[102:105], v[160:163], v[198:201], 0
	v_mfma_f32_16x16x32_bf16 v[94:97], v[142:145], v[206:209], 0
	v_mfma_f32_16x16x32_bf16 v[86:89], v[160:163], v[206:209], 0
	v_mfma_f32_16x16x32_bf16 v[78:81], v[142:145], v[214:217], 0
	v_mfma_f32_16x16x32_bf16 v[70:73], v[160:163], v[214:217], 0
	v_mfma_f32_16x16x32_bf16 v[126:129], v[156:159], v[194:197], v[126:129]
	v_mfma_f32_16x16x32_bf16 v[118:121], v[170:173], v[194:197], v[118:121]
	v_mfma_f32_16x16x32_bf16 v[110:113], v[156:159], v[202:205], v[110:113]
	v_mfma_f32_16x16x32_bf16 v[102:105], v[170:173], v[202:205], v[102:105]
	v_mfma_f32_16x16x32_bf16 v[94:97], v[156:159], v[210:213], v[94:97]
	v_mfma_f32_16x16x32_bf16 v[86:89], v[170:173], v[210:213], v[86:89]
	v_mfma_f32_16x16x32_bf16 v[78:81], v[156:159], v[218:221], v[78:81]
	v_mfma_f32_16x16x32_bf16 v[70:73], v[170:173], v[218:221], v[70:73]
	s_setprio 0
	s_setprio 1
	v_mfma_f32_16x16x32_bf16 v[122:125], v[174:177], v[190:193], 0
	v_mfma_f32_16x16x32_bf16 v[114:117], v[182:185], v[190:193], 0
	v_mfma_f32_16x16x32_bf16 v[106:109], v[174:177], v[198:201], 0
	v_mfma_f32_16x16x32_bf16 v[98:101], v[182:185], v[198:201], 0
	v_mfma_f32_16x16x32_bf16 v[90:93], v[174:177], v[206:209], 0
	v_mfma_f32_16x16x32_bf16 v[82:85], v[182:185], v[206:209], 0
	v_mfma_f32_16x16x32_bf16 v[74:77], v[174:177], v[214:217], 0
	v_mfma_f32_16x16x32_bf16 v[66:69], v[182:185], v[214:217], 0
	v_mfma_f32_16x16x32_bf16 v[122:125], v[178:181], v[194:197], v[122:125]
	v_mfma_f32_16x16x32_bf16 v[114:117], v[186:189], v[194:197], v[114:117]
	v_mfma_f32_16x16x32_bf16 v[106:109], v[178:181], v[202:205], v[106:109]
	v_mfma_f32_16x16x32_bf16 v[98:101], v[186:189], v[202:205], v[98:101]
	v_mfma_f32_16x16x32_bf16 v[90:93], v[178:181], v[210:213], v[90:93]
	v_mfma_f32_16x16x32_bf16 v[82:85], v[186:189], v[210:213], v[82:85]
	v_mfma_f32_16x16x32_bf16 v[74:77], v[178:181], v[218:221], v[74:77]
	v_mfma_f32_16x16x32_bf16 v[66:69], v[186:189], v[218:221], v[66:69]
	s_setprio 0
	s_barrier
	s_add_i32 s70, s70, s14
	v_lshl_add_u64 v[146:147], s[58:59], 0, v[166:167]
	s_mov_b32 m0, s70
	ds_read_b128 v[190:193], v154 offset:16384
	ds_read_b128 v[194:197], v154 offset:17408
	ds_read_b128 v[198:201], v154 offset:18432
	ds_read_b128 v[202:205], v154 offset:19456
	ds_read_b128 v[206:209], v154 offset:20480
	ds_read_b128 v[210:213], v154 offset:21504
	ds_read_b128 v[214:217], v154 offset:22528
	ds_read_b128 v[218:221], v154 offset:23552
	global_load_lds_dwordx4 v[146:147], off
	s_add_i32 m0, s70, 0x2000
	s_add_u32 s70, s58, 0x40000
	v_lshl_add_u64 v[164:165], s[58:59], 0, v[134:135]
	s_addc_u32 s71, s59, 0
	s_add_i32 s72, s72, s14
	global_load_lds_dwordx4 v[164:165], off
	v_lshl_add_u64 v[222:223], s[70:71], 0, v[166:167]
	s_mov_b32 m0, s72
	v_lshl_add_u64 v[232:233], s[60:61], 0, v[130:131]
	global_load_lds_dwordx4 v[222:223], off
	v_lshl_add_u64 v[222:223], s[70:71], 0, v[134:135]
	s_add_i32 m0, s72, 0x2000
	s_nop 0
	global_load_lds_dwordx4 v[222:223], off
	v_lshl_add_u64 v[222:223], s[60:61], 0, v[132:133]
	s_mov_b32 m0, s16
	s_nop 0
	global_load_lds_dwordx4 v[222:223], off
	s_mov_b32 m0, s20
	s_nop 0
	global_load_lds_dwordx4 v[232:233], off
	s_waitcnt vmcnt(8)
	s_waitcnt lgkmcnt(0)
	s_barrier
	s_setprio 1
	v_mfma_f32_16x16x32_bf16 v[62:65], v[142:145], v[190:193], 0
	v_mfma_f32_16x16x32_bf16 v[54:57], v[160:163], v[190:193], 0
	v_mfma_f32_16x16x32_bf16 v[46:49], v[142:145], v[198:201], 0
	v_mfma_f32_16x16x32_bf16 v[38:41], v[160:163], v[198:201], 0
	v_mfma_f32_16x16x32_bf16 v[30:33], v[142:145], v[206:209], 0
	v_mfma_f32_16x16x32_bf16 v[22:25], v[160:163], v[206:209], 0
	v_mfma_f32_16x16x32_bf16 v[14:17], v[142:145], v[214:217], 0
	v_mfma_f32_16x16x32_bf16 v[6:9], v[160:163], v[214:217], 0
	v_mfma_f32_16x16x32_bf16 v[62:65], v[156:159], v[194:197], v[62:65]
	v_mfma_f32_16x16x32_bf16 v[54:57], v[170:173], v[194:197], v[54:57]
	v_mfma_f32_16x16x32_bf16 v[46:49], v[156:159], v[202:205], v[46:49]
	v_mfma_f32_16x16x32_bf16 v[38:41], v[170:173], v[202:205], v[38:41]
	v_mfma_f32_16x16x32_bf16 v[30:33], v[156:159], v[210:213], v[30:33]
	v_mfma_f32_16x16x32_bf16 v[22:25], v[170:173], v[210:213], v[22:25]
	v_mfma_f32_16x16x32_bf16 v[14:17], v[156:159], v[218:221], v[14:17]
	v_mfma_f32_16x16x32_bf16 v[6:9], v[170:173], v[218:221], v[6:9]
	s_setprio 0
	s_setprio 1
	v_mfma_f32_16x16x32_bf16 v[58:61], v[174:177], v[190:193], 0
	v_mfma_f32_16x16x32_bf16 v[50:53], v[182:185], v[190:193], 0
	v_mfma_f32_16x16x32_bf16 v[42:45], v[174:177], v[198:201], 0
	v_mfma_f32_16x16x32_bf16 v[34:37], v[182:185], v[198:201], 0
	v_mfma_f32_16x16x32_bf16 v[26:29], v[174:177], v[206:209], 0
	v_mfma_f32_16x16x32_bf16 v[18:21], v[182:185], v[206:209], 0
	v_mfma_f32_16x16x32_bf16 v[10:13], v[174:177], v[214:217], 0
	v_mfma_f32_16x16x32_bf16 v[2:5], v[182:185], v[214:217], 0
	v_mfma_f32_16x16x32_bf16 v[58:61], v[178:181], v[194:197], v[58:61]
	v_mfma_f32_16x16x32_bf16 v[50:53], v[186:189], v[194:197], v[50:53]
	v_mfma_f32_16x16x32_bf16 v[42:45], v[178:181], v[202:205], v[42:45]
	v_mfma_f32_16x16x32_bf16 v[34:37], v[186:189], v[202:205], v[34:37]
	v_mfma_f32_16x16x32_bf16 v[26:29], v[178:181], v[210:213], v[26:29]
	v_mfma_f32_16x16x32_bf16 v[18:21], v[186:189], v[210:213], v[18:21]
	v_mfma_f32_16x16x32_bf16 v[10:13], v[178:181], v[218:221], v[10:13]
	v_mfma_f32_16x16x32_bf16 v[2:5], v[186:189], v[218:221], v[2:5]
	s_setprio 0
	s_barrier
	s_add_i32 s70, 0, 0x18000
	v_add_u32_e32 v148, s70, v151
	s_add_i32 s71, 0, 0x1c000
	ds_read_b128 v[142:145], v148
	ds_read_b128 v[156:159], v148 offset:1024
	ds_read_b128 v[160:163], v148 offset:2048
	ds_read_b128 v[170:173], v148 offset:3072
	v_add_u32_e32 v148, s71, v151
	ds_read_b128 v[174:177], v148
	ds_read_b128 v[178:181], v148 offset:1024
	ds_read_b128 v[182:185], v148 offset:2048
	ds_read_b128 v[186:189], v148 offset:3072
	s_add_u32 s60, s60, 0x40000
	s_addc_u32 s61, s61, 0
	s_mov_b32 m0, s21
	v_lshl_add_u64 v[234:235], s[60:61], 0, v[132:133]
	ds_read_b128 v[190:193], v154 offset:32768
	ds_read_b128 v[194:197], v154 offset:33792
	ds_read_b128 v[198:201], v154 offset:34816
	ds_read_b128 v[202:205], v154 offset:35840
	ds_read_b128 v[206:209], v154 offset:36864
	ds_read_b128 v[210:213], v154 offset:37888
	ds_read_b128 v[214:217], v154 offset:38912
	ds_read_b128 v[218:221], v154 offset:39936
	global_load_lds_dwordx4 v[234:235], off
	v_lshl_add_u64 v[234:235], s[60:61], 0, v[130:131]
	s_mov_b32 m0, s22
	s_nop 0
	global_load_lds_dwordx4 v[234:235], off
	s_waitcnt vmcnt(8)
	s_waitcnt lgkmcnt(0)
	s_barrier
	s_setprio 1
	v_mfma_f32_16x16x32_bf16 v[126:129], v[142:145], v[190:193], v[126:129]
	v_mfma_f32_16x16x32_bf16 v[118:121], v[160:163], v[190:193], v[118:121]
	v_mfma_f32_16x16x32_bf16 v[110:113], v[142:145], v[198:201], v[110:113]
	v_mfma_f32_16x16x32_bf16 v[102:105], v[160:163], v[198:201], v[102:105]
	v_mfma_f32_16x16x32_bf16 v[94:97], v[142:145], v[206:209], v[94:97]
	v_mfma_f32_16x16x32_bf16 v[86:89], v[160:163], v[206:209], v[86:89]
	v_mfma_f32_16x16x32_bf16 v[78:81], v[142:145], v[214:217], v[78:81]
	v_mfma_f32_16x16x32_bf16 v[70:73], v[160:163], v[214:217], v[70:73]
	v_mfma_f32_16x16x32_bf16 v[126:129], v[156:159], v[194:197], v[126:129]
	v_mfma_f32_16x16x32_bf16 v[118:121], v[170:173], v[194:197], v[118:121]
	v_mfma_f32_16x16x32_bf16 v[110:113], v[156:159], v[202:205], v[110:113]
	v_mfma_f32_16x16x32_bf16 v[102:105], v[170:173], v[202:205], v[102:105]
	v_mfma_f32_16x16x32_bf16 v[94:97], v[156:159], v[210:213], v[94:97]
	v_mfma_f32_16x16x32_bf16 v[86:89], v[170:173], v[210:213], v[86:89]
	v_mfma_f32_16x16x32_bf16 v[78:81], v[156:159], v[218:221], v[78:81]
	v_mfma_f32_16x16x32_bf16 v[70:73], v[170:173], v[218:221], v[70:73]
	s_setprio 0
	s_setprio 1
	v_mfma_f32_16x16x32_bf16 v[122:125], v[174:177], v[190:193], v[122:125]
	v_mfma_f32_16x16x32_bf16 v[114:117], v[182:185], v[190:193], v[114:117]
	v_mfma_f32_16x16x32_bf16 v[106:109], v[174:177], v[198:201], v[106:109]
	v_mfma_f32_16x16x32_bf16 v[98:101], v[182:185], v[198:201], v[98:101]
	v_mfma_f32_16x16x32_bf16 v[90:93], v[174:177], v[206:209], v[90:93]
	v_mfma_f32_16x16x32_bf16 v[82:85], v[182:185], v[206:209], v[82:85]
	v_mfma_f32_16x16x32_bf16 v[74:77], v[174:177], v[214:217], v[74:77]
	v_mfma_f32_16x16x32_bf16 v[66:69], v[182:185], v[214:217], v[66:69]
	v_mfma_f32_16x16x32_bf16 v[122:125], v[178:181], v[194:197], v[122:125]
	v_mfma_f32_16x16x32_bf16 v[114:117], v[186:189], v[194:197], v[114:117]
	v_mfma_f32_16x16x32_bf16 v[106:109], v[178:181], v[202:205], v[106:109]
	v_mfma_f32_16x16x32_bf16 v[98:101], v[186:189], v[202:205], v[98:101]
	v_mfma_f32_16x16x32_bf16 v[90:93], v[178:181], v[210:213], v[90:93]
	v_mfma_f32_16x16x32_bf16 v[82:85], v[186:189], v[210:213], v[82:85]
	v_mfma_f32_16x16x32_bf16 v[74:77], v[178:181], v[218:221], v[74:77]
	v_mfma_f32_16x16x32_bf16 v[66:69], v[186:189], v[218:221], v[66:69]
	s_setprio 0
	s_barrier
	s_add_i32 s60, s70, s14
	v_lshl_add_u64 v[146:147], v[146:147], 0, s[56:57]
	s_mov_b32 m0, s60
	ds_read_b128 v[190:193], v154 offset:49152
	ds_read_b128 v[194:197], v154 offset:50176
	ds_read_b128 v[198:201], v154 offset:51200
	ds_read_b128 v[202:205], v154 offset:52224
	ds_read_b128 v[206:209], v154 offset:53248
	ds_read_b128 v[210:213], v154 offset:54272
	ds_read_b128 v[214:217], v154 offset:55296
	ds_read_b128 v[218:221], v154 offset:56320
	global_load_lds_dwordx4 v[146:147], off
	s_add_i32 m0, s60, 0x2000
	s_add_u32 s58, s58, 0x40080
	v_lshl_add_u64 v[146:147], v[164:165], 0, s[56:57]
	s_addc_u32 s59, s59, 0
	s_add_i32 s60, s71, s14
	global_load_lds_dwordx4 v[146:147], off
	v_lshl_add_u64 v[146:147], s[58:59], 0, v[166:167]
	s_mov_b32 m0, s60
	s_nop 0
	global_load_lds_dwordx4 v[146:147], off
	v_lshl_add_u64 v[146:147], s[58:59], 0, v[134:135]
	s_add_i32 m0, s60, 0x2000
	s_nop 0
	global_load_lds_dwordx4 v[146:147], off
	v_lshl_add_u64 v[146:147], v[222:223], 0, s[56:57]
	s_mov_b32 m0, s23
	s_nop 0
	global_load_lds_dwordx4 v[146:147], off
	v_lshl_add_u64 v[146:147], v[232:233], 0, s[56:57]
	s_mov_b32 m0, s24
	s_nop 0
	global_load_lds_dwordx4 v[146:147], off
	s_waitcnt vmcnt(8)
	s_waitcnt lgkmcnt(0)
	s_barrier
	s_setprio 1
	v_mfma_f32_16x16x32_bf16 v[62:65], v[142:145], v[190:193], v[62:65]
	v_mfma_f32_16x16x32_bf16 v[54:57], v[160:163], v[190:193], v[54:57]
	v_mfma_f32_16x16x32_bf16 v[46:49], v[142:145], v[198:201], v[46:49]
	v_mfma_f32_16x16x32_bf16 v[38:41], v[160:163], v[198:201], v[38:41]
	v_mfma_f32_16x16x32_bf16 v[30:33], v[142:145], v[206:209], v[30:33]
	v_mfma_f32_16x16x32_bf16 v[22:25], v[160:163], v[206:209], v[22:25]
	v_mfma_f32_16x16x32_bf16 v[14:17], v[142:145], v[214:217], v[14:17]
	v_mfma_f32_16x16x32_bf16 v[6:9], v[160:163], v[214:217], v[6:9]
	v_mfma_f32_16x16x32_bf16 v[62:65], v[156:159], v[194:197], v[62:65]
	v_mfma_f32_16x16x32_bf16 v[54:57], v[170:173], v[194:197], v[54:57]
	v_mfma_f32_16x16x32_bf16 v[46:49], v[156:159], v[202:205], v[46:49]
	v_mfma_f32_16x16x32_bf16 v[38:41], v[170:173], v[202:205], v[38:41]
	v_mfma_f32_16x16x32_bf16 v[30:33], v[156:159], v[210:213], v[30:33]
	v_mfma_f32_16x16x32_bf16 v[22:25], v[170:173], v[210:213], v[22:25]
	v_mfma_f32_16x16x32_bf16 v[14:17], v[156:159], v[218:221], v[14:17]
	v_mfma_f32_16x16x32_bf16 v[6:9], v[170:173], v[218:221], v[6:9]
	s_setprio 0
	s_setprio 1
	v_mfma_f32_16x16x32_bf16 v[58:61], v[174:177], v[190:193], v[58:61]
	v_mfma_f32_16x16x32_bf16 v[50:53], v[182:185], v[190:193], v[50:53]
	v_mfma_f32_16x16x32_bf16 v[42:45], v[174:177], v[198:201], v[42:45]
	v_mfma_f32_16x16x32_bf16 v[34:37], v[182:185], v[198:201], v[34:37]
	v_mfma_f32_16x16x32_bf16 v[26:29], v[174:177], v[206:209], v[26:29]
	v_mfma_f32_16x16x32_bf16 v[18:21], v[182:185], v[206:209], v[18:21]
	v_mfma_f32_16x16x32_bf16 v[10:13], v[174:177], v[214:217], v[10:13]
	v_mfma_f32_16x16x32_bf16 v[2:5], v[182:185], v[214:217], v[2:5]
	v_mfma_f32_16x16x32_bf16 v[58:61], v[178:181], v[194:197], v[58:61]
	v_mfma_f32_16x16x32_bf16 v[50:53], v[186:189], v[194:197], v[50:53]
	v_mfma_f32_16x16x32_bf16 v[42:45], v[178:181], v[202:205], v[42:45]
	v_mfma_f32_16x16x32_bf16 v[34:37], v[186:189], v[202:205], v[34:37]
	v_mfma_f32_16x16x32_bf16 v[26:29], v[178:181], v[210:213], v[26:29]
	v_mfma_f32_16x16x32_bf16 v[18:21], v[186:189], v[210:213], v[18:21]
	v_mfma_f32_16x16x32_bf16 v[10:13], v[178:181], v[218:221], v[10:13]
	v_mfma_f32_16x16x32_bf16 v[2:5], v[186:189], v[218:221], v[2:5]
	s_setprio 0
	s_barrier
	s_add_u32 s66, s66, 0x100
	s_addc_u32 s68, s68, 0
	s_add_u32 s54, s54, 0x100
	s_addc_u32 s55, s55, 0
	s_cmp_ge_i32 s69, s13
	s_mov_b32 s58, s69
	s_cbranch_scc0 .LBB0_817
	s_branch .Lpeelexitph7b
	.p2align	6

.Lpeelph7f_0:
	s_add_i32 s66, s54, 2
	s_add_u32 s55, s52, 0xfffe0080
	s_addc_u32 s58, s53, -1
	s_add_i32 s68, 0, 0x10000
	s_cmp_eq_u32 s51, s54
	s_cselect_b32 s59, s41, s58
	s_cselect_b32 s58, s43, s55
	s_cselect_b32 s55, s62, s65
	s_cselect_b32 s54, s63, s64
	s_add_i32 s69, 0, 0x14000
	v_add_u32_e32 v2, s68, v196
	v_add_u32_e32 v6, s69, v196
	ds_read_b128 v[26:29], v2
	ds_read_b128 v[30:33], v2 offset:1024
	ds_read_b128 v[18:21], v2 offset:2048
	ds_read_b128 v[22:25], v2 offset:3072
	ds_read_b128 v[10:13], v6
	ds_read_b128 v[14:17], v6 offset:1024
	ds_read_b128 v[2:5], v6 offset:2048
	ds_read_b128 v[6:9], v6 offset:3072
	v_lshl_add_u64 v[170:171], s[52:53], 0, v[184:185]
	s_add_i32 m0, s16, 0xc000
	ds_read_b128 v[186:189], v198
	ds_read_b128 v[190:193], v198 offset:1024
	ds_read_b128 v[200:203], v198 offset:2048
	ds_read_b128 v[204:207], v198 offset:3072
	ds_read_b128 v[208:211], v198 offset:4096
	ds_read_b128 v[212:215], v198 offset:5120
	ds_read_b128 v[216:219], v198 offset:6144
	ds_read_b128 v[220:223], v198 offset:7168
	global_load_lds_dwordx4 v[170:171], off
	v_lshl_add_u64 v[170:171], s[52:53], 0, v[182:183]
	s_add_i32 m0, s16, 0xe000
	s_nop 0
	global_load_lds_dwordx4 v[170:171], off
	s_waitcnt vmcnt(8)
	s_waitcnt lgkmcnt(0)
	s_barrier
	s_setprio 1
	v_mfma_scale_f32_16x16x128_f8f6f4 v[158:161], v[26:33], v[186:193], 0, v194, v169 op_sel_hi:[0,0,0]
	v_mfma_scale_f32_16x16x128_f8f6f4 v[150:153], v[18:25], v[186:193], 0, v194, v169 op_sel_hi:[0,0,0]
	v_mfma_scale_f32_16x16x128_f8f6f4 v[142:145], v[26:33], v[200:207], 0, v194, v169 op_sel_hi:[0,0,0]
	v_mfma_scale_f32_16x16x128_f8f6f4 v[134:137], v[18:25], v[200:207], 0, v194, v169 op_sel_hi:[0,0,0]
	v_mfma_scale_f32_16x16x128_f8f6f4 v[126:129], v[26:33], v[208:215], 0, v194, v169 op_sel_hi:[0,0,0]
	v_mfma_scale_f32_16x16x128_f8f6f4 v[118:121], v[18:25], v[208:215], 0, v194, v169 op_sel_hi:[0,0,0]
	v_mfma_scale_f32_16x16x128_f8f6f4 v[110:113], v[26:33], v[216:223], 0, v194, v169 op_sel_hi:[0,0,0]
	v_mfma_scale_f32_16x16x128_f8f6f4 v[102:105], v[18:25], v[216:223], 0, v194, v169 op_sel_hi:[0,0,0]
	s_setprio 0
	s_setprio 1
	v_mfma_scale_f32_16x16x128_f8f6f4 v[154:157], v[10:17], v[186:193], 0, v194, v169 op_sel_hi:[0,0,0]
	v_mfma_scale_f32_16x16x128_f8f6f4 v[146:149], v[2:9], v[186:193], 0, v194, v169 op_sel_hi:[0,0,0]
	v_mfma_scale_f32_16x16x128_f8f6f4 v[138:141], v[10:17], v[200:207], 0, v194, v169 op_sel_hi:[0,0,0]
	v_mfma_scale_f32_16x16x128_f8f6f4 v[130:133], v[2:9], v[200:207], 0, v194, v169 op_sel_hi:[0,0,0]
	v_mfma_scale_f32_16x16x128_f8f6f4 v[122:125], v[10:17], v[208:215], 0, v194, v169 op_sel_hi:[0,0,0]
	v_mfma_scale_f32_16x16x128_f8f6f4 v[114:117], v[2:9], v[208:215], 0, v194, v169 op_sel_hi:[0,0,0]
	v_mfma_scale_f32_16x16x128_f8f6f4 v[106:109], v[10:17], v[216:223], 0, v194, v169 op_sel_hi:[0,0,0]
	v_mfma_scale_f32_16x16x128_f8f6f4 v[98:101], v[2:9], v[216:223], 0, v194, v169 op_sel_hi:[0,0,0]
	s_setprio 0
	s_barrier
	s_add_i32 s68, s68, s14
	v_lshl_add_u64 v[186:187], s[54:55], 0, v[166:167]
	s_mov_b32 m0, s68
	ds_read_b128 v[200:203], v198 offset:16384
	ds_read_b128 v[204:207], v198 offset:17408
	ds_read_b128 v[208:211], v198 offset:18432
	ds_read_b128 v[212:215], v198 offset:19456
	ds_read_b128 v[216:219], v198 offset:20480
	ds_read_b128 v[220:223], v198 offset:21504
	ds_read_b128 v[236:239], v198 offset:22528
	ds_read_b128 v[240:243], v198 offset:23552
	global_load_lds_dwordx4 v[186:187], off
	s_add_i32 m0, s68, 0x2000
	s_add_u32 s70, s54, 0x20000
	v_lshl_add_u64 v[188:189], s[54:55], 0, v[178:179]
	s_addc_u32 s71, s55, 0
	s_add_i32 s68, s69, s14
	global_load_lds_dwordx4 v[188:189], off
	v_lshl_add_u64 v[170:171], s[70:71], 0, v[166:167]
	s_mov_b32 m0, s68
	v_lshl_add_u64 v[190:191], s[58:59], 0, v[164:165]
	global_load_lds_dwordx4 v[170:171], off
	v_lshl_add_u64 v[170:171], s[70:71], 0, v[178:179]
	s_add_i32 m0, s68, 0x2000
	v_lshl_add_u64 v[192:193], s[58:59], 0, v[162:163]
	global_load_lds_dwordx4 v[170:171], off
	s_mov_b32 m0, s16
	s_nop 0
	global_load_lds_dwordx4 v[190:191], off
	s_mov_b32 m0, s20
	s_nop 0
	global_load_lds_dwordx4 v[192:193], off
	s_waitcnt vmcnt(8)
	s_waitcnt lgkmcnt(0)
	s_barrier
	s_setprio 1
	v_mfma_scale_f32_16x16x128_f8f6f4 v[94:97], v[26:33], v[200:207], 0, v194, v169 op_sel_hi:[0,0,0]
	v_mfma_scale_f32_16x16x128_f8f6f4 v[86:89], v[18:25], v[200:207], 0, v194, v169 op_sel_hi:[0,0,0]
	v_mfma_scale_f32_16x16x128_f8f6f4 v[78:81], v[26:33], v[208:215], 0, v194, v169 op_sel_hi:[0,0,0]
	v_mfma_scale_f32_16x16x128_f8f6f4 v[70:73], v[18:25], v[208:215], 0, v194, v169 op_sel_hi:[0,0,0]
	v_mfma_scale_f32_16x16x128_f8f6f4 v[62:65], v[26:33], v[216:223], 0, v194, v169 op_sel_hi:[0,0,0]
	v_mfma_scale_f32_16x16x128_f8f6f4 v[54:57], v[18:25], v[216:223], 0, v194, v169 op_sel_hi:[0,0,0]
	v_mfma_scale_f32_16x16x128_f8f6f4 v[46:49], v[26:33], v[236:243], 0, v194, v169 op_sel_hi:[0,0,0]
	v_mfma_scale_f32_16x16x128_f8f6f4 v[38:41], v[18:25], v[236:243], 0, v194, v169 op_sel_hi:[0,0,0]
	s_setprio 0
	s_setprio 1
	v_mfma_scale_f32_16x16x128_f8f6f4 v[90:93], v[10:17], v[200:207], 0, v194, v169 op_sel_hi:[0,0,0]
	v_mfma_scale_f32_16x16x128_f8f6f4 v[82:85], v[2:9], v[200:207], 0, v194, v169 op_sel_hi:[0,0,0]
	v_mfma_scale_f32_16x16x128_f8f6f4 v[74:77], v[10:17], v[208:215], 0, v194, v169 op_sel_hi:[0,0,0]
	v_mfma_scale_f32_16x16x128_f8f6f4 v[66:69], v[2:9], v[208:215], 0, v194, v169 op_sel_hi:[0,0,0]
	v_mfma_scale_f32_16x16x128_f8f6f4 v[58:61], v[10:17], v[216:223], 0, v194, v169 op_sel_hi:[0,0,0]
	v_mfma_scale_f32_16x16x128_f8f6f4 v[50:53], v[2:9], v[216:223], 0, v194, v169 op_sel_hi:[0,0,0]
	v_mfma_scale_f32_16x16x128_f8f6f4 v[42:45], v[10:17], v[236:243], 0, v194, v169 op_sel_hi:[0,0,0]
	v_mfma_scale_f32_16x16x128_f8f6f4 v[34:37], v[2:9], v[236:243], 0, v194, v169 op_sel_hi:[0,0,0]
	s_setprio 0
	s_barrier
	s_add_i32 s68, 0, 0x18000
	s_add_i32 s69, 0, 0x1c000
	v_add_u32_e32 v2, s68, v196
	v_add_u32_e32 v6, s69, v196
	ds_read_b128 v[26:29], v2
	ds_read_b128 v[30:33], v2 offset:1024
	ds_read_b128 v[18:21], v2 offset:2048
	ds_read_b128 v[22:25], v2 offset:3072
	ds_read_b128 v[10:13], v6
	ds_read_b128 v[14:17], v6 offset:1024
	ds_read_b128 v[2:5], v6 offset:2048
	ds_read_b128 v[6:9], v6 offset:3072
	s_add_u32 s58, s58, 0x20000
	s_addc_u32 s59, s59, 0
	s_mov_b32 m0, s21
	v_lshl_add_u64 v[170:171], s[58:59], 0, v[164:165]
	ds_read_b128 v[200:203], v198 offset:32768
	ds_read_b128 v[204:207], v198 offset:33792
	ds_read_b128 v[208:211], v198 offset:34816
	ds_read_b128 v[212:215], v198 offset:35840
	ds_read_b128 v[216:219], v198 offset:36864
	ds_read_b128 v[220:223], v198 offset:37888
	ds_read_b128 v[236:239], v198 offset:38912
	ds_read_b128 v[240:243], v198 offset:39936
	global_load_lds_dwordx4 v[170:171], off
	v_lshl_add_u64 v[170:171], s[58:59], 0, v[162:163]
	s_mov_b32 m0, s22
	s_nop 0
	global_load_lds_dwordx4 v[170:171], off
	s_waitcnt vmcnt(8)
	s_waitcnt lgkmcnt(0)
	s_barrier
	s_setprio 1
	v_mfma_scale_f32_16x16x128_f8f6f4 v[158:161], v[26:33], v[200:207], v[158:161], v194, v169 op_sel_hi:[0,0,0]
	v_mfma_scale_f32_16x16x128_f8f6f4 v[150:153], v[18:25], v[200:207], v[150:153], v194, v169 op_sel_hi:[0,0,0]
	v_mfma_scale_f32_16x16x128_f8f6f4 v[142:145], v[26:33], v[208:215], v[142:145], v194, v169 op_sel_hi:[0,0,0]
	v_mfma_scale_f32_16x16x128_f8f6f4 v[134:137], v[18:25], v[208:215], v[134:137], v194, v169 op_sel_hi:[0,0,0]
	v_mfma_scale_f32_16x16x128_f8f6f4 v[126:129], v[26:33], v[216:223], v[126:129], v194, v169 op_sel_hi:[0,0,0]
	v_mfma_scale_f32_16x16x128_f8f6f4 v[118:121], v[18:25], v[216:223], v[118:121], v194, v169 op_sel_hi:[0,0,0]
	v_mfma_scale_f32_16x16x128_f8f6f4 v[110:113], v[26:33], v[236:243], v[110:113], v194, v169 op_sel_hi:[0,0,0]
	v_mfma_scale_f32_16x16x128_f8f6f4 v[102:105], v[18:25], v[236:243], v[102:105], v194, v169 op_sel_hi:[0,0,0]
	s_setprio 0
	s_setprio 1
	v_mfma_scale_f32_16x16x128_f8f6f4 v[154:157], v[10:17], v[200:207], v[154:157], v194, v169 op_sel_hi:[0,0,0]
	v_mfma_scale_f32_16x16x128_f8f6f4 v[146:149], v[2:9], v[200:207], v[146:149], v194, v169 op_sel_hi:[0,0,0]
	v_mfma_scale_f32_16x16x128_f8f6f4 v[138:141], v[10:17], v[208:215], v[138:141], v194, v169 op_sel_hi:[0,0,0]
	v_mfma_scale_f32_16x16x128_f8f6f4 v[130:133], v[2:9], v[208:215], v[130:133], v194, v169 op_sel_hi:[0,0,0]
	v_mfma_scale_f32_16x16x128_f8f6f4 v[122:125], v[10:17], v[216:223], v[122:125], v194, v169 op_sel_hi:[0,0,0]
	v_mfma_scale_f32_16x16x128_f8f6f4 v[114:117], v[2:9], v[216:223], v[114:117], v194, v169 op_sel_hi:[0,0,0]
	v_mfma_scale_f32_16x16x128_f8f6f4 v[106:109], v[10:17], v[236:243], v[106:109], v194, v169 op_sel_hi:[0,0,0]
	v_mfma_scale_f32_16x16x128_f8f6f4 v[98:101], v[2:9], v[236:243], v[98:101], v194, v169 op_sel_hi:[0,0,0]
	s_setprio 0
	s_barrier
	s_add_i32 s58, s68, s14
	v_lshl_add_u64 v[170:171], v[186:187], 0, s[56:57]
	s_mov_b32 m0, s58
	ds_read_b128 v[200:203], v198 offset:49152
	ds_read_b128 v[204:207], v198 offset:50176
	ds_read_b128 v[208:211], v198 offset:51200
	ds_read_b128 v[212:215], v198 offset:52224
	ds_read_b128 v[216:219], v198 offset:53248
	ds_read_b128 v[220:223], v198 offset:54272
	ds_read_b128 v[236:239], v198 offset:55296
	ds_read_b128 v[240:243], v198 offset:56320
	global_load_lds_dwordx4 v[170:171], off
	s_add_i32 m0, s58, 0x2000
	s_add_u32 s54, s54, 0x20080
	v_lshl_add_u64 v[170:171], v[188:189], 0, s[56:57]
	s_addc_u32 s55, s55, 0
	s_add_i32 s58, s69, s14
	global_load_lds_dwordx4 v[170:171], off
	v_lshl_add_u64 v[170:171], s[54:55], 0, v[166:167]
	s_mov_b32 m0, s58
	s_nop 0
	global_load_lds_dwordx4 v[170:171], off
	v_lshl_add_u64 v[170:171], s[54:55], 0, v[178:179]
	s_add_i32 m0, s58, 0x2000
	s_nop 0
	global_load_lds_dwordx4 v[170:171], off
	v_lshl_add_u64 v[170:171], v[190:191], 0, s[56:57]
	s_mov_b32 m0, s23
	s_nop 0
	global_load_lds_dwordx4 v[170:171], off
	v_lshl_add_u64 v[170:171], v[192:193], 0, s[56:57]
	s_mov_b32 m0, s24
	s_nop 0
	global_load_lds_dwordx4 v[170:171], off
	s_waitcnt vmcnt(8)
	s_waitcnt lgkmcnt(0)
	s_barrier
	s_setprio 1
	v_mfma_scale_f32_16x16x128_f8f6f4 v[94:97], v[26:33], v[200:207], v[94:97], v194, v169 op_sel_hi:[0,0,0]
	v_mfma_scale_f32_16x16x128_f8f6f4 v[86:89], v[18:25], v[200:207], v[86:89], v194, v169 op_sel_hi:[0,0,0]
	v_mfma_scale_f32_16x16x128_f8f6f4 v[78:81], v[26:33], v[208:215], v[78:81], v194, v169 op_sel_hi:[0,0,0]
	v_mfma_scale_f32_16x16x128_f8f6f4 v[70:73], v[18:25], v[208:215], v[70:73], v194, v169 op_sel_hi:[0,0,0]
	v_mfma_scale_f32_16x16x128_f8f6f4 v[62:65], v[26:33], v[216:223], v[62:65], v194, v169 op_sel_hi:[0,0,0]
	v_mfma_scale_f32_16x16x128_f8f6f4 v[54:57], v[18:25], v[216:223], v[54:57], v194, v169 op_sel_hi:[0,0,0]
	v_mfma_scale_f32_16x16x128_f8f6f4 v[46:49], v[26:33], v[236:243], v[46:49], v194, v169 op_sel_hi:[0,0,0]
	v_mfma_scale_f32_16x16x128_f8f6f4 v[38:41], v[18:25], v[236:243], v[38:41], v194, v169 op_sel_hi:[0,0,0]
	s_setprio 0
	s_setprio 1
	v_mfma_scale_f32_16x16x128_f8f6f4 v[90:93], v[10:17], v[200:207], v[90:93], v194, v169 op_sel_hi:[0,0,0]
	v_mfma_scale_f32_16x16x128_f8f6f4 v[82:85], v[2:9], v[200:207], v[82:85], v194, v169 op_sel_hi:[0,0,0]
	v_mfma_scale_f32_16x16x128_f8f6f4 v[74:77], v[10:17], v[208:215], v[74:77], v194, v169 op_sel_hi:[0,0,0]
	v_mfma_scale_f32_16x16x128_f8f6f4 v[66:69], v[2:9], v[208:215], v[66:69], v194, v169 op_sel_hi:[0,0,0]
	v_mfma_scale_f32_16x16x128_f8f6f4 v[58:61], v[10:17], v[216:223], v[58:61], v194, v169 op_sel_hi:[0,0,0]
	v_mfma_scale_f32_16x16x128_f8f6f4 v[50:53], v[2:9], v[216:223], v[50:53], v194, v169 op_sel_hi:[0,0,0]
	v_mfma_scale_f32_16x16x128_f8f6f4 v[42:45], v[10:17], v[236:243], v[42:45], v194, v169 op_sel_hi:[0,0,0]
	v_mfma_scale_f32_16x16x128_f8f6f4 v[34:37], v[2:9], v[236:243], v[34:37], v194, v169 op_sel_hi:[0,0,0]
	s_setprio 0
	s_barrier
	s_add_u32 s64, s64, 0x100
	s_addc_u32 s65, s65, 0
	s_add_u32 s52, s52, 0x100
	s_addc_u32 s53, s53, 0
	s_cmp_ge_i32 s66, s13
	s_mov_b32 s54, s66
	s_cbranch_scc0 .LBB0_842
	s_branch .Lpeelexitph7f
	.p2align	6

.Lpeelph8_0:
	s_add_i32 s75, s62, 2
	s_add_u32 s60, s58, 0x100
	s_addc_u32 s61, s59, 0
	s_add_i32 s76, 0, 0x10000
	s_cmp_eq_u32 s68, s62
	s_cselect_b32 s65, s53, s61
	s_cselect_b32 s64, s52, s60
	s_cselect_b32 s63, s55, s74
	s_cselect_b32 s62, s54, s73
	s_add_i32 s77, 0, 0x14000
	v_add_u32_e32 v2, s76, v200
	v_add_u32_e32 v6, s77, v200
	ds_read_b128 v[26:29], v2
	ds_read_b128 v[30:33], v2 offset:1024
	ds_read_b128 v[18:21], v2 offset:2048
	ds_read_b128 v[22:25], v2 offset:3072
	ds_read_b128 v[10:13], v6
	ds_read_b128 v[14:17], v6 offset:1024
	s_waitcnt lgkmcnt(0)
	ds_read_b128 v[2:5], v6 offset:2048
	ds_read_b128 v[6:9], v6 offset:3072
	v_lshl_add_u64 v[170:171], s[58:59], 0, v[184:185]
	s_add_i32 m0, s15, 0xc000
	ds_read_b128 v[186:189], v204
	ds_read_b128 v[190:193], v204 offset:1024
	ds_read_b128 v[206:209], v204 offset:2048
	ds_read_b128 v[210:213], v204 offset:3072
	ds_read_b128 v[214:217], v204 offset:4096
	ds_read_b128 v[218:221], v204 offset:5120
	ds_read_b128 v[236:239], v204 offset:6144
	ds_read_b128 v[240:243], v204 offset:7168
	global_load_lds_dwordx4 v[170:171], off
	v_lshl_add_u64 v[170:171], s[58:59], 0, v[182:183]
	s_add_i32 m0, s15, 0xe000
	s_nop 0
	global_load_lds_dwordx4 v[170:171], off
	s_waitcnt vmcnt(8)
	s_waitcnt lgkmcnt(0)
	s_barrier
	s_setprio 1
	v_mfma_scale_f32_16x16x128_f8f6f4 v[158:161], v[26:33], v[186:193], 0, v198, v169 op_sel_hi:[0,0,0]
	v_mfma_scale_f32_16x16x128_f8f6f4 v[154:157], v[18:25], v[186:193], 0, v198, v169 op_sel_hi:[0,0,0]
	v_mfma_scale_f32_16x16x128_f8f6f4 v[142:145], v[26:33], v[206:213], 0, v198, v169 op_sel_hi:[0,0,0]
	v_mfma_scale_f32_16x16x128_f8f6f4 v[138:141], v[18:25], v[206:213], 0, v198, v169 op_sel_hi:[0,0,0]
	v_mfma_scale_f32_16x16x128_f8f6f4 v[126:129], v[26:33], v[214:221], 0, v198, v169 op_sel_hi:[0,0,0]
	v_mfma_scale_f32_16x16x128_f8f6f4 v[122:125], v[18:25], v[214:221], 0, v198, v169 op_sel_hi:[0,0,0]
	v_mfma_scale_f32_16x16x128_f8f6f4 v[110:113], v[26:33], v[236:243], 0, v198, v169 op_sel_hi:[0,0,0]
	v_mfma_scale_f32_16x16x128_f8f6f4 v[106:109], v[18:25], v[236:243], 0, v198, v169 op_sel_hi:[0,0,0]
	s_setprio 0
	s_setprio 1
	v_mfma_scale_f32_16x16x128_f8f6f4 v[150:153], v[10:17], v[186:193], 0, v198, v169 op_sel_hi:[0,0,0]
	v_mfma_scale_f32_16x16x128_f8f6f4 v[146:149], v[2:9], v[186:193], 0, v198, v169 op_sel_hi:[0,0,0]
	v_mfma_scale_f32_16x16x128_f8f6f4 v[134:137], v[10:17], v[206:213], 0, v198, v169 op_sel_hi:[0,0,0]
	v_mfma_scale_f32_16x16x128_f8f6f4 v[130:133], v[2:9], v[206:213], 0, v198, v169 op_sel_hi:[0,0,0]
	v_mfma_scale_f32_16x16x128_f8f6f4 v[118:121], v[10:17], v[214:221], 0, v198, v169 op_sel_hi:[0,0,0]
	v_mfma_scale_f32_16x16x128_f8f6f4 v[114:117], v[2:9], v[214:221], 0, v198, v169 op_sel_hi:[0,0,0]
	v_mfma_scale_f32_16x16x128_f8f6f4 v[102:105], v[10:17], v[236:243], 0, v198, v169 op_sel_hi:[0,0,0]
	v_mfma_scale_f32_16x16x128_f8f6f4 v[98:101], v[2:9], v[236:243], 0, v198, v169 op_sel_hi:[0,0,0]
	s_setprio 0
	s_barrier
	s_add_i32 s58, s76, s14
	v_lshl_add_u64 v[186:187], s[62:63], 0, v[166:167]
	s_mov_b32 m0, s58
	ds_read_b128 v[206:209], v204 offset:16384
	ds_read_b128 v[210:213], v204 offset:17408
	ds_read_b128 v[214:217], v204 offset:18432
	ds_read_b128 v[218:221], v204 offset:19456
	ds_read_b128 v[236:239], v204 offset:20480
	ds_read_b128 v[240:243], v204 offset:21504
	ds_read_b128 v[244:247], v204 offset:22528
	ds_read_b128 v[248:251], v204 offset:23552
	global_load_lds_dwordx4 v[186:187], off
	s_add_i32 m0, s58, 0x2000
	s_add_u32 s58, s62, 0x70000
	v_lshl_add_u64 v[188:189], s[62:63], 0, v[162:163]
	s_addc_u32 s59, s63, 0
	s_add_i32 s76, s77, s14
	global_load_lds_dwordx4 v[188:189], off
	v_lshl_add_u64 v[170:171], s[58:59], 0, v[166:167]
	s_mov_b32 m0, s76
	v_lshl_add_u64 v[190:191], s[64:65], 0, v[164:165]
	global_load_lds_dwordx4 v[170:171], off
	v_lshl_add_u64 v[170:171], s[58:59], 0, v[162:163]
	s_add_i32 m0, s76, 0x2000
	v_lshl_add_u64 v[192:193], s[64:65], 0, v[178:179]
	global_load_lds_dwordx4 v[170:171], off
	s_mov_b32 m0, s15
	s_nop 0
	global_load_lds_dwordx4 v[190:191], off
	s_mov_b32 m0, s16
	s_nop 0
	global_load_lds_dwordx4 v[192:193], off
	s_waitcnt vmcnt(8)
	s_waitcnt lgkmcnt(0)
	s_barrier
	s_setprio 1
	v_mfma_scale_f32_16x16x128_f8f6f4 v[94:97], v[26:33], v[206:213], 0, v198, v169 op_sel_hi:[0,0,0]
	v_mfma_scale_f32_16x16x128_f8f6f4 v[90:93], v[18:25], v[206:213], 0, v198, v169 op_sel_hi:[0,0,0]
	v_mfma_scale_f32_16x16x128_f8f6f4 v[78:81], v[26:33], v[214:221], 0, v198, v169 op_sel_hi:[0,0,0]
	v_mfma_scale_f32_16x16x128_f8f6f4 v[74:77], v[18:25], v[214:221], 0, v198, v169 op_sel_hi:[0,0,0]
	v_mfma_scale_f32_16x16x128_f8f6f4 v[62:65], v[26:33], v[236:243], 0, v198, v169 op_sel_hi:[0,0,0]
	v_mfma_scale_f32_16x16x128_f8f6f4 v[58:61], v[18:25], v[236:243], 0, v198, v169 op_sel_hi:[0,0,0]
	v_mfma_scale_f32_16x16x128_f8f6f4 v[46:49], v[26:33], v[244:251], 0, v198, v169 op_sel_hi:[0,0,0]
	v_mfma_scale_f32_16x16x128_f8f6f4 v[42:45], v[18:25], v[244:251], 0, v198, v169 op_sel_hi:[0,0,0]
	s_setprio 0
	s_setprio 1
	v_mfma_scale_f32_16x16x128_f8f6f4 v[86:89], v[10:17], v[206:213], 0, v198, v169 op_sel_hi:[0,0,0]
	v_mfma_scale_f32_16x16x128_f8f6f4 v[82:85], v[2:9], v[206:213], 0, v198, v169 op_sel_hi:[0,0,0]
	v_mfma_scale_f32_16x16x128_f8f6f4 v[70:73], v[10:17], v[214:221], 0, v198, v169 op_sel_hi:[0,0,0]
	v_mfma_scale_f32_16x16x128_f8f6f4 v[66:69], v[2:9], v[214:221], 0, v198, v169 op_sel_hi:[0,0,0]
	v_mfma_scale_f32_16x16x128_f8f6f4 v[54:57], v[10:17], v[236:243], 0, v198, v169 op_sel_hi:[0,0,0]
	v_mfma_scale_f32_16x16x128_f8f6f4 v[50:53], v[2:9], v[236:243], 0, v198, v169 op_sel_hi:[0,0,0]
	v_mfma_scale_f32_16x16x128_f8f6f4 v[38:41], v[10:17], v[244:251], 0, v198, v169 op_sel_hi:[0,0,0]
	v_mfma_scale_f32_16x16x128_f8f6f4 v[34:37], v[2:9], v[244:251], 0, v198, v169 op_sel_hi:[0,0,0]
	s_setprio 0
	s_barrier
	s_add_i32 s76, 0, 0x18000
	s_add_i32 s77, 0, 0x1c000
	v_add_u32_e32 v2, s76, v200
	v_add_u32_e32 v6, s77, v200
	ds_read_b128 v[26:29], v2
	ds_read_b128 v[30:33], v2 offset:1024
	ds_read_b128 v[18:21], v2 offset:2048
	ds_read_b128 v[22:25], v2 offset:3072
	ds_read_b128 v[10:13], v6
	ds_read_b128 v[14:17], v6 offset:1024
	ds_read_b128 v[2:5], v6 offset:2048
	ds_read_b128 v[6:9], v6 offset:3072
	s_add_u32 s58, s64, 0x70000
	s_addc_u32 s59, s65, 0
	s_mov_b32 m0, s20
	v_lshl_add_u64 v[170:171], s[58:59], 0, v[164:165]
	ds_read_b128 v[206:209], v204 offset:32768
	ds_read_b128 v[210:213], v204 offset:33792
	ds_read_b128 v[214:217], v204 offset:34816
	ds_read_b128 v[218:221], v204 offset:35840
	ds_read_b128 v[236:239], v204 offset:36864
	ds_read_b128 v[240:243], v204 offset:37888
	ds_read_b128 v[244:247], v204 offset:38912
	ds_read_b128 v[248:251], v204 offset:39936
	global_load_lds_dwordx4 v[170:171], off
	v_lshl_add_u64 v[170:171], s[58:59], 0, v[178:179]
	s_mov_b32 m0, s21
	s_nop 0
	global_load_lds_dwordx4 v[170:171], off
	s_waitcnt vmcnt(8)
	s_waitcnt lgkmcnt(0)
	s_barrier
	s_setprio 1
	v_mfma_scale_f32_16x16x128_f8f6f4 v[158:161], v[26:33], v[206:213], v[158:161], v198, v169 op_sel_hi:[0,0,0]
	v_mfma_scale_f32_16x16x128_f8f6f4 v[154:157], v[18:25], v[206:213], v[154:157], v198, v169 op_sel_hi:[0,0,0]
	v_mfma_scale_f32_16x16x128_f8f6f4 v[142:145], v[26:33], v[214:221], v[142:145], v198, v169 op_sel_hi:[0,0,0]
	v_mfma_scale_f32_16x16x128_f8f6f4 v[138:141], v[18:25], v[214:221], v[138:141], v198, v169 op_sel_hi:[0,0,0]
	v_mfma_scale_f32_16x16x128_f8f6f4 v[126:129], v[26:33], v[236:243], v[126:129], v198, v169 op_sel_hi:[0,0,0]
	v_mfma_scale_f32_16x16x128_f8f6f4 v[122:125], v[18:25], v[236:243], v[122:125], v198, v169 op_sel_hi:[0,0,0]
	v_mfma_scale_f32_16x16x128_f8f6f4 v[110:113], v[26:33], v[244:251], v[110:113], v198, v169 op_sel_hi:[0,0,0]
	v_mfma_scale_f32_16x16x128_f8f6f4 v[106:109], v[18:25], v[244:251], v[106:109], v198, v169 op_sel_hi:[0,0,0]
	s_setprio 0
	s_setprio 1
	v_mfma_scale_f32_16x16x128_f8f6f4 v[150:153], v[10:17], v[206:213], v[150:153], v198, v169 op_sel_hi:[0,0,0]
	v_mfma_scale_f32_16x16x128_f8f6f4 v[146:149], v[2:9], v[206:213], v[146:149], v198, v169 op_sel_hi:[0,0,0]
	v_mfma_scale_f32_16x16x128_f8f6f4 v[134:137], v[10:17], v[214:221], v[134:137], v198, v169 op_sel_hi:[0,0,0]
	v_mfma_scale_f32_16x16x128_f8f6f4 v[130:133], v[2:9], v[214:221], v[130:133], v198, v169 op_sel_hi:[0,0,0]
	v_mfma_scale_f32_16x16x128_f8f6f4 v[118:121], v[10:17], v[236:243], v[118:121], v198, v169 op_sel_hi:[0,0,0]
	v_mfma_scale_f32_16x16x128_f8f6f4 v[114:117], v[2:9], v[236:243], v[114:117], v198, v169 op_sel_hi:[0,0,0]
	v_mfma_scale_f32_16x16x128_f8f6f4 v[102:105], v[10:17], v[244:251], v[102:105], v198, v169 op_sel_hi:[0,0,0]
	v_mfma_scale_f32_16x16x128_f8f6f4 v[98:101], v[2:9], v[244:251], v[98:101], v198, v169 op_sel_hi:[0,0,0]
	s_setprio 0
	s_barrier
	s_add_i32 s58, s76, s14
	v_lshl_add_u64 v[170:171], v[186:187], 0, s[56:57]
	s_mov_b32 m0, s58
	ds_read_b128 v[206:209], v204 offset:49152
	ds_read_b128 v[210:213], v204 offset:50176
	ds_read_b128 v[214:217], v204 offset:51200
	ds_read_b128 v[218:221], v204 offset:52224
	ds_read_b128 v[236:239], v204 offset:53248
	ds_read_b128 v[240:243], v204 offset:54272
	ds_read_b128 v[244:247], v204 offset:55296
	ds_read_b128 v[248:251], v204 offset:56320
	global_load_lds_dwordx4 v[170:171], off
	s_add_i32 m0, s58, 0x2000
	s_add_u32 s58, s62, 0x70080
	v_lshl_add_u64 v[170:171], v[188:189], 0, s[56:57]
	s_addc_u32 s59, s63, 0
	s_add_i32 s62, s77, s14
	global_load_lds_dwordx4 v[170:171], off
	v_lshl_add_u64 v[170:171], s[58:59], 0, v[166:167]
	s_mov_b32 m0, s62
	s_nop 0
	global_load_lds_dwordx4 v[170:171], off
	v_lshl_add_u64 v[170:171], s[58:59], 0, v[162:163]
	s_add_i32 m0, s62, 0x2000
	s_nop 0
	global_load_lds_dwordx4 v[170:171], off
	v_lshl_add_u64 v[170:171], v[190:191], 0, s[56:57]
	s_mov_b32 m0, s24
	s_nop 0
	global_load_lds_dwordx4 v[170:171], off
	v_lshl_add_u64 v[170:171], v[192:193], 0, s[56:57]
	s_mov_b32 m0, s25
	s_nop 0
	global_load_lds_dwordx4 v[170:171], off
	s_waitcnt vmcnt(8)
	s_waitcnt lgkmcnt(0)
	s_barrier
	s_setprio 1
	v_mfma_scale_f32_16x16x128_f8f6f4 v[94:97], v[26:33], v[206:213], v[94:97], v198, v169 op_sel_hi:[0,0,0]
	v_mfma_scale_f32_16x16x128_f8f6f4 v[90:93], v[18:25], v[206:213], v[90:93], v198, v169 op_sel_hi:[0,0,0]
	v_mfma_scale_f32_16x16x128_f8f6f4 v[78:81], v[26:33], v[214:221], v[78:81], v198, v169 op_sel_hi:[0,0,0]
	v_mfma_scale_f32_16x16x128_f8f6f4 v[74:77], v[18:25], v[214:221], v[74:77], v198, v169 op_sel_hi:[0,0,0]
	v_mfma_scale_f32_16x16x128_f8f6f4 v[62:65], v[26:33], v[236:243], v[62:65], v198, v169 op_sel_hi:[0,0,0]
	v_mfma_scale_f32_16x16x128_f8f6f4 v[58:61], v[18:25], v[236:243], v[58:61], v198, v169 op_sel_hi:[0,0,0]
	v_mfma_scale_f32_16x16x128_f8f6f4 v[46:49], v[26:33], v[244:251], v[46:49], v198, v169 op_sel_hi:[0,0,0]
	v_mfma_scale_f32_16x16x128_f8f6f4 v[42:45], v[18:25], v[244:251], v[42:45], v198, v169 op_sel_hi:[0,0,0]
	s_setprio 0
	s_setprio 1
	v_mfma_scale_f32_16x16x128_f8f6f4 v[86:89], v[10:17], v[206:213], v[86:89], v198, v169 op_sel_hi:[0,0,0]
	v_mfma_scale_f32_16x16x128_f8f6f4 v[82:85], v[2:9], v[206:213], v[82:85], v198, v169 op_sel_hi:[0,0,0]
	v_mfma_scale_f32_16x16x128_f8f6f4 v[70:73], v[10:17], v[214:221], v[70:73], v198, v169 op_sel_hi:[0,0,0]
	v_mfma_scale_f32_16x16x128_f8f6f4 v[66:69], v[2:9], v[214:221], v[66:69], v198, v169 op_sel_hi:[0,0,0]
	v_mfma_scale_f32_16x16x128_f8f6f4 v[54:57], v[10:17], v[236:243], v[54:57], v198, v169 op_sel_hi:[0,0,0]
	v_mfma_scale_f32_16x16x128_f8f6f4 v[50:53], v[2:9], v[236:243], v[50:53], v198, v169 op_sel_hi:[0,0,0]
	v_mfma_scale_f32_16x16x128_f8f6f4 v[38:41], v[10:17], v[244:251], v[38:41], v198, v169 op_sel_hi:[0,0,0]
	v_mfma_scale_f32_16x16x128_f8f6f4 v[34:37], v[2:9], v[244:251], v[34:37], v198, v169 op_sel_hi:[0,0,0]
	s_setprio 0
	s_barrier
	s_add_u32 s73, s73, 0x100
	s_addc_u32 s74, s74, 0
	s_cmp_ge_i32 s75, s1
	s_mov_b64 s[58:59], s[60:61]
	s_mov_b32 s62, s75
	s_cbranch_scc0 .LBB0_924
	s_branch .Lpeelexitph8
	.p2align	6

.Lpeelph9_0:
	s_add_i32 s27, s37, 2
	s_add_u32 s40, s38, 0xfffe0080
	s_addc_u32 s41, s39, -1
	s_add_i32 s65, 0, 0x10000
	s_cmp_eq_u32 s95, s37
	s_cselect_b32 s69, s0, s41
	s_cselect_b32 s68, s1, s40
	s_cselect_b32 s41, s8, s19
	s_cselect_b32 s40, s11, s16
	s_add_i32 s37, 0, 0x14000
	v_add_u32_e32 v2, s65, v221
	v_add_u32_e32 v6, s37, v221
	ds_read_b128 v[26:29], v2
	ds_read_b128 v[30:33], v2 offset:1024
	ds_read_b128 v[18:21], v2 offset:2048
	ds_read_b128 v[22:25], v2 offset:3072
	ds_read_b128 v[10:13], v6
	ds_read_b128 v[14:17], v6 offset:1024
	ds_read_b128 v[2:5], v6 offset:2048
	ds_read_b128 v[6:9], v6 offset:3072
	v_lshl_add_u64 v[170:171], s[38:39], 0, v[192:193]
	s_add_i32 m0, s21, 0xc000
	ds_read_b128 v[194:197], v222
	ds_read_b128 v[198:201], v222 offset:1024
	ds_read_b128 v[202:205], v222 offset:2048
	ds_read_b128 v[206:209], v222 offset:3072
	ds_read_b128 v[210:213], v222 offset:4096
	ds_read_b128 v[214:217], v222 offset:5120
	ds_read_b128 v[236:239], v222 offset:6144
	ds_read_b128 v[240:243], v222 offset:7168
	global_load_lds_dwordx4 v[170:171], off
	v_lshl_add_u64 v[170:171], s[38:39], 0, v[190:191]
	s_add_i32 m0, s21, 0xe000
	s_nop 0
	global_load_lds_dwordx4 v[170:171], off
	s_waitcnt vmcnt(8)
	s_waitcnt lgkmcnt(0)
	s_barrier
	s_setprio 1
	v_mfma_scale_f32_16x16x128_f8f6f4 v[94:97], v[26:33], v[194:201], 0, v183, v169 op_sel_hi:[0,0,0]
	v_mfma_scale_f32_16x16x128_f8f6f4 v[90:93], v[18:25], v[194:201], 0, v183, v169 op_sel_hi:[0,0,0]
	v_mfma_scale_f32_16x16x128_f8f6f4 v[86:89], v[26:33], v[202:209], 0, v183, v169 op_sel_hi:[0,0,0]
	v_mfma_scale_f32_16x16x128_f8f6f4 v[82:85], v[18:25], v[202:209], 0, v183, v169 op_sel_hi:[0,0,0]
	v_mfma_scale_f32_16x16x128_f8f6f4 v[78:81], v[26:33], v[210:217], 0, v183, v169 op_sel_hi:[0,0,0]
	v_mfma_scale_f32_16x16x128_f8f6f4 v[74:77], v[18:25], v[210:217], 0, v183, v169 op_sel_hi:[0,0,0]
	v_mfma_scale_f32_16x16x128_f8f6f4 v[70:73], v[26:33], v[236:243], 0, v183, v169 op_sel_hi:[0,0,0]
	v_mfma_scale_f32_16x16x128_f8f6f4 v[66:69], v[18:25], v[236:243], 0, v183, v169 op_sel_hi:[0,0,0]
	s_setprio 0
	s_setprio 1
	v_mfma_scale_f32_16x16x128_f8f6f4 v[158:161], v[10:17], v[194:201], 0, v183, v169 op_sel_hi:[0,0,0]
	v_mfma_scale_f32_16x16x128_f8f6f4 v[154:157], v[2:9], v[194:201], 0, v183, v169 op_sel_hi:[0,0,0]
	v_mfma_scale_f32_16x16x128_f8f6f4 v[150:153], v[10:17], v[202:209], 0, v183, v169 op_sel_hi:[0,0,0]
	v_mfma_scale_f32_16x16x128_f8f6f4 v[146:149], v[2:9], v[202:209], 0, v183, v169 op_sel_hi:[0,0,0]
	v_mfma_scale_f32_16x16x128_f8f6f4 v[142:145], v[10:17], v[210:217], 0, v183, v169 op_sel_hi:[0,0,0]
	v_mfma_scale_f32_16x16x128_f8f6f4 v[138:141], v[2:9], v[210:217], 0, v183, v169 op_sel_hi:[0,0,0]
	v_mfma_scale_f32_16x16x128_f8f6f4 v[134:137], v[10:17], v[236:243], 0, v183, v169 op_sel_hi:[0,0,0]
	v_mfma_scale_f32_16x16x128_f8f6f4 v[130:133], v[2:9], v[236:243], 0, v183, v169 op_sel_hi:[0,0,0]
	s_setprio 0
	s_barrier
	s_add_i32 s65, s65, s20
	v_lshl_add_u64 v[194:195], s[40:41], 0, v[162:163]
	s_mov_b32 m0, s65
	ds_read_b128 v[202:205], v222 offset:16384
	ds_read_b128 v[206:209], v222 offset:17408
	ds_read_b128 v[210:213], v222 offset:18432
	ds_read_b128 v[214:217], v222 offset:19456
	ds_read_b128 v[236:239], v222 offset:20480
	ds_read_b128 v[240:243], v222 offset:21504
	ds_read_b128 v[244:247], v222 offset:22528
	ds_read_b128 v[248:251], v222 offset:23552
	global_load_lds_dwordx4 v[194:195], off
	s_add_i32 m0, s65, 0x2000
	s_add_u32 s70, s40, 0x20000
	v_lshl_add_u64 v[196:197], s[40:41], 0, v[164:165]
	s_addc_u32 s71, s41, 0
	s_add_i32 s37, s37, s20
	global_load_lds_dwordx4 v[196:197], off
	v_lshl_add_u64 v[170:171], s[70:71], 0, v[162:163]
	s_mov_b32 m0, s37
	v_lshl_add_u64 v[198:199], s[68:69], 0, v[178:179]
	global_load_lds_dwordx4 v[170:171], off
	v_lshl_add_u64 v[170:171], s[70:71], 0, v[164:165]
	s_add_i32 m0, s37, 0x2000
	v_lshl_add_u64 v[200:201], s[68:69], 0, v[180:181]
	global_load_lds_dwordx4 v[170:171], off
	s_mov_b32 m0, s21
	s_nop 0
	global_load_lds_dwordx4 v[198:199], off
	s_mov_b32 m0, s22
	s_nop 0
	global_load_lds_dwordx4 v[200:201], off
	s_waitcnt vmcnt(8)
	s_waitcnt lgkmcnt(0)
	s_barrier
	s_setprio 1
	v_mfma_scale_f32_16x16x128_f8f6f4 v[62:65], v[26:33], v[202:209], 0, v183, v169 op_sel_hi:[0,0,0]
	v_mfma_scale_f32_16x16x128_f8f6f4 v[58:61], v[18:25], v[202:209], 0, v183, v169 op_sel_hi:[0,0,0]
	v_mfma_scale_f32_16x16x128_f8f6f4 v[54:57], v[26:33], v[210:217], 0, v183, v169 op_sel_hi:[0,0,0]
	v_mfma_scale_f32_16x16x128_f8f6f4 v[50:53], v[18:25], v[210:217], 0, v183, v169 op_sel_hi:[0,0,0]
	v_mfma_scale_f32_16x16x128_f8f6f4 v[46:49], v[26:33], v[236:243], 0, v183, v169 op_sel_hi:[0,0,0]
	v_mfma_scale_f32_16x16x128_f8f6f4 v[42:45], v[18:25], v[236:243], 0, v183, v169 op_sel_hi:[0,0,0]
	v_mfma_scale_f32_16x16x128_f8f6f4 v[38:41], v[26:33], v[244:251], 0, v183, v169 op_sel_hi:[0,0,0]
	v_mfma_scale_f32_16x16x128_f8f6f4 v[34:37], v[18:25], v[244:251], 0, v183, v169 op_sel_hi:[0,0,0]
	s_setprio 0
	s_setprio 1
	v_mfma_scale_f32_16x16x128_f8f6f4 v[126:129], v[10:17], v[202:209], 0, v183, v169 op_sel_hi:[0,0,0]
	v_mfma_scale_f32_16x16x128_f8f6f4 v[122:125], v[2:9], v[202:209], 0, v183, v169 op_sel_hi:[0,0,0]
	v_mfma_scale_f32_16x16x128_f8f6f4 v[118:121], v[10:17], v[210:217], 0, v183, v169 op_sel_hi:[0,0,0]
	v_mfma_scale_f32_16x16x128_f8f6f4 v[114:117], v[2:9], v[210:217], 0, v183, v169 op_sel_hi:[0,0,0]
	v_mfma_scale_f32_16x16x128_f8f6f4 v[110:113], v[10:17], v[236:243], 0, v183, v169 op_sel_hi:[0,0,0]
	v_mfma_scale_f32_16x16x128_f8f6f4 v[106:109], v[2:9], v[236:243], 0, v183, v169 op_sel_hi:[0,0,0]
	v_mfma_scale_f32_16x16x128_f8f6f4 v[102:105], v[10:17], v[244:251], 0, v183, v169 op_sel_hi:[0,0,0]
	v_mfma_scale_f32_16x16x128_f8f6f4 v[98:101], v[2:9], v[244:251], 0, v183, v169 op_sel_hi:[0,0,0]
	s_setprio 0
	s_barrier
	s_add_i32 s37, 0, 0x18000
	s_add_i32 s65, 0, 0x1c000
	v_add_u32_e32 v2, s37, v221
	v_add_u32_e32 v6, s65, v221
	ds_read_b128 v[26:29], v2
	ds_read_b128 v[30:33], v2 offset:1024
	ds_read_b128 v[18:21], v2 offset:2048
	ds_read_b128 v[22:25], v2 offset:3072
	ds_read_b128 v[10:13], v6
	ds_read_b128 v[14:17], v6 offset:1024
	ds_read_b128 v[2:5], v6 offset:2048
	ds_read_b128 v[6:9], v6 offset:3072
	s_add_u32 s68, s68, 0x20000
	s_addc_u32 s69, s69, 0
	s_mov_b32 m0, s23
	v_lshl_add_u64 v[170:171], s[68:69], 0, v[178:179]
	ds_read_b128 v[202:205], v222 offset:32768
	ds_read_b128 v[206:209], v222 offset:33792
	ds_read_b128 v[210:213], v222 offset:34816
	ds_read_b128 v[214:217], v222 offset:35840
	ds_read_b128 v[236:239], v222 offset:36864
	ds_read_b128 v[240:243], v222 offset:37888
	ds_read_b128 v[244:247], v222 offset:38912
	ds_read_b128 v[248:251], v222 offset:39936
	global_load_lds_dwordx4 v[170:171], off
	v_lshl_add_u64 v[170:171], s[68:69], 0, v[180:181]
	s_mov_b32 m0, s12
	s_nop 0
	global_load_lds_dwordx4 v[170:171], off
	s_waitcnt vmcnt(8)
	s_waitcnt lgkmcnt(0)
	s_barrier
	s_setprio 1
	v_mfma_scale_f32_16x16x128_f8f6f4 v[94:97], v[26:33], v[202:209], v[94:97], v183, v169 op_sel_hi:[0,0,0]
	v_mfma_scale_f32_16x16x128_f8f6f4 v[90:93], v[18:25], v[202:209], v[90:93], v183, v169 op_sel_hi:[0,0,0]
	v_mfma_scale_f32_16x16x128_f8f6f4 v[86:89], v[26:33], v[210:217], v[86:89], v183, v169 op_sel_hi:[0,0,0]
	v_mfma_scale_f32_16x16x128_f8f6f4 v[82:85], v[18:25], v[210:217], v[82:85], v183, v169 op_sel_hi:[0,0,0]
	v_mfma_scale_f32_16x16x128_f8f6f4 v[78:81], v[26:33], v[236:243], v[78:81], v183, v169 op_sel_hi:[0,0,0]
	v_mfma_scale_f32_16x16x128_f8f6f4 v[74:77], v[18:25], v[236:243], v[74:77], v183, v169 op_sel_hi:[0,0,0]
	v_mfma_scale_f32_16x16x128_f8f6f4 v[70:73], v[26:33], v[244:251], v[70:73], v183, v169 op_sel_hi:[0,0,0]
	v_mfma_scale_f32_16x16x128_f8f6f4 v[66:69], v[18:25], v[244:251], v[66:69], v183, v169 op_sel_hi:[0,0,0]
	s_setprio 0
	s_setprio 1
	v_mfma_scale_f32_16x16x128_f8f6f4 v[158:161], v[10:17], v[202:209], v[158:161], v183, v169 op_sel_hi:[0,0,0]
	v_mfma_scale_f32_16x16x128_f8f6f4 v[154:157], v[2:9], v[202:209], v[154:157], v183, v169 op_sel_hi:[0,0,0]
	v_mfma_scale_f32_16x16x128_f8f6f4 v[150:153], v[10:17], v[210:217], v[150:153], v183, v169 op_sel_hi:[0,0,0]
	v_mfma_scale_f32_16x16x128_f8f6f4 v[146:149], v[2:9], v[210:217], v[146:149], v183, v169 op_sel_hi:[0,0,0]
	v_mfma_scale_f32_16x16x128_f8f6f4 v[142:145], v[10:17], v[236:243], v[142:145], v183, v169 op_sel_hi:[0,0,0]
	v_mfma_scale_f32_16x16x128_f8f6f4 v[138:141], v[2:9], v[236:243], v[138:141], v183, v169 op_sel_hi:[0,0,0]
	v_mfma_scale_f32_16x16x128_f8f6f4 v[134:137], v[10:17], v[244:251], v[134:137], v183, v169 op_sel_hi:[0,0,0]
	v_mfma_scale_f32_16x16x128_f8f6f4 v[130:133], v[2:9], v[244:251], v[130:133], v183, v169 op_sel_hi:[0,0,0]
	s_setprio 0
	s_barrier
	s_add_i32 s37, s37, s20
	v_lshl_add_u64 v[170:171], v[194:195], 0, s[56:57]
	s_mov_b32 m0, s37
	ds_read_b128 v[202:205], v222 offset:49152
	ds_read_b128 v[206:209], v222 offset:50176
	ds_read_b128 v[210:213], v222 offset:51200
	ds_read_b128 v[214:217], v222 offset:52224
	ds_read_b128 v[236:239], v222 offset:53248
	ds_read_b128 v[240:243], v222 offset:54272
	ds_read_b128 v[244:247], v222 offset:55296
	ds_read_b128 v[248:251], v222 offset:56320
	global_load_lds_dwordx4 v[170:171], off
	s_add_i32 m0, s37, 0x2000
	s_add_u32 s40, s40, 0x20080
	v_lshl_add_u64 v[170:171], v[196:197], 0, s[56:57]
	s_addc_u32 s41, s41, 0
	s_add_i32 s37, s65, s20
	global_load_lds_dwordx4 v[170:171], off
	v_lshl_add_u64 v[170:171], s[40:41], 0, v[162:163]
	s_mov_b32 m0, s37
	s_nop 0
	global_load_lds_dwordx4 v[170:171], off
	v_lshl_add_u64 v[170:171], s[40:41], 0, v[164:165]
	s_add_i32 m0, s37, 0x2000
	s_nop 0
	global_load_lds_dwordx4 v[170:171], off
	v_lshl_add_u64 v[170:171], v[198:199], 0, s[56:57]
	s_mov_b32 m0, s92
	s_nop 0
	global_load_lds_dwordx4 v[170:171], off
	v_lshl_add_u64 v[170:171], v[200:201], 0, s[56:57]
	s_mov_b32 m0, s93
	s_nop 0
	global_load_lds_dwordx4 v[170:171], off
	s_waitcnt vmcnt(8)
	s_waitcnt lgkmcnt(0)
	s_barrier
	s_setprio 1
	v_mfma_scale_f32_16x16x128_f8f6f4 v[62:65], v[26:33], v[202:209], v[62:65], v183, v169 op_sel_hi:[0,0,0]
	v_mfma_scale_f32_16x16x128_f8f6f4 v[58:61], v[18:25], v[202:209], v[58:61], v183, v169 op_sel_hi:[0,0,0]
	v_mfma_scale_f32_16x16x128_f8f6f4 v[54:57], v[26:33], v[210:217], v[54:57], v183, v169 op_sel_hi:[0,0,0]
	v_mfma_scale_f32_16x16x128_f8f6f4 v[50:53], v[18:25], v[210:217], v[50:53], v183, v169 op_sel_hi:[0,0,0]
	v_mfma_scale_f32_16x16x128_f8f6f4 v[46:49], v[26:33], v[236:243], v[46:49], v183, v169 op_sel_hi:[0,0,0]
	v_mfma_scale_f32_16x16x128_f8f6f4 v[42:45], v[18:25], v[236:243], v[42:45], v183, v169 op_sel_hi:[0,0,0]
	v_mfma_scale_f32_16x16x128_f8f6f4 v[38:41], v[26:33], v[244:251], v[38:41], v183, v169 op_sel_hi:[0,0,0]
	v_mfma_scale_f32_16x16x128_f8f6f4 v[34:37], v[18:25], v[244:251], v[34:37], v183, v169 op_sel_hi:[0,0,0]
	s_setprio 0
	s_setprio 1
	v_mfma_scale_f32_16x16x128_f8f6f4 v[126:129], v[10:17], v[202:209], v[126:129], v183, v169 op_sel_hi:[0,0,0]
	v_mfma_scale_f32_16x16x128_f8f6f4 v[122:125], v[2:9], v[202:209], v[122:125], v183, v169 op_sel_hi:[0,0,0]
	v_mfma_scale_f32_16x16x128_f8f6f4 v[118:121], v[10:17], v[210:217], v[118:121], v183, v169 op_sel_hi:[0,0,0]
	v_mfma_scale_f32_16x16x128_f8f6f4 v[114:117], v[2:9], v[210:217], v[114:117], v183, v169 op_sel_hi:[0,0,0]
	v_mfma_scale_f32_16x16x128_f8f6f4 v[110:113], v[10:17], v[236:243], v[110:113], v183, v169 op_sel_hi:[0,0,0]
	v_mfma_scale_f32_16x16x128_f8f6f4 v[106:109], v[2:9], v[236:243], v[106:109], v183, v169 op_sel_hi:[0,0,0]
	v_mfma_scale_f32_16x16x128_f8f6f4 v[102:105], v[10:17], v[244:251], v[102:105], v183, v169 op_sel_hi:[0,0,0]
	v_mfma_scale_f32_16x16x128_f8f6f4 v[98:101], v[2:9], v[244:251], v[98:101], v183, v169 op_sel_hi:[0,0,0]
	s_setprio 0
	s_barrier
	s_add_u32 s16, s16, 0x100
	s_addc_u32 s19, s19, 0
	s_add_u32 s38, s38, 0x100
	s_addc_u32 s39, s39, 0
	s_cmp_ge_i32 s27, s74
	s_mov_b32 s37, s27
	s_cbranch_scc0 .LBB0_1016
	s_branch .Lpeelexitph9
	.p2align	6

.Lpeelph12_0:
	s_add_i32 s66, s54, 2
	s_add_u32 s55, s52, 0xfffc0080
	s_addc_u32 s58, s53, -1
	s_add_i32 s68, 0, 0x10000
	s_cmp_eq_u32 s60, s54
	s_cselect_b32 s59, s41, s58
	s_cselect_b32 s58, s43, s55
	v_add_u32_e32 v144, s68, v147
	s_cselect_b32 s55, s62, s65
	s_cselect_b32 s54, s63, s64
	s_add_i32 s70, 0, 0x14000
	ds_read_b128 v[140:143], v144
	ds_read_b128 v[150:153], v144 offset:1024
	ds_read_b128 v[154:157], v144 offset:2048
	ds_read_b128 v[158:161], v144 offset:3072
	v_add_u32_e32 v144, s70, v147
	ds_read_b128 v[162:165], v144
	ds_read_b128 v[170:173], v144 offset:1024
	ds_read_b128 v[174:177], v144 offset:2048
	ds_read_b128 v[178:181], v144 offset:3072
	v_lshl_add_u64 v[144:145], s[52:53], 0, v[138:139]
	s_add_i32 m0, s16, 0xc000
	ds_read_b128 v[182:185], v149
	ds_read_b128 v[186:189], v149 offset:1024
	ds_read_b128 v[190:193], v149 offset:2048
	ds_read_b128 v[194:197], v149 offset:3072
	ds_read_b128 v[198:201], v149 offset:4096
	ds_read_b128 v[202:205], v149 offset:5120
	ds_read_b128 v[206:209], v149 offset:6144
	ds_read_b128 v[210:213], v149 offset:7168
	global_load_lds_dwordx4 v[144:145], off
	v_lshl_add_u64 v[144:145], s[52:53], 0, v[136:137]
	s_add_i32 m0, s16, 0xe000
	s_nop 0
	global_load_lds_dwordx4 v[144:145], off
	s_waitcnt vmcnt(8)
	s_waitcnt lgkmcnt(0)
	s_barrier
	s_setprio 1
	v_mfma_f32_16x16x32_bf16 v[126:129], v[140:143], v[182:185], 0
	v_mfma_f32_16x16x32_bf16 v[122:125], v[154:157], v[182:185], 0
	v_mfma_f32_16x16x32_bf16 v[110:113], v[140:143], v[190:193], 0
	v_mfma_f32_16x16x32_bf16 v[106:109], v[154:157], v[190:193], 0
	v_mfma_f32_16x16x32_bf16 v[94:97], v[140:143], v[198:201], 0
	v_mfma_f32_16x16x32_bf16 v[90:93], v[154:157], v[198:201], 0
	v_mfma_f32_16x16x32_bf16 v[78:81], v[140:143], v[206:209], 0
	v_mfma_f32_16x16x32_bf16 v[74:77], v[154:157], v[206:209], 0
	v_mfma_f32_16x16x32_bf16 v[126:129], v[150:153], v[186:189], v[126:129]
	v_mfma_f32_16x16x32_bf16 v[122:125], v[158:161], v[186:189], v[122:125]
	v_mfma_f32_16x16x32_bf16 v[110:113], v[150:153], v[194:197], v[110:113]
	v_mfma_f32_16x16x32_bf16 v[106:109], v[158:161], v[194:197], v[106:109]
	v_mfma_f32_16x16x32_bf16 v[94:97], v[150:153], v[202:205], v[94:97]
	v_mfma_f32_16x16x32_bf16 v[90:93], v[158:161], v[202:205], v[90:93]
	v_mfma_f32_16x16x32_bf16 v[78:81], v[150:153], v[210:213], v[78:81]
	v_mfma_f32_16x16x32_bf16 v[74:77], v[158:161], v[210:213], v[74:77]
	s_setprio 0
	s_setprio 1
	v_mfma_f32_16x16x32_bf16 v[118:121], v[162:165], v[182:185], 0
	v_mfma_f32_16x16x32_bf16 v[114:117], v[174:177], v[182:185], 0
	v_mfma_f32_16x16x32_bf16 v[102:105], v[162:165], v[190:193], 0
	v_mfma_f32_16x16x32_bf16 v[98:101], v[174:177], v[190:193], 0
	v_mfma_f32_16x16x32_bf16 v[86:89], v[162:165], v[198:201], 0
	v_mfma_f32_16x16x32_bf16 v[82:85], v[174:177], v[198:201], 0
	v_mfma_f32_16x16x32_bf16 v[70:73], v[162:165], v[206:209], 0
	v_mfma_f32_16x16x32_bf16 v[66:69], v[174:177], v[206:209], 0
	v_mfma_f32_16x16x32_bf16 v[118:121], v[170:173], v[186:189], v[118:121]
	v_mfma_f32_16x16x32_bf16 v[114:117], v[178:181], v[186:189], v[114:117]
	v_mfma_f32_16x16x32_bf16 v[102:105], v[170:173], v[194:197], v[102:105]
	v_mfma_f32_16x16x32_bf16 v[98:101], v[178:181], v[194:197], v[98:101]
	v_mfma_f32_16x16x32_bf16 v[86:89], v[170:173], v[202:205], v[86:89]
	v_mfma_f32_16x16x32_bf16 v[82:85], v[178:181], v[202:205], v[82:85]
	v_mfma_f32_16x16x32_bf16 v[70:73], v[170:173], v[210:213], v[70:73]
	v_mfma_f32_16x16x32_bf16 v[66:69], v[178:181], v[210:213], v[66:69]
	s_setprio 0
	s_barrier
	s_add_i32 s68, s68, s15
	v_lshl_add_u64 v[144:145], s[54:55], 0, v[166:167]
	s_mov_b32 m0, s68
	ds_read_b128 v[182:185], v149 offset:16384
	ds_read_b128 v[186:189], v149 offset:17408
	ds_read_b128 v[190:193], v149 offset:18432
	ds_read_b128 v[194:197], v149 offset:19456
	ds_read_b128 v[198:201], v149 offset:20480
	ds_read_b128 v[202:205], v149 offset:21504
	ds_read_b128 v[206:209], v149 offset:22528
	ds_read_b128 v[210:213], v149 offset:23552
	global_load_lds_dwordx4 v[144:145], off
	s_add_i32 m0, s68, 0x2000
	s_add_u32 s68, s54, 0x40000
	v_lshl_add_u64 v[214:215], s[54:55], 0, v[130:131]
	s_addc_u32 s69, s55, 0
	s_add_i32 s70, s70, s15
	global_load_lds_dwordx4 v[214:215], off
	v_lshl_add_u64 v[216:217], s[68:69], 0, v[166:167]
	s_mov_b32 m0, s70
	v_lshl_add_u64 v[218:219], s[58:59], 0, v[134:135]
	global_load_lds_dwordx4 v[216:217], off
	v_lshl_add_u64 v[216:217], s[68:69], 0, v[130:131]
	s_add_i32 m0, s70, 0x2000
	s_nop 0
	global_load_lds_dwordx4 v[216:217], off
	v_lshl_add_u64 v[216:217], s[58:59], 0, v[132:133]
	s_mov_b32 m0, s16
	s_nop 0
	global_load_lds_dwordx4 v[216:217], off
	s_mov_b32 m0, s20
	s_nop 0
	global_load_lds_dwordx4 v[218:219], off
	s_waitcnt vmcnt(8)
	s_waitcnt lgkmcnt(0)
	s_barrier
	s_setprio 1
	v_mfma_f32_16x16x32_bf16 v[62:65], v[140:143], v[182:185], 0
	v_mfma_f32_16x16x32_bf16 v[58:61], v[154:157], v[182:185], 0
	v_mfma_f32_16x16x32_bf16 v[46:49], v[140:143], v[190:193], 0
	v_mfma_f32_16x16x32_bf16 v[42:45], v[154:157], v[190:193], 0
	v_mfma_f32_16x16x32_bf16 v[30:33], v[140:143], v[198:201], 0
	v_mfma_f32_16x16x32_bf16 v[26:29], v[154:157], v[198:201], 0
	v_mfma_f32_16x16x32_bf16 v[14:17], v[140:143], v[206:209], 0
	v_mfma_f32_16x16x32_bf16 v[10:13], v[154:157], v[206:209], 0
	v_mfma_f32_16x16x32_bf16 v[62:65], v[150:153], v[186:189], v[62:65]
	v_mfma_f32_16x16x32_bf16 v[58:61], v[158:161], v[186:189], v[58:61]
	v_mfma_f32_16x16x32_bf16 v[46:49], v[150:153], v[194:197], v[46:49]
	v_mfma_f32_16x16x32_bf16 v[42:45], v[158:161], v[194:197], v[42:45]
	v_mfma_f32_16x16x32_bf16 v[30:33], v[150:153], v[202:205], v[30:33]
	v_mfma_f32_16x16x32_bf16 v[26:29], v[158:161], v[202:205], v[26:29]
	v_mfma_f32_16x16x32_bf16 v[14:17], v[150:153], v[210:213], v[14:17]
	v_mfma_f32_16x16x32_bf16 v[10:13], v[158:161], v[210:213], v[10:13]
	s_setprio 0
	s_setprio 1
	v_mfma_f32_16x16x32_bf16 v[54:57], v[162:165], v[182:185], 0
	v_mfma_f32_16x16x32_bf16 v[50:53], v[174:177], v[182:185], 0
	v_mfma_f32_16x16x32_bf16 v[38:41], v[162:165], v[190:193], 0
	v_mfma_f32_16x16x32_bf16 v[34:37], v[174:177], v[190:193], 0
	v_mfma_f32_16x16x32_bf16 v[22:25], v[162:165], v[198:201], 0
	v_mfma_f32_16x16x32_bf16 v[18:21], v[174:177], v[198:201], 0
	v_mfma_f32_16x16x32_bf16 v[6:9], v[162:165], v[206:209], 0
	v_mfma_f32_16x16x32_bf16 v[2:5], v[174:177], v[206:209], 0
	v_mfma_f32_16x16x32_bf16 v[54:57], v[170:173], v[186:189], v[54:57]
	v_mfma_f32_16x16x32_bf16 v[50:53], v[178:181], v[186:189], v[50:53]
	v_mfma_f32_16x16x32_bf16 v[38:41], v[170:173], v[194:197], v[38:41]
	v_mfma_f32_16x16x32_bf16 v[34:37], v[178:181], v[194:197], v[34:37]
	v_mfma_f32_16x16x32_bf16 v[22:25], v[170:173], v[202:205], v[22:25]
	v_mfma_f32_16x16x32_bf16 v[18:21], v[178:181], v[202:205], v[18:21]
	v_mfma_f32_16x16x32_bf16 v[6:9], v[170:173], v[210:213], v[6:9]
	v_mfma_f32_16x16x32_bf16 v[2:5], v[178:181], v[210:213], v[2:5]
	s_setprio 0
	s_barrier
	s_add_i32 s68, 0, 0x18000
	s_add_i32 s69, 0, 0x1c000
	v_add_u32_e32 v158, s68, v147
	v_add_u32_e32 v169, s69, v147
	ds_read_b128 v[140:143], v158
	ds_read_b128 v[150:153], v158 offset:1024
	ds_read_b128 v[154:157], v158 offset:2048
	ds_read_b128 v[158:161], v158 offset:3072
	ds_read_b128 v[162:165], v169
	ds_read_b128 v[170:173], v169 offset:1024
	ds_read_b128 v[174:177], v169 offset:2048
	ds_read_b128 v[178:181], v169 offset:3072
	s_add_u32 s58, s58, 0x40000
	s_addc_u32 s59, s59, 0
	s_mov_b32 m0, s21
	v_lshl_add_u64 v[220:221], s[58:59], 0, v[132:133]
	ds_read_b128 v[182:185], v149 offset:32768
	ds_read_b128 v[186:189], v149 offset:33792
	ds_read_b128 v[190:193], v149 offset:34816
	ds_read_b128 v[194:197], v149 offset:35840
	ds_read_b128 v[198:201], v149 offset:36864
	ds_read_b128 v[202:205], v149 offset:37888
	ds_read_b128 v[206:209], v149 offset:38912
	ds_read_b128 v[210:213], v149 offset:39936
	global_load_lds_dwordx4 v[220:221], off
	v_lshl_add_u64 v[220:221], s[58:59], 0, v[134:135]
	s_mov_b32 m0, s22
	s_nop 0
	global_load_lds_dwordx4 v[220:221], off
	s_waitcnt vmcnt(8)
	s_waitcnt lgkmcnt(0)
	s_barrier
	s_setprio 1
	v_mfma_f32_16x16x32_bf16 v[126:129], v[140:143], v[182:185], v[126:129]
	v_mfma_f32_16x16x32_bf16 v[122:125], v[154:157], v[182:185], v[122:125]
	v_mfma_f32_16x16x32_bf16 v[110:113], v[140:143], v[190:193], v[110:113]
	v_mfma_f32_16x16x32_bf16 v[106:109], v[154:157], v[190:193], v[106:109]
	v_mfma_f32_16x16x32_bf16 v[94:97], v[140:143], v[198:201], v[94:97]
	v_mfma_f32_16x16x32_bf16 v[90:93], v[154:157], v[198:201], v[90:93]
	v_mfma_f32_16x16x32_bf16 v[78:81], v[140:143], v[206:209], v[78:81]
	v_mfma_f32_16x16x32_bf16 v[74:77], v[154:157], v[206:209], v[74:77]
	v_mfma_f32_16x16x32_bf16 v[126:129], v[150:153], v[186:189], v[126:129]
	v_mfma_f32_16x16x32_bf16 v[122:125], v[158:161], v[186:189], v[122:125]
	v_mfma_f32_16x16x32_bf16 v[110:113], v[150:153], v[194:197], v[110:113]
	v_mfma_f32_16x16x32_bf16 v[106:109], v[158:161], v[194:197], v[106:109]
	v_mfma_f32_16x16x32_bf16 v[94:97], v[150:153], v[202:205], v[94:97]
	v_mfma_f32_16x16x32_bf16 v[90:93], v[158:161], v[202:205], v[90:93]
	v_mfma_f32_16x16x32_bf16 v[78:81], v[150:153], v[210:213], v[78:81]
	v_mfma_f32_16x16x32_bf16 v[74:77], v[158:161], v[210:213], v[74:77]
	s_setprio 0
	s_setprio 1
	v_mfma_f32_16x16x32_bf16 v[118:121], v[162:165], v[182:185], v[118:121]
	v_mfma_f32_16x16x32_bf16 v[114:117], v[174:177], v[182:185], v[114:117]
	v_mfma_f32_16x16x32_bf16 v[102:105], v[162:165], v[190:193], v[102:105]
	v_mfma_f32_16x16x32_bf16 v[98:101], v[174:177], v[190:193], v[98:101]
	v_mfma_f32_16x16x32_bf16 v[86:89], v[162:165], v[198:201], v[86:89]
	v_mfma_f32_16x16x32_bf16 v[82:85], v[174:177], v[198:201], v[82:85]
	v_mfma_f32_16x16x32_bf16 v[70:73], v[162:165], v[206:209], v[70:73]
	v_mfma_f32_16x16x32_bf16 v[66:69], v[174:177], v[206:209], v[66:69]
	v_mfma_f32_16x16x32_bf16 v[118:121], v[170:173], v[186:189], v[118:121]
	v_mfma_f32_16x16x32_bf16 v[114:117], v[178:181], v[186:189], v[114:117]
	v_mfma_f32_16x16x32_bf16 v[102:105], v[170:173], v[194:197], v[102:105]
	v_mfma_f32_16x16x32_bf16 v[98:101], v[178:181], v[194:197], v[98:101]
	v_mfma_f32_16x16x32_bf16 v[86:89], v[170:173], v[202:205], v[86:89]
	v_mfma_f32_16x16x32_bf16 v[82:85], v[178:181], v[202:205], v[82:85]
	v_mfma_f32_16x16x32_bf16 v[70:73], v[170:173], v[210:213], v[70:73]
	v_mfma_f32_16x16x32_bf16 v[66:69], v[178:181], v[210:213], v[66:69]
	s_setprio 0
	s_barrier
	s_add_i32 s58, s68, s15
	v_lshl_add_u64 v[144:145], v[144:145], 0, s[56:57]
	s_mov_b32 m0, s58
	ds_read_b128 v[182:185], v149 offset:49152
	ds_read_b128 v[186:189], v149 offset:50176
	ds_read_b128 v[190:193], v149 offset:51200
	ds_read_b128 v[194:197], v149 offset:52224
	ds_read_b128 v[198:201], v149 offset:53248
	ds_read_b128 v[202:205], v149 offset:54272
	ds_read_b128 v[206:209], v149 offset:55296
	ds_read_b128 v[210:213], v149 offset:56320
	global_load_lds_dwordx4 v[144:145], off
	s_add_i32 m0, s58, 0x2000
	s_add_u32 s54, s54, 0x40080
	v_lshl_add_u64 v[144:145], v[214:215], 0, s[56:57]
	s_addc_u32 s55, s55, 0
	s_add_i32 s58, s69, s15
	global_load_lds_dwordx4 v[144:145], off
	v_lshl_add_u64 v[144:145], s[54:55], 0, v[166:167]
	s_mov_b32 m0, s58
	s_nop 0
	global_load_lds_dwordx4 v[144:145], off
	v_lshl_add_u64 v[144:145], s[54:55], 0, v[130:131]
	s_add_i32 m0, s58, 0x2000
	s_nop 0
	global_load_lds_dwordx4 v[144:145], off
	v_lshl_add_u64 v[144:145], v[216:217], 0, s[56:57]
	s_mov_b32 m0, s23
	s_nop 0
	global_load_lds_dwordx4 v[144:145], off
	v_lshl_add_u64 v[144:145], v[218:219], 0, s[56:57]
	s_mov_b32 m0, s24
	s_nop 0
	global_load_lds_dwordx4 v[144:145], off
	s_waitcnt vmcnt(8)
	s_waitcnt lgkmcnt(0)
	s_barrier
	s_setprio 1
	v_mfma_f32_16x16x32_bf16 v[62:65], v[140:143], v[182:185], v[62:65]
	v_mfma_f32_16x16x32_bf16 v[58:61], v[154:157], v[182:185], v[58:61]
	v_mfma_f32_16x16x32_bf16 v[46:49], v[140:143], v[190:193], v[46:49]
	v_mfma_f32_16x16x32_bf16 v[42:45], v[154:157], v[190:193], v[42:45]
	v_mfma_f32_16x16x32_bf16 v[30:33], v[140:143], v[198:201], v[30:33]
	v_mfma_f32_16x16x32_bf16 v[26:29], v[154:157], v[198:201], v[26:29]
	v_mfma_f32_16x16x32_bf16 v[14:17], v[140:143], v[206:209], v[14:17]
	v_mfma_f32_16x16x32_bf16 v[10:13], v[154:157], v[206:209], v[10:13]
	v_mfma_f32_16x16x32_bf16 v[62:65], v[150:153], v[186:189], v[62:65]
	v_mfma_f32_16x16x32_bf16 v[58:61], v[158:161], v[186:189], v[58:61]
	v_mfma_f32_16x16x32_bf16 v[46:49], v[150:153], v[194:197], v[46:49]
	v_mfma_f32_16x16x32_bf16 v[42:45], v[158:161], v[194:197], v[42:45]
	v_mfma_f32_16x16x32_bf16 v[30:33], v[150:153], v[202:205], v[30:33]
	v_mfma_f32_16x16x32_bf16 v[26:29], v[158:161], v[202:205], v[26:29]
	v_mfma_f32_16x16x32_bf16 v[14:17], v[150:153], v[210:213], v[14:17]
	v_mfma_f32_16x16x32_bf16 v[10:13], v[158:161], v[210:213], v[10:13]
	s_setprio 0
	s_setprio 1
	v_mfma_f32_16x16x32_bf16 v[54:57], v[162:165], v[182:185], v[54:57]
	v_mfma_f32_16x16x32_bf16 v[50:53], v[174:177], v[182:185], v[50:53]
	v_mfma_f32_16x16x32_bf16 v[38:41], v[162:165], v[190:193], v[38:41]
	v_mfma_f32_16x16x32_bf16 v[34:37], v[174:177], v[190:193], v[34:37]
	v_mfma_f32_16x16x32_bf16 v[22:25], v[162:165], v[198:201], v[22:25]
	v_mfma_f32_16x16x32_bf16 v[18:21], v[174:177], v[198:201], v[18:21]
	v_mfma_f32_16x16x32_bf16 v[6:9], v[162:165], v[206:209], v[6:9]
	v_mfma_f32_16x16x32_bf16 v[2:5], v[174:177], v[206:209], v[2:5]
	v_mfma_f32_16x16x32_bf16 v[54:57], v[170:173], v[186:189], v[54:57]
	v_mfma_f32_16x16x32_bf16 v[50:53], v[178:181], v[186:189], v[50:53]
	v_mfma_f32_16x16x32_bf16 v[38:41], v[170:173], v[194:197], v[38:41]
	v_mfma_f32_16x16x32_bf16 v[34:37], v[178:181], v[194:197], v[34:37]
	v_mfma_f32_16x16x32_bf16 v[22:25], v[170:173], v[202:205], v[22:25]
	v_mfma_f32_16x16x32_bf16 v[18:21], v[178:181], v[202:205], v[18:21]
	v_mfma_f32_16x16x32_bf16 v[6:9], v[170:173], v[210:213], v[6:9]
	v_mfma_f32_16x16x32_bf16 v[2:5], v[178:181], v[210:213], v[2:5]
	s_setprio 0
	s_barrier
	s_add_u32 s64, s64, 0x100
	s_addc_u32 s65, s65, 0
	s_add_u32 s52, s52, 0x100
	s_addc_u32 s53, s53, 0
	s_cmp_ge_i32 s66, s1
	s_mov_b32 s54, s66
	s_cbranch_scc0 .LBB0_1438
	s_branch .Lpeelexitph12
	.p2align	6

.Lpeelph15_1:
	s_add_i32 s91, s91, 2
	s_add_u32 s64, s70, 0x100
	s_addc_u32 s65, s71, 0
	s_and_b64 s[74:75], s[68:69], exec
	s_cselect_b32 s74, 0, s64
	s_cselect_b32 s75, 0, s65
	s_add_u32 s74, s28, s74
	s_addc_u32 s75, s29, s75
	s_add_u32 s92, s51, s70
	s_addc_u32 s93, s53, s71
	s_and_b64 s[68:69], s[68:69], exec
	s_cselect_b32 s69, s55, s93
	s_cselect_b32 s68, s54, s92
	s_add_i32 s93, 0, 0x10000
	s_add_i32 s92, 0, 0x14000
	v_add_u32_e32 v2, s93, v210
	v_add_u32_e32 v6, s92, v210
	ds_read_b128 v[26:29], v2
	ds_read_b128 v[30:33], v2 offset:1024
	ds_read_b128 v[18:21], v2 offset:2048
	ds_read_b128 v[22:25], v2 offset:3072
	ds_read_b128 v[10:13], v6
	ds_read_b128 v[14:17], v6 offset:1024
	ds_read_b128 v[2:5], v6 offset:2048
	ds_read_b128 v[6:9], v6 offset:3072
	v_lshl_add_u64 v[170:171], v[194:195], 0, s[70:71]
	s_add_i32 m0, s59, 0xc000
	ds_read_b128 v[196:199], v212
	ds_read_b128 v[200:203], v212 offset:1024
	ds_read_b128 v[214:217], v212 offset:2048
	ds_read_b128 v[218:221], v212 offset:3072
	ds_read_b128 v[236:239], v212 offset:4096
	ds_read_b128 v[240:243], v212 offset:5120
	ds_read_b128 v[244:247], v212 offset:6144
	ds_read_b128 v[248:251], v212 offset:7168
	global_load_lds_dwordx4 v[170:171], off
	v_lshl_add_u64 v[170:171], v[192:193], 0, s[70:71]
	s_add_i32 m0, s59, 0xe000
	s_nop 0
	global_load_lds_dwordx4 v[170:171], off
	s_waitcnt vmcnt(8)
	s_waitcnt lgkmcnt(0)
	s_barrier
	s_setprio 1
	v_mfma_scale_f32_16x16x128_f8f6f4 v[154:157], v[26:33], v[196:203], 0, v208, v207 op_sel_hi:[0,0,0]
	v_mfma_scale_f32_16x16x128_f8f6f4 v[150:153], v[18:25], v[196:203], 0, v208, v207 op_sel_hi:[0,0,0]
	v_mfma_scale_f32_16x16x128_f8f6f4 v[142:145], v[26:33], v[214:221], 0, v208, v207 op_sel_hi:[0,0,0]
	v_mfma_scale_f32_16x16x128_f8f6f4 v[134:137], v[18:25], v[214:221], 0, v208, v207 op_sel_hi:[0,0,0]
	v_mfma_scale_f32_16x16x128_f8f6f4 v[126:129], v[26:33], v[236:243], 0, v208, v207 op_sel_hi:[0,0,0]
	v_mfma_scale_f32_16x16x128_f8f6f4 v[118:121], v[18:25], v[236:243], 0, v208, v207 op_sel_hi:[0,0,0]
	v_mfma_scale_f32_16x16x128_f8f6f4 v[110:113], v[26:33], v[244:251], 0, v208, v207 op_sel_hi:[0,0,0]
	v_mfma_scale_f32_16x16x128_f8f6f4 v[102:105], v[18:25], v[244:251], 0, v208, v207 op_sel_hi:[0,0,0]
	s_setprio 0
	s_setprio 1
	v_mfma_scale_f32_16x16x128_f8f6f4 v[158:161], v[10:17], v[196:203], 0, v208, v207 op_sel_hi:[0,0,0]
	v_mfma_scale_f32_16x16x128_f8f6f4 v[146:149], v[2:9], v[196:203], 0, v208, v207 op_sel_hi:[0,0,0]
	v_mfma_scale_f32_16x16x128_f8f6f4 v[138:141], v[10:17], v[214:221], 0, v208, v207 op_sel_hi:[0,0,0]
	v_mfma_scale_f32_16x16x128_f8f6f4 v[130:133], v[2:9], v[214:221], 0, v208, v207 op_sel_hi:[0,0,0]
	v_mfma_scale_f32_16x16x128_f8f6f4 v[122:125], v[10:17], v[236:243], 0, v208, v207 op_sel_hi:[0,0,0]
	v_mfma_scale_f32_16x16x128_f8f6f4 v[114:117], v[2:9], v[236:243], 0, v208, v207 op_sel_hi:[0,0,0]
	v_mfma_scale_f32_16x16x128_f8f6f4 v[106:109], v[10:17], v[244:251], 0, v208, v207 op_sel_hi:[0,0,0]
	v_mfma_scale_f32_16x16x128_f8f6f4 v[98:101], v[2:9], v[244:251], 0, v208, v207 op_sel_hi:[0,0,0]
	s_setprio 0
	s_barrier
	s_add_i32 s70, s93, s72
	v_lshl_add_u64 v[196:197], s[68:69], 0, v[162:163]
	s_mov_b32 m0, s70
	ds_read_b128 v[214:217], v212 offset:16384
	ds_read_b128 v[218:221], v212 offset:17408
	ds_read_b128 v[236:239], v212 offset:18432
	ds_read_b128 v[240:243], v212 offset:19456
	ds_read_b128 v[244:247], v212 offset:20480
	ds_read_b128 v[248:251], v212 offset:21504
	ds_read_b128 v[170:173], v212 offset:22528
	ds_read_b128 v[174:177], v212 offset:23552
	global_load_lds_dwordx4 v[196:197], off
	s_add_i32 m0, s70, 0x2000
	s_add_u32 s70, s68, 0x20000
	v_lshl_add_u64 v[198:199], s[68:69], 0, v[164:165]
	s_addc_u32 s71, s69, 0
	s_add_i32 s92, s92, s72
	global_load_lds_dwordx4 v[198:199], off
	v_lshl_add_u64 v[200:201], s[70:71], 0, v[162:163]
	s_mov_b32 m0, s92
	v_mov_b32_e32 v179, v167
	global_load_lds_dwordx4 v[200:201], off
	v_lshl_add_u64 v[200:201], s[70:71], 0, v[164:165]
	s_add_i32 m0, s92, 0x2000
	v_lshl_add_u64 v[202:203], s[74:75], 0, v[166:167]
	global_load_lds_dwordx4 v[200:201], off
	s_mov_b32 m0, s59
	v_lshl_add_u64 v[200:201], s[74:75], 0, v[178:179]
	global_load_lds_dwordx4 v166, s[74:75]
	s_mov_b32 m0, s61
	s_nop 0
	global_load_lds_dwordx4 v178, s[74:75]
	s_waitcnt vmcnt(8)
	s_waitcnt lgkmcnt(0)
	s_barrier
	s_setprio 1
	v_mfma_scale_f32_16x16x128_f8f6f4 v[94:97], v[26:33], v[214:221], 0, v208, v207 op_sel_hi:[0,0,0]
	v_mfma_scale_f32_16x16x128_f8f6f4 v[86:89], v[18:25], v[214:221], 0, v208, v207 op_sel_hi:[0,0,0]
	v_mfma_scale_f32_16x16x128_f8f6f4 v[78:81], v[26:33], v[236:243], 0, v208, v207 op_sel_hi:[0,0,0]
	v_mfma_scale_f32_16x16x128_f8f6f4 v[70:73], v[18:25], v[236:243], 0, v208, v207 op_sel_hi:[0,0,0]
	v_mfma_scale_f32_16x16x128_f8f6f4 v[62:65], v[26:33], v[244:251], 0, v208, v207 op_sel_hi:[0,0,0]
	v_mfma_scale_f32_16x16x128_f8f6f4 v[54:57], v[18:25], v[244:251], 0, v208, v207 op_sel_hi:[0,0,0]
	v_mfma_scale_f32_16x16x128_f8f6f4 v[46:49], v[26:33], v[170:177], 0, v208, v207 op_sel_hi:[0,0,0]
	v_mfma_scale_f32_16x16x128_f8f6f4 v[38:41], v[18:25], v[170:177], 0, v208, v207 op_sel_hi:[0,0,0]
	s_setprio 0
	s_setprio 1
	v_mfma_scale_f32_16x16x128_f8f6f4 v[90:93], v[10:17], v[214:221], 0, v208, v207 op_sel_hi:[0,0,0]
	v_mfma_scale_f32_16x16x128_f8f6f4 v[82:85], v[2:9], v[214:221], 0, v208, v207 op_sel_hi:[0,0,0]
	v_mfma_scale_f32_16x16x128_f8f6f4 v[74:77], v[10:17], v[236:243], 0, v208, v207 op_sel_hi:[0,0,0]
	v_mfma_scale_f32_16x16x128_f8f6f4 v[66:69], v[2:9], v[236:243], 0, v208, v207 op_sel_hi:[0,0,0]
	v_mfma_scale_f32_16x16x128_f8f6f4 v[58:61], v[10:17], v[244:251], 0, v208, v207 op_sel_hi:[0,0,0]
	v_mfma_scale_f32_16x16x128_f8f6f4 v[50:53], v[2:9], v[244:251], 0, v208, v207 op_sel_hi:[0,0,0]
	v_mfma_scale_f32_16x16x128_f8f6f4 v[42:45], v[10:17], v[170:177], 0, v208, v207 op_sel_hi:[0,0,0]
	v_mfma_scale_f32_16x16x128_f8f6f4 v[34:37], v[2:9], v[170:177], 0, v208, v207 op_sel_hi:[0,0,0]
	s_setprio 0
	s_barrier
	s_add_i32 s70, 0, 0x18000
	s_add_i32 s71, 0, 0x1c000
	v_add_u32_e32 v2, s70, v210
	v_add_u32_e32 v6, s71, v210
	ds_read_b128 v[26:29], v2
	ds_read_b128 v[30:33], v2 offset:1024
	ds_read_b128 v[18:21], v2 offset:2048
	ds_read_b128 v[22:25], v2 offset:3072
	ds_read_b128 v[10:13], v6
	ds_read_b128 v[14:17], v6 offset:1024
	ds_read_b128 v[2:5], v6 offset:2048
	ds_read_b128 v[6:9], v6 offset:3072
	s_mov_b32 m0, s73
	ds_read_b128 v[170:173], v212 offset:32768
	ds_read_b128 v[174:177], v212 offset:33792
	ds_read_b128 v[214:217], v212 offset:34816
	ds_read_b128 v[218:221], v212 offset:35840
	ds_read_b128 v[236:239], v212 offset:36864
	ds_read_b128 v[240:243], v212 offset:37888
	ds_read_b128 v[244:247], v212 offset:38912
	ds_read_b128 v[248:251], v212 offset:39936
	global_load_lds_dwordx4 v180, s[74:75]
	s_mov_b32 m0, s76
	s_nop 0
	global_load_lds_dwordx4 v182, s[74:75]
	s_waitcnt vmcnt(8)
	s_waitcnt lgkmcnt(0)
	s_barrier
	s_setprio 1
	v_mfma_scale_f32_16x16x128_f8f6f4 v[154:157], v[26:33], v[170:177], v[154:157], v208, v207 op_sel_hi:[0,0,0]
	v_mfma_scale_f32_16x16x128_f8f6f4 v[150:153], v[18:25], v[170:177], v[150:153], v208, v207 op_sel_hi:[0,0,0]
	v_mfma_scale_f32_16x16x128_f8f6f4 v[142:145], v[26:33], v[214:221], v[142:145], v208, v207 op_sel_hi:[0,0,0]
	v_mfma_scale_f32_16x16x128_f8f6f4 v[134:137], v[18:25], v[214:221], v[134:137], v208, v207 op_sel_hi:[0,0,0]
	v_mfma_scale_f32_16x16x128_f8f6f4 v[126:129], v[26:33], v[236:243], v[126:129], v208, v207 op_sel_hi:[0,0,0]
	v_mfma_scale_f32_16x16x128_f8f6f4 v[118:121], v[18:25], v[236:243], v[118:121], v208, v207 op_sel_hi:[0,0,0]
	v_mfma_scale_f32_16x16x128_f8f6f4 v[110:113], v[26:33], v[244:251], v[110:113], v208, v207 op_sel_hi:[0,0,0]
	v_mfma_scale_f32_16x16x128_f8f6f4 v[102:105], v[18:25], v[244:251], v[102:105], v208, v207 op_sel_hi:[0,0,0]
	s_setprio 0
	s_setprio 1
	v_mfma_scale_f32_16x16x128_f8f6f4 v[158:161], v[10:17], v[170:177], v[158:161], v208, v207 op_sel_hi:[0,0,0]
	v_mfma_scale_f32_16x16x128_f8f6f4 v[146:149], v[2:9], v[170:177], v[146:149], v208, v207 op_sel_hi:[0,0,0]
	v_mfma_scale_f32_16x16x128_f8f6f4 v[138:141], v[10:17], v[214:221], v[138:141], v208, v207 op_sel_hi:[0,0,0]
	v_mfma_scale_f32_16x16x128_f8f6f4 v[130:133], v[2:9], v[214:221], v[130:133], v208, v207 op_sel_hi:[0,0,0]
	v_mfma_scale_f32_16x16x128_f8f6f4 v[122:125], v[10:17], v[236:243], v[122:125], v208, v207 op_sel_hi:[0,0,0]
	v_mfma_scale_f32_16x16x128_f8f6f4 v[114:117], v[2:9], v[236:243], v[114:117], v208, v207 op_sel_hi:[0,0,0]
	v_mfma_scale_f32_16x16x128_f8f6f4 v[106:109], v[10:17], v[244:251], v[106:109], v208, v207 op_sel_hi:[0,0,0]
	v_mfma_scale_f32_16x16x128_f8f6f4 v[98:101], v[2:9], v[244:251], v[98:101], v208, v207 op_sel_hi:[0,0,0]
	s_setprio 0
	s_barrier
	s_add_i32 s70, s70, s72
	v_lshl_add_u64 v[196:197], v[196:197], 0, s[56:57]
	s_mov_b32 m0, s70
	ds_read_b128 v[170:173], v212 offset:49152
	ds_read_b128 v[174:177], v212 offset:50176
	ds_read_b128 v[214:217], v212 offset:51200
	ds_read_b128 v[218:221], v212 offset:52224
	ds_read_b128 v[236:239], v212 offset:53248
	ds_read_b128 v[240:243], v212 offset:54272
	ds_read_b128 v[244:247], v212 offset:55296
	ds_read_b128 v[248:251], v212 offset:56320
	global_load_lds_dwordx4 v[196:197], off
	s_add_i32 m0, s70, 0x2000
	s_add_u32 s68, s68, 0x20080
	v_lshl_add_u64 v[196:197], v[198:199], 0, s[56:57]
	s_addc_u32 s69, s69, 0
	s_add_i32 s70, s71, s72
	global_load_lds_dwordx4 v[196:197], off
	v_lshl_add_u64 v[196:197], s[68:69], 0, v[162:163]
	s_mov_b32 m0, s70
	s_nop 0
	global_load_lds_dwordx4 v[196:197], off
	v_lshl_add_u64 v[196:197], s[68:69], 0, v[164:165]
	s_add_i32 m0, s70, 0x2000
	s_nop 0
	global_load_lds_dwordx4 v[196:197], off
	v_lshl_add_u64 v[196:197], v[202:203], 0, s[56:57]
	s_mov_b32 m0, s77
	s_nop 0
	global_load_lds_dwordx4 v[196:197], off
	v_lshl_add_u64 v[196:197], v[200:201], 0, s[56:57]
	s_mov_b32 m0, s79
	s_nop 0
	global_load_lds_dwordx4 v[196:197], off
	s_waitcnt vmcnt(8)
	s_waitcnt lgkmcnt(0)
	s_barrier
	s_setprio 1
	v_mfma_scale_f32_16x16x128_f8f6f4 v[94:97], v[26:33], v[170:177], v[94:97], v208, v207 op_sel_hi:[0,0,0]
	v_mfma_scale_f32_16x16x128_f8f6f4 v[86:89], v[18:25], v[170:177], v[86:89], v208, v207 op_sel_hi:[0,0,0]
	v_mfma_scale_f32_16x16x128_f8f6f4 v[78:81], v[26:33], v[214:221], v[78:81], v208, v207 op_sel_hi:[0,0,0]
	v_mfma_scale_f32_16x16x128_f8f6f4 v[70:73], v[18:25], v[214:221], v[70:73], v208, v207 op_sel_hi:[0,0,0]
	v_mfma_scale_f32_16x16x128_f8f6f4 v[62:65], v[26:33], v[236:243], v[62:65], v208, v207 op_sel_hi:[0,0,0]
	v_mfma_scale_f32_16x16x128_f8f6f4 v[54:57], v[18:25], v[236:243], v[54:57], v208, v207 op_sel_hi:[0,0,0]
	v_mfma_scale_f32_16x16x128_f8f6f4 v[46:49], v[26:33], v[244:251], v[46:49], v208, v207 op_sel_hi:[0,0,0]
	v_mfma_scale_f32_16x16x128_f8f6f4 v[38:41], v[18:25], v[244:251], v[38:41], v208, v207 op_sel_hi:[0,0,0]
	s_setprio 0
	s_setprio 1
	v_mfma_scale_f32_16x16x128_f8f6f4 v[90:93], v[10:17], v[170:177], v[90:93], v208, v207 op_sel_hi:[0,0,0]
	v_mfma_scale_f32_16x16x128_f8f6f4 v[82:85], v[2:9], v[170:177], v[82:85], v208, v207 op_sel_hi:[0,0,0]
	v_mfma_scale_f32_16x16x128_f8f6f4 v[74:77], v[10:17], v[214:221], v[74:77], v208, v207 op_sel_hi:[0,0,0]
	v_mfma_scale_f32_16x16x128_f8f6f4 v[66:69], v[2:9], v[214:221], v[66:69], v208, v207 op_sel_hi:[0,0,0]
	v_mfma_scale_f32_16x16x128_f8f6f4 v[58:61], v[10:17], v[236:243], v[58:61], v208, v207 op_sel_hi:[0,0,0]
	v_mfma_scale_f32_16x16x128_f8f6f4 v[50:53], v[2:9], v[236:243], v[50:53], v208, v207 op_sel_hi:[0,0,0]
	v_mfma_scale_f32_16x16x128_f8f6f4 v[42:45], v[10:17], v[244:251], v[42:45], v208, v207 op_sel_hi:[0,0,0]
	v_mfma_scale_f32_16x16x128_f8f6f4 v[34:37], v[2:9], v[244:251], v[34:37], v208, v207 op_sel_hi:[0,0,0]
	s_setprio 0
	s_barrier
	s_cmp_ge_i32 s91, s11
	s_cbranch_scc1 .LBB0_1695
	s_mov_b64 s[70:71], s[64:65]
	s_branch .LBB0_1691
	.p2align	6

.Lpeelph16_0:
	s_add_i32 s91, s64, 2
	s_add_u32 s62, s60, 0x100
	s_addc_u32 s63, s61, 0
	s_add_i32 s92, 0, 0x10000
	s_cmp_eq_u32 s74, s64
	s_cselect_b32 s69, s53, s63
	s_cselect_b32 s68, s52, s62
	s_cselect_b32 s65, s55, s59
	s_cselect_b32 s64, s54, s51
	s_add_i32 s93, 0, 0x14000
	v_add_u32_e32 v2, s92, v196
	v_add_u32_e32 v6, s93, v196
	ds_read_b128 v[26:29], v2
	ds_read_b128 v[30:33], v2 offset:1024
	ds_read_b128 v[18:21], v2 offset:2048
	ds_read_b128 v[22:25], v2 offset:3072
	ds_read_b128 v[10:13], v6
	ds_read_b128 v[14:17], v6 offset:1024
	ds_read_b128 v[2:5], v6 offset:2048
	ds_read_b128 v[6:9], v6 offset:3072
	v_lshl_add_u64 v[216:217], s[60:61], 0, v[184:185]
	s_add_i32 m0, s21, 0xc000
	ds_read_b128 v[170:173], v198
	ds_read_b128 v[174:177], v198 offset:1024
	ds_read_b128 v[186:189], v198 offset:2048
	ds_read_b128 v[190:193], v198 offset:3072
	ds_read_b128 v[200:203], v198 offset:4096
	ds_read_b128 v[204:207], v198 offset:5120
	ds_read_b128 v[208:211], v198 offset:6144
	ds_read_b128 v[212:215], v198 offset:7168
	global_load_lds_dwordx4 v[216:217], off
	v_lshl_add_u64 v[216:217], s[60:61], 0, v[182:183]
	s_add_i32 m0, s21, 0xe000
	s_nop 0
	global_load_lds_dwordx4 v[216:217], off
	s_waitcnt vmcnt(8)
	s_waitcnt lgkmcnt(0)
	s_barrier
	s_setprio 1
	v_mfma_scale_f32_16x16x128_f8f6f4 v[154:157], v[26:33], v[170:177], 0, v194, v169 op_sel_hi:[0,0,0]
	v_mfma_scale_f32_16x16x128_f8f6f4 v[158:161], v[18:25], v[170:177], 0, v194, v169 op_sel_hi:[0,0,0]
	v_mfma_scale_f32_16x16x128_f8f6f4 v[138:141], v[26:33], v[186:193], 0, v194, v169 op_sel_hi:[0,0,0]
	v_mfma_scale_f32_16x16x128_f8f6f4 v[142:145], v[18:25], v[186:193], 0, v194, v169 op_sel_hi:[0,0,0]
	v_mfma_scale_f32_16x16x128_f8f6f4 v[122:125], v[26:33], v[200:207], 0, v194, v169 op_sel_hi:[0,0,0]
	v_mfma_scale_f32_16x16x128_f8f6f4 v[126:129], v[18:25], v[200:207], 0, v194, v169 op_sel_hi:[0,0,0]
	v_mfma_scale_f32_16x16x128_f8f6f4 v[106:109], v[26:33], v[208:215], 0, v194, v169 op_sel_hi:[0,0,0]
	v_mfma_scale_f32_16x16x128_f8f6f4 v[110:113], v[18:25], v[208:215], 0, v194, v169 op_sel_hi:[0,0,0]
	s_setprio 0
	s_setprio 1
	v_mfma_scale_f32_16x16x128_f8f6f4 v[146:149], v[10:17], v[170:177], 0, v194, v169 op_sel_hi:[0,0,0]
	v_mfma_scale_f32_16x16x128_f8f6f4 v[150:153], v[2:9], v[170:177], 0, v194, v169 op_sel_hi:[0,0,0]
	v_mfma_scale_f32_16x16x128_f8f6f4 v[130:133], v[10:17], v[186:193], 0, v194, v169 op_sel_hi:[0,0,0]
	v_mfma_scale_f32_16x16x128_f8f6f4 v[134:137], v[2:9], v[186:193], 0, v194, v169 op_sel_hi:[0,0,0]
	v_mfma_scale_f32_16x16x128_f8f6f4 v[114:117], v[10:17], v[200:207], 0, v194, v169 op_sel_hi:[0,0,0]
	v_mfma_scale_f32_16x16x128_f8f6f4 v[118:121], v[2:9], v[200:207], 0, v194, v169 op_sel_hi:[0,0,0]
	v_mfma_scale_f32_16x16x128_f8f6f4 v[98:101], v[10:17], v[208:215], 0, v194, v169 op_sel_hi:[0,0,0]
	v_mfma_scale_f32_16x16x128_f8f6f4 v[102:105], v[2:9], v[208:215], 0, v194, v169 op_sel_hi:[0,0,0]
	s_setprio 0
	s_barrier
	s_add_i32 s60, s92, s20
	v_lshl_add_u64 v[186:187], s[64:65], 0, v[164:165]
	s_mov_b32 m0, s60
	ds_read_b128 v[170:173], v198 offset:16384
	ds_read_b128 v[174:177], v198 offset:17408
	ds_read_b128 v[200:203], v198 offset:18432
	ds_read_b128 v[204:207], v198 offset:19456
	ds_read_b128 v[208:211], v198 offset:20480
	ds_read_b128 v[212:215], v198 offset:21504
	ds_read_b128 v[216:219], v198 offset:22528
	ds_read_b128 v[220:223], v198 offset:23552
	global_load_lds_dwordx4 v[186:187], off
	s_add_i32 m0, s60, 0x2000
	s_add_u32 s60, s64, 0x70000
	v_lshl_add_u64 v[188:189], s[64:65], 0, v[180:181]
	s_addc_u32 s61, s65, 0
	s_add_i32 s92, s93, s20
	global_load_lds_dwordx4 v[188:189], off
	v_lshl_add_u64 v[190:191], s[60:61], 0, v[164:165]
	s_mov_b32 m0, s92
	v_lshl_add_u64 v[192:193], s[68:69], 0, v[178:179]
	global_load_lds_dwordx4 v[190:191], off
	v_lshl_add_u64 v[190:191], s[60:61], 0, v[180:181]
	s_add_i32 m0, s92, 0x2000
	s_nop 0
	global_load_lds_dwordx4 v[190:191], off
	v_lshl_add_u64 v[190:191], s[68:69], 0, v[162:163]
	s_mov_b32 m0, s21
	s_nop 0
	global_load_lds_dwordx4 v[190:191], off
	s_mov_b32 m0, s22
	s_nop 0
	global_load_lds_dwordx4 v[192:193], off
	s_waitcnt vmcnt(8)
	s_waitcnt lgkmcnt(0)
	s_barrier
	s_setprio 1
	v_mfma_scale_f32_16x16x128_f8f6f4 v[90:93], v[26:33], v[170:177], 0, v194, v169 op_sel_hi:[0,0,0]
	v_mfma_scale_f32_16x16x128_f8f6f4 v[94:97], v[18:25], v[170:177], 0, v194, v169 op_sel_hi:[0,0,0]
	v_mfma_scale_f32_16x16x128_f8f6f4 v[74:77], v[26:33], v[200:207], 0, v194, v169 op_sel_hi:[0,0,0]
	v_mfma_scale_f32_16x16x128_f8f6f4 v[78:81], v[18:25], v[200:207], 0, v194, v169 op_sel_hi:[0,0,0]
	v_mfma_scale_f32_16x16x128_f8f6f4 v[58:61], v[26:33], v[208:215], 0, v194, v169 op_sel_hi:[0,0,0]
	v_mfma_scale_f32_16x16x128_f8f6f4 v[62:65], v[18:25], v[208:215], 0, v194, v169 op_sel_hi:[0,0,0]
	v_mfma_scale_f32_16x16x128_f8f6f4 v[42:45], v[26:33], v[216:223], 0, v194, v169 op_sel_hi:[0,0,0]
	v_mfma_scale_f32_16x16x128_f8f6f4 v[46:49], v[18:25], v[216:223], 0, v194, v169 op_sel_hi:[0,0,0]
	s_setprio 0
	s_setprio 1
	v_mfma_scale_f32_16x16x128_f8f6f4 v[82:85], v[10:17], v[170:177], 0, v194, v169 op_sel_hi:[0,0,0]
	v_mfma_scale_f32_16x16x128_f8f6f4 v[86:89], v[2:9], v[170:177], 0, v194, v169 op_sel_hi:[0,0,0]
	v_mfma_scale_f32_16x16x128_f8f6f4 v[66:69], v[10:17], v[200:207], 0, v194, v169 op_sel_hi:[0,0,0]
	v_mfma_scale_f32_16x16x128_f8f6f4 v[70:73], v[2:9], v[200:207], 0, v194, v169 op_sel_hi:[0,0,0]
	v_mfma_scale_f32_16x16x128_f8f6f4 v[50:53], v[10:17], v[208:215], 0, v194, v169 op_sel_hi:[0,0,0]
	v_mfma_scale_f32_16x16x128_f8f6f4 v[54:57], v[2:9], v[208:215], 0, v194, v169 op_sel_hi:[0,0,0]
	v_mfma_scale_f32_16x16x128_f8f6f4 v[34:37], v[10:17], v[216:223], 0, v194, v169 op_sel_hi:[0,0,0]
	v_mfma_scale_f32_16x16x128_f8f6f4 v[38:41], v[2:9], v[216:223], 0, v194, v169 op_sel_hi:[0,0,0]
	s_setprio 0
	s_barrier
	s_add_i32 s92, 0, 0x18000
	s_add_i32 s93, 0, 0x1c000
	v_add_u32_e32 v2, s92, v196
	v_add_u32_e32 v6, s93, v196
	ds_read_b128 v[26:29], v2
	ds_read_b128 v[30:33], v2 offset:1024
	ds_read_b128 v[18:21], v2 offset:2048
	ds_read_b128 v[22:25], v2 offset:3072
	ds_read_b128 v[10:13], v6
	ds_read_b128 v[14:17], v6 offset:1024
	ds_read_b128 v[2:5], v6 offset:2048
	ds_read_b128 v[6:9], v6 offset:3072
	s_add_u32 s60, s68, 0x70000
	s_addc_u32 s61, s69, 0
	s_mov_b32 m0, s23
	v_lshl_add_u64 v[232:233], s[60:61], 0, v[162:163]
	ds_read_b128 v[170:173], v198 offset:32768
	ds_read_b128 v[174:177], v198 offset:33792
	ds_read_b128 v[200:203], v198 offset:34816
	ds_read_b128 v[204:207], v198 offset:35840
	ds_read_b128 v[208:211], v198 offset:36864
	ds_read_b128 v[212:215], v198 offset:37888
	ds_read_b128 v[216:219], v198 offset:38912
	ds_read_b128 v[220:223], v198 offset:39936
	global_load_lds_dwordx4 v[232:233], off
	v_lshl_add_u64 v[232:233], s[60:61], 0, v[178:179]
	s_mov_b32 m0, s70
	s_nop 0
	global_load_lds_dwordx4 v[232:233], off
	s_waitcnt vmcnt(8)
	s_waitcnt lgkmcnt(0)
	s_barrier
	s_setprio 1
	v_mfma_scale_f32_16x16x128_f8f6f4 v[154:157], v[26:33], v[170:177], v[154:157], v194, v169 op_sel_hi:[0,0,0]
	v_mfma_scale_f32_16x16x128_f8f6f4 v[158:161], v[18:25], v[170:177], v[158:161], v194, v169 op_sel_hi:[0,0,0]
	v_mfma_scale_f32_16x16x128_f8f6f4 v[138:141], v[26:33], v[200:207], v[138:141], v194, v169 op_sel_hi:[0,0,0]
	v_mfma_scale_f32_16x16x128_f8f6f4 v[142:145], v[18:25], v[200:207], v[142:145], v194, v169 op_sel_hi:[0,0,0]
	v_mfma_scale_f32_16x16x128_f8f6f4 v[122:125], v[26:33], v[208:215], v[122:125], v194, v169 op_sel_hi:[0,0,0]
	v_mfma_scale_f32_16x16x128_f8f6f4 v[126:129], v[18:25], v[208:215], v[126:129], v194, v169 op_sel_hi:[0,0,0]
	v_mfma_scale_f32_16x16x128_f8f6f4 v[106:109], v[26:33], v[216:223], v[106:109], v194, v169 op_sel_hi:[0,0,0]
	v_mfma_scale_f32_16x16x128_f8f6f4 v[110:113], v[18:25], v[216:223], v[110:113], v194, v169 op_sel_hi:[0,0,0]
	s_setprio 0
	s_setprio 1
	v_mfma_scale_f32_16x16x128_f8f6f4 v[146:149], v[10:17], v[170:177], v[146:149], v194, v169 op_sel_hi:[0,0,0]
	v_mfma_scale_f32_16x16x128_f8f6f4 v[150:153], v[2:9], v[170:177], v[150:153], v194, v169 op_sel_hi:[0,0,0]
	v_mfma_scale_f32_16x16x128_f8f6f4 v[130:133], v[10:17], v[200:207], v[130:133], v194, v169 op_sel_hi:[0,0,0]
	v_mfma_scale_f32_16x16x128_f8f6f4 v[134:137], v[2:9], v[200:207], v[134:137], v194, v169 op_sel_hi:[0,0,0]
	v_mfma_scale_f32_16x16x128_f8f6f4 v[114:117], v[10:17], v[208:215], v[114:117], v194, v169 op_sel_hi:[0,0,0]
	v_mfma_scale_f32_16x16x128_f8f6f4 v[118:121], v[2:9], v[208:215], v[118:121], v194, v169 op_sel_hi:[0,0,0]
	v_mfma_scale_f32_16x16x128_f8f6f4 v[98:101], v[10:17], v[216:223], v[98:101], v194, v169 op_sel_hi:[0,0,0]
	v_mfma_scale_f32_16x16x128_f8f6f4 v[102:105], v[2:9], v[216:223], v[102:105], v194, v169 op_sel_hi:[0,0,0]
	s_setprio 0
	s_barrier
	s_add_i32 s60, s92, s20
	v_lshl_add_u64 v[186:187], v[186:187], 0, s[56:57]
	s_mov_b32 m0, s60
	ds_read_b128 v[170:173], v198 offset:49152
	ds_read_b128 v[174:177], v198 offset:50176
	ds_read_b128 v[200:203], v198 offset:51200
	ds_read_b128 v[204:207], v198 offset:52224
	ds_read_b128 v[208:211], v198 offset:53248
	ds_read_b128 v[212:215], v198 offset:54272
	ds_read_b128 v[216:219], v198 offset:55296
	ds_read_b128 v[220:223], v198 offset:56320
	global_load_lds_dwordx4 v[186:187], off
	s_add_i32 m0, s60, 0x2000
	s_add_u32 s60, s64, 0x70080
	v_lshl_add_u64 v[186:187], v[188:189], 0, s[56:57]
	s_addc_u32 s61, s65, 0
	s_add_i32 s64, s93, s20
	global_load_lds_dwordx4 v[186:187], off
	v_lshl_add_u64 v[186:187], s[60:61], 0, v[164:165]
	s_mov_b32 m0, s64
	s_nop 0
	global_load_lds_dwordx4 v[186:187], off
	v_lshl_add_u64 v[186:187], s[60:61], 0, v[180:181]
	s_add_i32 m0, s64, 0x2000
	s_nop 0
	global_load_lds_dwordx4 v[186:187], off
	v_lshl_add_u64 v[186:187], v[190:191], 0, s[56:57]
	s_mov_b32 m0, s71
	s_nop 0
	global_load_lds_dwordx4 v[186:187], off
	v_lshl_add_u64 v[186:187], v[192:193], 0, s[56:57]
	s_mov_b32 m0, s72
	s_nop 0
	global_load_lds_dwordx4 v[186:187], off
	s_waitcnt vmcnt(8)
	s_waitcnt lgkmcnt(0)
	s_barrier
	s_setprio 1
	v_mfma_scale_f32_16x16x128_f8f6f4 v[90:93], v[26:33], v[170:177], v[90:93], v194, v169 op_sel_hi:[0,0,0]
	v_mfma_scale_f32_16x16x128_f8f6f4 v[94:97], v[18:25], v[170:177], v[94:97], v194, v169 op_sel_hi:[0,0,0]
	v_mfma_scale_f32_16x16x128_f8f6f4 v[74:77], v[26:33], v[200:207], v[74:77], v194, v169 op_sel_hi:[0,0,0]
	v_mfma_scale_f32_16x16x128_f8f6f4 v[78:81], v[18:25], v[200:207], v[78:81], v194, v169 op_sel_hi:[0,0,0]
	v_mfma_scale_f32_16x16x128_f8f6f4 v[58:61], v[26:33], v[208:215], v[58:61], v194, v169 op_sel_hi:[0,0,0]
	v_mfma_scale_f32_16x16x128_f8f6f4 v[62:65], v[18:25], v[208:215], v[62:65], v194, v169 op_sel_hi:[0,0,0]
	v_mfma_scale_f32_16x16x128_f8f6f4 v[42:45], v[26:33], v[216:223], v[42:45], v194, v169 op_sel_hi:[0,0,0]
	v_mfma_scale_f32_16x16x128_f8f6f4 v[46:49], v[18:25], v[216:223], v[46:49], v194, v169 op_sel_hi:[0,0,0]
	s_setprio 0
	s_setprio 1
	v_mfma_scale_f32_16x16x128_f8f6f4 v[82:85], v[10:17], v[170:177], v[82:85], v194, v169 op_sel_hi:[0,0,0]
	v_mfma_scale_f32_16x16x128_f8f6f4 v[86:89], v[2:9], v[170:177], v[86:89], v194, v169 op_sel_hi:[0,0,0]
	v_mfma_scale_f32_16x16x128_f8f6f4 v[66:69], v[10:17], v[200:207], v[66:69], v194, v169 op_sel_hi:[0,0,0]
	v_mfma_scale_f32_16x16x128_f8f6f4 v[70:73], v[2:9], v[200:207], v[70:73], v194, v169 op_sel_hi:[0,0,0]
	v_mfma_scale_f32_16x16x128_f8f6f4 v[50:53], v[10:17], v[208:215], v[50:53], v194, v169 op_sel_hi:[0,0,0]
	v_mfma_scale_f32_16x16x128_f8f6f4 v[54:57], v[2:9], v[208:215], v[54:57], v194, v169 op_sel_hi:[0,0,0]
	v_mfma_scale_f32_16x16x128_f8f6f4 v[34:37], v[10:17], v[216:223], v[34:37], v194, v169 op_sel_hi:[0,0,0]
	v_mfma_scale_f32_16x16x128_f8f6f4 v[38:41], v[2:9], v[216:223], v[38:41], v194, v169 op_sel_hi:[0,0,0]
	s_setprio 0
	s_barrier
	s_add_u32 s51, s51, 0x100
	s_addc_u32 s59, s59, 0
	s_cmp_ge_i32 s91, s8
	s_mov_b64 s[60:61], s[62:63]
	s_mov_b32 s64, s91
	s_cbranch_scc0 .LBB0_1777
	s_branch .Lpeelexitph16
	.p2align	6

.Lpeelph17_1:
	s_add_i32 s55, s55, 2
	s_add_u32 s60, s64, 0x100
	s_addc_u32 s61, s65, 0
	s_and_b64 s[68:69], s[62:63], exec
	s_cselect_b32 s68, 0, s60
	s_cselect_b32 s69, 0, s61
	s_add_u32 s68, s30, s68
	s_addc_u32 s69, s31, s69
	s_add_u32 s91, s47, s64
	s_addc_u32 s92, s49, s65
	s_and_b64 s[62:63], s[62:63], exec
	s_cselect_b32 s63, s53, s92
	s_cselect_b32 s62, s52, s91
	s_add_i32 s92, 0, 0x10000
	s_add_i32 s91, 0, 0x14000
	v_add_u32_e32 v2, s92, v210
	v_add_u32_e32 v6, s91, v210
	ds_read_b128 v[26:29], v2
	ds_read_b128 v[30:33], v2 offset:1024
	ds_read_b128 v[18:21], v2 offset:2048
	ds_read_b128 v[22:25], v2 offset:3072
	ds_read_b128 v[10:13], v6
	ds_read_b128 v[14:17], v6 offset:1024
	ds_read_b128 v[2:5], v6 offset:2048
	ds_read_b128 v[6:9], v6 offset:3072
	v_lshl_add_u64 v[222:223], v[194:195], 0, s[64:65]
	s_add_i32 m0, s59, 0xc000
	ds_read_b128 v[170:173], v212
	ds_read_b128 v[174:177], v212 offset:1024
	ds_read_b128 v[196:199], v212 offset:2048
	ds_read_b128 v[200:203], v212 offset:3072
	ds_read_b128 v[214:217], v212 offset:4096
	ds_read_b128 v[218:221], v212 offset:5120
	ds_read_b128 v[236:239], v212 offset:6144
	ds_read_b128 v[240:243], v212 offset:7168
	global_load_lds_dwordx4 v[222:223], off
	v_lshl_add_u64 v[222:223], v[192:193], 0, s[64:65]
	s_add_i32 m0, s59, 0xe000
	s_nop 0
	global_load_lds_dwordx4 v[222:223], off
	s_waitcnt vmcnt(8)
	s_waitcnt lgkmcnt(0)
	s_barrier
	s_setprio 1
	v_mfma_scale_f32_16x16x128_f8f6f4 v[154:157], v[26:33], v[170:177], 0, v208, v207 op_sel_hi:[0,0,0]
	v_mfma_scale_f32_16x16x128_f8f6f4 v[150:153], v[18:25], v[170:177], 0, v208, v207 op_sel_hi:[0,0,0]
	v_mfma_scale_f32_16x16x128_f8f6f4 v[142:145], v[26:33], v[196:203], 0, v208, v207 op_sel_hi:[0,0,0]
	v_mfma_scale_f32_16x16x128_f8f6f4 v[134:137], v[18:25], v[196:203], 0, v208, v207 op_sel_hi:[0,0,0]
	v_mfma_scale_f32_16x16x128_f8f6f4 v[126:129], v[26:33], v[214:221], 0, v208, v207 op_sel_hi:[0,0,0]
	v_mfma_scale_f32_16x16x128_f8f6f4 v[118:121], v[18:25], v[214:221], 0, v208, v207 op_sel_hi:[0,0,0]
	v_mfma_scale_f32_16x16x128_f8f6f4 v[110:113], v[26:33], v[236:243], 0, v208, v207 op_sel_hi:[0,0,0]
	v_mfma_scale_f32_16x16x128_f8f6f4 v[102:105], v[18:25], v[236:243], 0, v208, v207 op_sel_hi:[0,0,0]
	s_setprio 0
	s_setprio 1
	v_mfma_scale_f32_16x16x128_f8f6f4 v[158:161], v[10:17], v[170:177], 0, v208, v207 op_sel_hi:[0,0,0]
	v_mfma_scale_f32_16x16x128_f8f6f4 v[146:149], v[2:9], v[170:177], 0, v208, v207 op_sel_hi:[0,0,0]
	v_mfma_scale_f32_16x16x128_f8f6f4 v[138:141], v[10:17], v[196:203], 0, v208, v207 op_sel_hi:[0,0,0]
	v_mfma_scale_f32_16x16x128_f8f6f4 v[130:133], v[2:9], v[196:203], 0, v208, v207 op_sel_hi:[0,0,0]
	v_mfma_scale_f32_16x16x128_f8f6f4 v[122:125], v[10:17], v[214:221], 0, v208, v207 op_sel_hi:[0,0,0]
	v_mfma_scale_f32_16x16x128_f8f6f4 v[114:117], v[2:9], v[214:221], 0, v208, v207 op_sel_hi:[0,0,0]
	v_mfma_scale_f32_16x16x128_f8f6f4 v[106:109], v[10:17], v[236:243], 0, v208, v207 op_sel_hi:[0,0,0]
	v_mfma_scale_f32_16x16x128_f8f6f4 v[98:101], v[2:9], v[236:243], 0, v208, v207 op_sel_hi:[0,0,0]
	s_setprio 0
	s_barrier
	s_add_i32 s64, s92, s22
	v_lshl_add_u64 v[196:197], s[62:63], 0, v[162:163]
	s_mov_b32 m0, s64
	ds_read_b128 v[170:173], v212 offset:16384
	ds_read_b128 v[174:177], v212 offset:17408
	ds_read_b128 v[214:217], v212 offset:18432
	ds_read_b128 v[218:221], v212 offset:19456
	ds_read_b128 v[236:239], v212 offset:20480
	ds_read_b128 v[240:243], v212 offset:21504
	ds_read_b128 v[244:247], v212 offset:22528
	ds_read_b128 v[248:251], v212 offset:23552
	global_load_lds_dwordx4 v[196:197], off
	s_add_i32 m0, s64, 0x2000
	s_add_u32 s64, s62, 0x20000
	v_lshl_add_u64 v[198:199], s[62:63], 0, v[164:165]
	s_addc_u32 s65, s63, 0
	s_add_i32 s91, s91, s22
	global_load_lds_dwordx4 v[198:199], off
	v_lshl_add_u64 v[200:201], s[64:65], 0, v[162:163]
	s_mov_b32 m0, s91
	v_mov_b32_e32 v179, v167
	global_load_lds_dwordx4 v[200:201], off
	v_lshl_add_u64 v[200:201], s[64:65], 0, v[164:165]
	s_add_i32 m0, s91, 0x2000
	v_lshl_add_u64 v[202:203], s[68:69], 0, v[166:167]
	global_load_lds_dwordx4 v[200:201], off
	s_mov_b32 m0, s59
	v_lshl_add_u64 v[200:201], s[68:69], 0, v[178:179]
	global_load_lds_dwordx4 v166, s[68:69]
	s_mov_b32 m0, s71
	s_nop 0
	global_load_lds_dwordx4 v178, s[68:69]
	s_waitcnt vmcnt(8)
	s_waitcnt lgkmcnt(0)
	s_barrier
	s_setprio 1
	v_mfma_scale_f32_16x16x128_f8f6f4 v[94:97], v[26:33], v[170:177], 0, v208, v207 op_sel_hi:[0,0,0]
	v_mfma_scale_f32_16x16x128_f8f6f4 v[86:89], v[18:25], v[170:177], 0, v208, v207 op_sel_hi:[0,0,0]
	v_mfma_scale_f32_16x16x128_f8f6f4 v[78:81], v[26:33], v[214:221], 0, v208, v207 op_sel_hi:[0,0,0]
	v_mfma_scale_f32_16x16x128_f8f6f4 v[70:73], v[18:25], v[214:221], 0, v208, v207 op_sel_hi:[0,0,0]
	v_mfma_scale_f32_16x16x128_f8f6f4 v[62:65], v[26:33], v[236:243], 0, v208, v207 op_sel_hi:[0,0,0]
	v_mfma_scale_f32_16x16x128_f8f6f4 v[54:57], v[18:25], v[236:243], 0, v208, v207 op_sel_hi:[0,0,0]
	v_mfma_scale_f32_16x16x128_f8f6f4 v[46:49], v[26:33], v[244:251], 0, v208, v207 op_sel_hi:[0,0,0]
	v_mfma_scale_f32_16x16x128_f8f6f4 v[38:41], v[18:25], v[244:251], 0, v208, v207 op_sel_hi:[0,0,0]
	s_setprio 0
	s_setprio 1
	v_mfma_scale_f32_16x16x128_f8f6f4 v[90:93], v[10:17], v[170:177], 0, v208, v207 op_sel_hi:[0,0,0]
	v_mfma_scale_f32_16x16x128_f8f6f4 v[82:85], v[2:9], v[170:177], 0, v208, v207 op_sel_hi:[0,0,0]
	v_mfma_scale_f32_16x16x128_f8f6f4 v[74:77], v[10:17], v[214:221], 0, v208, v207 op_sel_hi:[0,0,0]
	v_mfma_scale_f32_16x16x128_f8f6f4 v[66:69], v[2:9], v[214:221], 0, v208, v207 op_sel_hi:[0,0,0]
	v_mfma_scale_f32_16x16x128_f8f6f4 v[58:61], v[10:17], v[236:243], 0, v208, v207 op_sel_hi:[0,0,0]
	v_mfma_scale_f32_16x16x128_f8f6f4 v[50:53], v[2:9], v[236:243], 0, v208, v207 op_sel_hi:[0,0,0]
	v_mfma_scale_f32_16x16x128_f8f6f4 v[42:45], v[10:17], v[244:251], 0, v208, v207 op_sel_hi:[0,0,0]
	v_mfma_scale_f32_16x16x128_f8f6f4 v[34:37], v[2:9], v[244:251], 0, v208, v207 op_sel_hi:[0,0,0]
	s_setprio 0
	s_barrier
	s_add_i32 s64, 0, 0x18000
	s_add_i32 s65, 0, 0x1c000
	v_add_u32_e32 v2, s64, v210
	v_add_u32_e32 v6, s65, v210
	ds_read_b128 v[26:29], v2
	ds_read_b128 v[30:33], v2 offset:1024
	ds_read_b128 v[18:21], v2 offset:2048
	ds_read_b128 v[22:25], v2 offset:3072
	ds_read_b128 v[10:13], v6
	ds_read_b128 v[14:17], v6 offset:1024
	ds_read_b128 v[2:5], v6 offset:2048
	ds_read_b128 v[6:9], v6 offset:3072
	s_mov_b32 m0, s72
	ds_read_b128 v[170:173], v212 offset:32768
	ds_read_b128 v[174:177], v212 offset:33792
	ds_read_b128 v[214:217], v212 offset:34816
	ds_read_b128 v[218:221], v212 offset:35840
	ds_read_b128 v[236:239], v212 offset:36864
	ds_read_b128 v[240:243], v212 offset:37888
	ds_read_b128 v[244:247], v212 offset:38912
	ds_read_b128 v[248:251], v212 offset:39936
	global_load_lds_dwordx4 v180, s[68:69]
	s_mov_b32 m0, s73
	s_nop 0
	global_load_lds_dwordx4 v182, s[68:69]
	s_waitcnt vmcnt(8)
	s_waitcnt lgkmcnt(0)
	s_barrier
	s_setprio 1
	v_mfma_scale_f32_16x16x128_f8f6f4 v[154:157], v[26:33], v[170:177], v[154:157], v208, v207 op_sel_hi:[0,0,0]
	v_mfma_scale_f32_16x16x128_f8f6f4 v[150:153], v[18:25], v[170:177], v[150:153], v208, v207 op_sel_hi:[0,0,0]
	v_mfma_scale_f32_16x16x128_f8f6f4 v[142:145], v[26:33], v[214:221], v[142:145], v208, v207 op_sel_hi:[0,0,0]
	v_mfma_scale_f32_16x16x128_f8f6f4 v[134:137], v[18:25], v[214:221], v[134:137], v208, v207 op_sel_hi:[0,0,0]
	v_mfma_scale_f32_16x16x128_f8f6f4 v[126:129], v[26:33], v[236:243], v[126:129], v208, v207 op_sel_hi:[0,0,0]
	v_mfma_scale_f32_16x16x128_f8f6f4 v[118:121], v[18:25], v[236:243], v[118:121], v208, v207 op_sel_hi:[0,0,0]
	v_mfma_scale_f32_16x16x128_f8f6f4 v[110:113], v[26:33], v[244:251], v[110:113], v208, v207 op_sel_hi:[0,0,0]
	v_mfma_scale_f32_16x16x128_f8f6f4 v[102:105], v[18:25], v[244:251], v[102:105], v208, v207 op_sel_hi:[0,0,0]
	s_setprio 0
	s_setprio 1
	v_mfma_scale_f32_16x16x128_f8f6f4 v[158:161], v[10:17], v[170:177], v[158:161], v208, v207 op_sel_hi:[0,0,0]
	v_mfma_scale_f32_16x16x128_f8f6f4 v[146:149], v[2:9], v[170:177], v[146:149], v208, v207 op_sel_hi:[0,0,0]
	v_mfma_scale_f32_16x16x128_f8f6f4 v[138:141], v[10:17], v[214:221], v[138:141], v208, v207 op_sel_hi:[0,0,0]
	v_mfma_scale_f32_16x16x128_f8f6f4 v[130:133], v[2:9], v[214:221], v[130:133], v208, v207 op_sel_hi:[0,0,0]
	v_mfma_scale_f32_16x16x128_f8f6f4 v[122:125], v[10:17], v[236:243], v[122:125], v208, v207 op_sel_hi:[0,0,0]
	v_mfma_scale_f32_16x16x128_f8f6f4 v[114:117], v[2:9], v[236:243], v[114:117], v208, v207 op_sel_hi:[0,0,0]
	v_mfma_scale_f32_16x16x128_f8f6f4 v[106:109], v[10:17], v[244:251], v[106:109], v208, v207 op_sel_hi:[0,0,0]
	v_mfma_scale_f32_16x16x128_f8f6f4 v[98:101], v[2:9], v[244:251], v[98:101], v208, v207 op_sel_hi:[0,0,0]
	s_setprio 0
	s_barrier
	s_add_i32 s64, s64, s22
	v_lshl_add_u64 v[196:197], v[196:197], 0, s[56:57]
	s_mov_b32 m0, s64
	ds_read_b128 v[170:173], v212 offset:49152
	ds_read_b128 v[174:177], v212 offset:50176
	ds_read_b128 v[214:217], v212 offset:51200
	ds_read_b128 v[218:221], v212 offset:52224
	ds_read_b128 v[236:239], v212 offset:53248
	ds_read_b128 v[240:243], v212 offset:54272
	ds_read_b128 v[244:247], v212 offset:55296
	ds_read_b128 v[248:251], v212 offset:56320
	global_load_lds_dwordx4 v[196:197], off
	s_add_i32 m0, s64, 0x2000
	s_add_u32 s62, s62, 0x20080
	v_lshl_add_u64 v[196:197], v[198:199], 0, s[56:57]
	s_addc_u32 s63, s63, 0
	s_add_i32 s64, s65, s22
	global_load_lds_dwordx4 v[196:197], off
	v_lshl_add_u64 v[196:197], s[62:63], 0, v[162:163]
	s_mov_b32 m0, s64
	s_nop 0
	global_load_lds_dwordx4 v[196:197], off
	v_lshl_add_u64 v[196:197], s[62:63], 0, v[164:165]
	s_add_i32 m0, s64, 0x2000
	s_nop 0
	global_load_lds_dwordx4 v[196:197], off
	v_lshl_add_u64 v[196:197], v[202:203], 0, s[56:57]
	s_mov_b32 m0, s74
	s_nop 0
	global_load_lds_dwordx4 v[196:197], off
	v_lshl_add_u64 v[196:197], v[200:201], 0, s[56:57]
	s_mov_b32 m0, s75
	s_nop 0
	global_load_lds_dwordx4 v[196:197], off
	s_waitcnt vmcnt(8)
	s_waitcnt lgkmcnt(0)
	s_barrier
	s_setprio 1
	v_mfma_scale_f32_16x16x128_f8f6f4 v[94:97], v[26:33], v[170:177], v[94:97], v208, v207 op_sel_hi:[0,0,0]
	v_mfma_scale_f32_16x16x128_f8f6f4 v[86:89], v[18:25], v[170:177], v[86:89], v208, v207 op_sel_hi:[0,0,0]
	v_mfma_scale_f32_16x16x128_f8f6f4 v[78:81], v[26:33], v[214:221], v[78:81], v208, v207 op_sel_hi:[0,0,0]
	v_mfma_scale_f32_16x16x128_f8f6f4 v[70:73], v[18:25], v[214:221], v[70:73], v208, v207 op_sel_hi:[0,0,0]
	v_mfma_scale_f32_16x16x128_f8f6f4 v[62:65], v[26:33], v[236:243], v[62:65], v208, v207 op_sel_hi:[0,0,0]
	v_mfma_scale_f32_16x16x128_f8f6f4 v[54:57], v[18:25], v[236:243], v[54:57], v208, v207 op_sel_hi:[0,0,0]
	v_mfma_scale_f32_16x16x128_f8f6f4 v[46:49], v[26:33], v[244:251], v[46:49], v208, v207 op_sel_hi:[0,0,0]
	v_mfma_scale_f32_16x16x128_f8f6f4 v[38:41], v[18:25], v[244:251], v[38:41], v208, v207 op_sel_hi:[0,0,0]
	s_setprio 0
	s_setprio 1
	v_mfma_scale_f32_16x16x128_f8f6f4 v[90:93], v[10:17], v[170:177], v[90:93], v208, v207 op_sel_hi:[0,0,0]
	v_mfma_scale_f32_16x16x128_f8f6f4 v[82:85], v[2:9], v[170:177], v[82:85], v208, v207 op_sel_hi:[0,0,0]
	v_mfma_scale_f32_16x16x128_f8f6f4 v[74:77], v[10:17], v[214:221], v[74:77], v208, v207 op_sel_hi:[0,0,0]
	v_mfma_scale_f32_16x16x128_f8f6f4 v[66:69], v[2:9], v[214:221], v[66:69], v208, v207 op_sel_hi:[0,0,0]
	v_mfma_scale_f32_16x16x128_f8f6f4 v[58:61], v[10:17], v[236:243], v[58:61], v208, v207 op_sel_hi:[0,0,0]
	v_mfma_scale_f32_16x16x128_f8f6f4 v[50:53], v[2:9], v[236:243], v[50:53], v208, v207 op_sel_hi:[0,0,0]
	v_mfma_scale_f32_16x16x128_f8f6f4 v[42:45], v[10:17], v[244:251], v[42:45], v208, v207 op_sel_hi:[0,0,0]
	v_mfma_scale_f32_16x16x128_f8f6f4 v[34:37], v[2:9], v[244:251], v[34:37], v208, v207 op_sel_hi:[0,0,0]
	s_setprio 0
	s_barrier
	s_cmp_lt_i32 s55, s11
	s_cbranch_scc0 .LBB0_1841
	s_mov_b64 s[64:65], s[60:61]
	s_branch .LBB0_1836
	.p2align	6

.Lpeelph18_0:
	s_add_i32 s75, s70, 2
	s_add_u32 s42, s18, 0x100
	s_addc_u32 s43, s19, 0
	s_add_i32 s46, 0, 0x10000
	s_cmp_eq_u32 s14, s70
	s_cselect_b32 vcc_hi, s69, s43
	s_cselect_b32 vcc_lo, s68, s42
	s_cselect_b32 s71, s37, s45
	s_cselect_b32 s70, s36, s35
	s_add_i32 s47, 0, 0x14000
	v_add_u32_e32 v2, s46, v196
	v_add_u32_e32 v6, s47, v196
	ds_read_b128 v[26:29], v2
	ds_read_b128 v[30:33], v2 offset:1024
	ds_read_b128 v[18:21], v2 offset:2048
	ds_read_b128 v[22:25], v2 offset:3072
	ds_read_b128 v[10:13], v6
	ds_read_b128 v[14:17], v6 offset:1024
	ds_read_b128 v[2:5], v6 offset:2048
	ds_read_b128 v[6:9], v6 offset:3072
	v_lshl_add_u64 v[218:219], s[18:19], 0, v[184:185]
	s_add_i32 m0, s73, 0xc000
	ds_read_b128 v[170:173], v201
	ds_read_b128 v[174:177], v201 offset:1024
	ds_read_b128 v[186:189], v201 offset:2048
	ds_read_b128 v[190:193], v201 offset:3072
	ds_read_b128 v[202:205], v201 offset:4096
	ds_read_b128 v[206:209], v201 offset:5120
	ds_read_b128 v[210:213], v201 offset:6144
	ds_read_b128 v[214:217], v201 offset:7168
	global_load_lds_dwordx4 v[218:219], off
	v_lshl_add_u64 v[218:219], s[18:19], 0, v[182:183]
	s_add_i32 m0, s73, 0xe000
	s_nop 0
	global_load_lds_dwordx4 v[218:219], off
	s_waitcnt vmcnt(8)
	s_waitcnt lgkmcnt(0)
	s_barrier
	s_setprio 1
	v_mfma_scale_f32_16x16x128_f8f6f4 v[158:161], v[26:33], v[170:177], 0, v194, v169 op_sel_hi:[0,0,0]
	v_mfma_scale_f32_16x16x128_f8f6f4 v[154:157], v[18:25], v[170:177], 0, v194, v169 op_sel_hi:[0,0,0]
	v_mfma_scale_f32_16x16x128_f8f6f4 v[142:145], v[26:33], v[186:193], 0, v194, v169 op_sel_hi:[0,0,0]
	v_mfma_scale_f32_16x16x128_f8f6f4 v[138:141], v[18:25], v[186:193], 0, v194, v169 op_sel_hi:[0,0,0]
	v_mfma_scale_f32_16x16x128_f8f6f4 v[126:129], v[26:33], v[202:209], 0, v194, v169 op_sel_hi:[0,0,0]
	v_mfma_scale_f32_16x16x128_f8f6f4 v[122:125], v[18:25], v[202:209], 0, v194, v169 op_sel_hi:[0,0,0]
	v_mfma_scale_f32_16x16x128_f8f6f4 v[110:113], v[26:33], v[210:217], 0, v194, v169 op_sel_hi:[0,0,0]
	v_mfma_scale_f32_16x16x128_f8f6f4 v[106:109], v[18:25], v[210:217], 0, v194, v169 op_sel_hi:[0,0,0]
	s_setprio 0
	s_setprio 1
	v_mfma_scale_f32_16x16x128_f8f6f4 v[150:153], v[10:17], v[170:177], 0, v194, v169 op_sel_hi:[0,0,0]
	v_mfma_scale_f32_16x16x128_f8f6f4 v[146:149], v[2:9], v[170:177], 0, v194, v169 op_sel_hi:[0,0,0]
	v_mfma_scale_f32_16x16x128_f8f6f4 v[134:137], v[10:17], v[186:193], 0, v194, v169 op_sel_hi:[0,0,0]
	v_mfma_scale_f32_16x16x128_f8f6f4 v[130:133], v[2:9], v[186:193], 0, v194, v169 op_sel_hi:[0,0,0]
	v_mfma_scale_f32_16x16x128_f8f6f4 v[118:121], v[10:17], v[202:209], 0, v194, v169 op_sel_hi:[0,0,0]
	v_mfma_scale_f32_16x16x128_f8f6f4 v[114:117], v[2:9], v[202:209], 0, v194, v169 op_sel_hi:[0,0,0]
	v_mfma_scale_f32_16x16x128_f8f6f4 v[102:105], v[10:17], v[210:217], 0, v194, v169 op_sel_hi:[0,0,0]
	v_mfma_scale_f32_16x16x128_f8f6f4 v[98:101], v[2:9], v[210:217], 0, v194, v169 op_sel_hi:[0,0,0]
	s_setprio 0
	s_barrier
	s_add_i32 s18, s46, s95
	v_lshl_add_u64 v[186:187], s[70:71], 0, v[164:165]
	s_mov_b32 m0, s18
	ds_read_b128 v[170:173], v201 offset:16384
	ds_read_b128 v[174:177], v201 offset:17408
	ds_read_b128 v[202:205], v201 offset:18432
	ds_read_b128 v[206:209], v201 offset:19456
	ds_read_b128 v[210:213], v201 offset:20480
	ds_read_b128 v[214:217], v201 offset:21504
	ds_read_b128 v[236:239], v201 offset:22528
	ds_read_b128 v[240:243], v201 offset:23552
	global_load_lds_dwordx4 v[186:187], off
	s_add_i32 m0, s18, 0x2000
	s_add_u32 s18, s70, 0x70000
	v_lshl_add_u64 v[188:189], s[70:71], 0, v[180:181]
	s_addc_u32 s19, s71, 0
	s_add_i32 s46, s47, s95
	global_load_lds_dwordx4 v[188:189], off
	v_lshl_add_u64 v[190:191], s[18:19], 0, v[164:165]
	s_mov_b32 m0, s46
	v_lshl_add_u64 v[192:193], vcc, 0, v[178:179]
	global_load_lds_dwordx4 v[190:191], off
	v_lshl_add_u64 v[190:191], s[18:19], 0, v[180:181]
	s_add_i32 m0, s46, 0x2000
	s_nop 0
	global_load_lds_dwordx4 v[190:191], off
	v_lshl_add_u64 v[190:191], vcc, 0, v[162:163]
	s_mov_b32 m0, s73
	s_nop 0
	global_load_lds_dwordx4 v[190:191], off
	s_mov_b32 m0, s8
	s_nop 0
	global_load_lds_dwordx4 v[192:193], off
	s_waitcnt vmcnt(8)
	s_waitcnt lgkmcnt(0)
	s_barrier
	s_setprio 1
	v_mfma_scale_f32_16x16x128_f8f6f4 v[94:97], v[26:33], v[170:177], 0, v194, v169 op_sel_hi:[0,0,0]
	v_mfma_scale_f32_16x16x128_f8f6f4 v[90:93], v[18:25], v[170:177], 0, v194, v169 op_sel_hi:[0,0,0]
	v_mfma_scale_f32_16x16x128_f8f6f4 v[78:81], v[26:33], v[202:209], 0, v194, v169 op_sel_hi:[0,0,0]
	v_mfma_scale_f32_16x16x128_f8f6f4 v[74:77], v[18:25], v[202:209], 0, v194, v169 op_sel_hi:[0,0,0]
	v_mfma_scale_f32_16x16x128_f8f6f4 v[62:65], v[26:33], v[210:217], 0, v194, v169 op_sel_hi:[0,0,0]
	v_mfma_scale_f32_16x16x128_f8f6f4 v[58:61], v[18:25], v[210:217], 0, v194, v169 op_sel_hi:[0,0,0]
	v_mfma_scale_f32_16x16x128_f8f6f4 v[46:49], v[26:33], v[236:243], 0, v194, v169 op_sel_hi:[0,0,0]
	v_mfma_scale_f32_16x16x128_f8f6f4 v[42:45], v[18:25], v[236:243], 0, v194, v169 op_sel_hi:[0,0,0]
	s_setprio 0
	s_setprio 1
	v_mfma_scale_f32_16x16x128_f8f6f4 v[86:89], v[10:17], v[170:177], 0, v194, v169 op_sel_hi:[0,0,0]
	v_mfma_scale_f32_16x16x128_f8f6f4 v[82:85], v[2:9], v[170:177], 0, v194, v169 op_sel_hi:[0,0,0]
	v_mfma_scale_f32_16x16x128_f8f6f4 v[70:73], v[10:17], v[202:209], 0, v194, v169 op_sel_hi:[0,0,0]
	v_mfma_scale_f32_16x16x128_f8f6f4 v[66:69], v[2:9], v[202:209], 0, v194, v169 op_sel_hi:[0,0,0]
	v_mfma_scale_f32_16x16x128_f8f6f4 v[54:57], v[10:17], v[210:217], 0, v194, v169 op_sel_hi:[0,0,0]
	v_mfma_scale_f32_16x16x128_f8f6f4 v[50:53], v[2:9], v[210:217], 0, v194, v169 op_sel_hi:[0,0,0]
	v_mfma_scale_f32_16x16x128_f8f6f4 v[38:41], v[10:17], v[236:243], 0, v194, v169 op_sel_hi:[0,0,0]
	v_mfma_scale_f32_16x16x128_f8f6f4 v[34:37], v[2:9], v[236:243], 0, v194, v169 op_sel_hi:[0,0,0]
	s_setprio 0
	s_barrier
	s_add_i32 s46, 0, 0x18000
	s_add_i32 s47, 0, 0x1c000
	v_add_u32_e32 v2, s46, v196
	v_add_u32_e32 v6, s47, v196
	ds_read_b128 v[26:29], v2
	ds_read_b128 v[30:33], v2 offset:1024
	ds_read_b128 v[18:21], v2 offset:2048
	ds_read_b128 v[22:25], v2 offset:3072
	ds_read_b128 v[10:13], v6
	ds_read_b128 v[14:17], v6 offset:1024
	ds_read_b128 v[2:5], v6 offset:2048
	ds_read_b128 v[6:9], v6 offset:3072
	s_add_u32 s18, vcc_lo, 0x70000
	s_addc_u32 s19, vcc_hi, 0
	s_mov_b32 m0, s11
	v_lshl_add_u64 v[218:219], s[18:19], 0, v[162:163]
	ds_read_b128 v[170:173], v201 offset:32768
	ds_read_b128 v[174:177], v201 offset:33792
	ds_read_b128 v[202:205], v201 offset:34816
	ds_read_b128 v[206:209], v201 offset:35840
	ds_read_b128 v[210:213], v201 offset:36864
	ds_read_b128 v[214:217], v201 offset:37888
	ds_read_b128 v[236:239], v201 offset:38912
	ds_read_b128 v[240:243], v201 offset:39936
	global_load_lds_dwordx4 v[218:219], off
	v_lshl_add_u64 v[218:219], s[18:19], 0, v[178:179]
	s_mov_b32 m0, s84
	s_nop 0
	global_load_lds_dwordx4 v[218:219], off
	s_waitcnt vmcnt(8)
	s_waitcnt lgkmcnt(0)
	s_barrier
	s_setprio 1
	v_mfma_scale_f32_16x16x128_f8f6f4 v[158:161], v[26:33], v[170:177], v[158:161], v194, v169 op_sel_hi:[0,0,0]
	v_mfma_scale_f32_16x16x128_f8f6f4 v[154:157], v[18:25], v[170:177], v[154:157], v194, v169 op_sel_hi:[0,0,0]
	v_mfma_scale_f32_16x16x128_f8f6f4 v[142:145], v[26:33], v[202:209], v[142:145], v194, v169 op_sel_hi:[0,0,0]
	v_mfma_scale_f32_16x16x128_f8f6f4 v[138:141], v[18:25], v[202:209], v[138:141], v194, v169 op_sel_hi:[0,0,0]
	v_mfma_scale_f32_16x16x128_f8f6f4 v[126:129], v[26:33], v[210:217], v[126:129], v194, v169 op_sel_hi:[0,0,0]
	v_mfma_scale_f32_16x16x128_f8f6f4 v[122:125], v[18:25], v[210:217], v[122:125], v194, v169 op_sel_hi:[0,0,0]
	v_mfma_scale_f32_16x16x128_f8f6f4 v[110:113], v[26:33], v[236:243], v[110:113], v194, v169 op_sel_hi:[0,0,0]
	v_mfma_scale_f32_16x16x128_f8f6f4 v[106:109], v[18:25], v[236:243], v[106:109], v194, v169 op_sel_hi:[0,0,0]
	s_setprio 0
	s_setprio 1
	v_mfma_scale_f32_16x16x128_f8f6f4 v[150:153], v[10:17], v[170:177], v[150:153], v194, v169 op_sel_hi:[0,0,0]
	v_mfma_scale_f32_16x16x128_f8f6f4 v[146:149], v[2:9], v[170:177], v[146:149], v194, v169 op_sel_hi:[0,0,0]
	v_mfma_scale_f32_16x16x128_f8f6f4 v[134:137], v[10:17], v[202:209], v[134:137], v194, v169 op_sel_hi:[0,0,0]
	v_mfma_scale_f32_16x16x128_f8f6f4 v[130:133], v[2:9], v[202:209], v[130:133], v194, v169 op_sel_hi:[0,0,0]
	v_mfma_scale_f32_16x16x128_f8f6f4 v[118:121], v[10:17], v[210:217], v[118:121], v194, v169 op_sel_hi:[0,0,0]
	v_mfma_scale_f32_16x16x128_f8f6f4 v[114:117], v[2:9], v[210:217], v[114:117], v194, v169 op_sel_hi:[0,0,0]
	v_mfma_scale_f32_16x16x128_f8f6f4 v[102:105], v[10:17], v[236:243], v[102:105], v194, v169 op_sel_hi:[0,0,0]
	v_mfma_scale_f32_16x16x128_f8f6f4 v[98:101], v[2:9], v[236:243], v[98:101], v194, v169 op_sel_hi:[0,0,0]
	s_setprio 0
	s_barrier
	s_add_i32 s18, s46, s95
	v_lshl_add_u64 v[186:187], v[186:187], 0, s[56:57]
	s_mov_b32 m0, s18
	ds_read_b128 v[170:173], v201 offset:49152
	ds_read_b128 v[174:177], v201 offset:50176
	ds_read_b128 v[202:205], v201 offset:51200
	ds_read_b128 v[206:209], v201 offset:52224
	ds_read_b128 v[210:213], v201 offset:53248
	ds_read_b128 v[214:217], v201 offset:54272
	ds_read_b128 v[236:239], v201 offset:55296
	ds_read_b128 v[240:243], v201 offset:56320
	global_load_lds_dwordx4 v[186:187], off
	s_add_i32 m0, s18, 0x2000
	s_add_u32 s18, s70, 0x70080
	v_lshl_add_u64 v[186:187], v[188:189], 0, s[56:57]
	s_addc_u32 s19, s71, 0
	s_add_i32 s46, s47, s95
	global_load_lds_dwordx4 v[186:187], off
	v_lshl_add_u64 v[186:187], s[18:19], 0, v[164:165]
	s_mov_b32 m0, s46
	s_nop 0
	global_load_lds_dwordx4 v[186:187], off
	v_lshl_add_u64 v[186:187], s[18:19], 0, v[180:181]
	s_add_i32 m0, s46, 0x2000
	s_nop 0
	global_load_lds_dwordx4 v[186:187], off
	v_lshl_add_u64 v[186:187], v[190:191], 0, s[56:57]
	s_mov_b32 m0, s0
	s_nop 0
	global_load_lds_dwordx4 v[186:187], off
	v_lshl_add_u64 v[186:187], v[192:193], 0, s[56:57]
	s_mov_b32 m0, s88
	s_nop 0
	global_load_lds_dwordx4 v[186:187], off
	s_waitcnt vmcnt(8)
	s_waitcnt lgkmcnt(0)
	s_barrier
	s_setprio 1
	v_mfma_scale_f32_16x16x128_f8f6f4 v[94:97], v[26:33], v[170:177], v[94:97], v194, v169 op_sel_hi:[0,0,0]
	v_mfma_scale_f32_16x16x128_f8f6f4 v[90:93], v[18:25], v[170:177], v[90:93], v194, v169 op_sel_hi:[0,0,0]
	v_mfma_scale_f32_16x16x128_f8f6f4 v[78:81], v[26:33], v[202:209], v[78:81], v194, v169 op_sel_hi:[0,0,0]
	v_mfma_scale_f32_16x16x128_f8f6f4 v[74:77], v[18:25], v[202:209], v[74:77], v194, v169 op_sel_hi:[0,0,0]
	v_mfma_scale_f32_16x16x128_f8f6f4 v[62:65], v[26:33], v[210:217], v[62:65], v194, v169 op_sel_hi:[0,0,0]
	v_mfma_scale_f32_16x16x128_f8f6f4 v[58:61], v[18:25], v[210:217], v[58:61], v194, v169 op_sel_hi:[0,0,0]
	v_mfma_scale_f32_16x16x128_f8f6f4 v[46:49], v[26:33], v[236:243], v[46:49], v194, v169 op_sel_hi:[0,0,0]
	v_mfma_scale_f32_16x16x128_f8f6f4 v[42:45], v[18:25], v[236:243], v[42:45], v194, v169 op_sel_hi:[0,0,0]
	s_setprio 0
	s_setprio 1
	v_mfma_scale_f32_16x16x128_f8f6f4 v[86:89], v[10:17], v[170:177], v[86:89], v194, v169 op_sel_hi:[0,0,0]
	v_mfma_scale_f32_16x16x128_f8f6f4 v[82:85], v[2:9], v[170:177], v[82:85], v194, v169 op_sel_hi:[0,0,0]
	v_mfma_scale_f32_16x16x128_f8f6f4 v[70:73], v[10:17], v[202:209], v[70:73], v194, v169 op_sel_hi:[0,0,0]
	v_mfma_scale_f32_16x16x128_f8f6f4 v[66:69], v[2:9], v[202:209], v[66:69], v194, v169 op_sel_hi:[0,0,0]
	v_mfma_scale_f32_16x16x128_f8f6f4 v[54:57], v[10:17], v[210:217], v[54:57], v194, v169 op_sel_hi:[0,0,0]
	v_mfma_scale_f32_16x16x128_f8f6f4 v[50:53], v[2:9], v[210:217], v[50:53], v194, v169 op_sel_hi:[0,0,0]
	v_mfma_scale_f32_16x16x128_f8f6f4 v[38:41], v[10:17], v[236:243], v[38:41], v194, v169 op_sel_hi:[0,0,0]
	v_mfma_scale_f32_16x16x128_f8f6f4 v[34:37], v[2:9], v[236:243], v[34:37], v194, v169 op_sel_hi:[0,0,0]
	s_setprio 0
	s_barrier
	s_add_u32 s35, s35, 0x100
	s_addc_u32 s45, s45, 0
	s_cmp_lt_i32 s75, s16
	s_mov_b64 s[18:19], s[42:43]
	s_mov_b32 s70, s75
	s_cbranch_scc1 .LBB0_1923
	s_branch .Lpeelexitph18
	.p2align	6
